# code prefetch sites also at every loop-nest exit outside the seams (K-loop exits before epilogues)
# baseline (speedup 1.0000x reference)
.LBB0_255:
	s_getpc_b64 s[100:101]
	global_load_dword a0, v250, s[100:101]
	s_mov_b32 s5, 0
	v_mbcnt_lo_u32_b32 v154, -1, 0
	v_mbcnt_hi_u32_b32 v154, -1, v154
	s_cmp_gt_i32 s36, 3
	s_mov_b64 s[30:31], -1
	s_cbranch_scc0 .LBB0_257
	s_lshl_b32 s5, s71, 1
	s_cmp_eq_u32 s36, 4
	s_cselect_b32 s23, s43, s45
	s_movk_i32 s25, 0x400
	s_cselect_b32 s18, s44, s48
	s_cselect_b32 s25, s25, 0x500
	s_add_u32 s38, s23, s5
	s_addc_u32 s39, s18, 0
	s_or_b32 s18, s71, s25
	s_mov_b64 s[30:31], 0
	s_mov_b64 s[40:41], s[18:19]

.LBB0_336:
	s_getpc_b64 s[100:101]
	global_load_dword a0, v250, s[100:101]
	s_lshl_b32 s1, s25, 6
	s_sext_i32_i8 s13, s0
	v_mbcnt_lo_u32_b32 v82, -1, 0
	v_mbcnt_hi_u32_b32 v82, -1, v82
	s_cmp_gt_i32 s13, 3
	s_cbranch_scc0 .LBB0_339
	s_cmp_lg_u32 s13, 4
	s_cbranch_scc0 .LBB0_341
	s_or_b32 s0, s1, 0x500
	s_lshl_b32 s4, s1, 1
	s_add_u32 s14, s45, s4
	s_addc_u32 s15, s48, 0
	s_mov_b64 s[4:5], 0
	s_branch .LBB0_342

.LBB0_560:
	s_getpc_b64 s[100:101]
	global_load_dword a0, v250, s[100:101]
	v_readlane_b32 s72, v249, 55
	v_readlane_b32 s73, v249, 56
	v_readlane_b32 s74, v249, 57
	v_readlane_b32 s75, v249, 58
	v_readlane_b32 s76, v249, 59
	v_readlane_b32 s77, v249, 60
	v_readlane_b32 s78, v249, 61
	v_readlane_b32 s79, v249, 62
	s_barrier

.LBB0_728:
	s_getpc_b64 s[100:101]
	global_load_dword a0, v250, s[100:101]
	s_mov_b32 s15, 0
	v_mbcnt_lo_u32_b32 v152, -1, 0
	v_mbcnt_hi_u32_b32 v152, -1, v152
	s_lshl_b32 s15, s53, 8
	v_readlane_b32 s56, v249, 18
	v_lshrrev_b32_e32 v130, 1, v152
	v_and_or_b32 v130, v130, 24, s15
	s_lshr_b32 s15, s22, 5
	s_mul_i32 s24, s15, 0x1800
	s_ashr_i32 s25, s24, 31
	s_lshl_b64 s[24:25], s[24:25], 2
	s_add_u32 s26, s41, s24
	s_addc_u32 s27, s42, s25
	s_add_u32 s28, s96, s24
	v_or_b32_e32 v130, s45, v130
	s_addc_u32 s29, s97, s25
	v_ashrrev_i32_e32 v131, 31, v130
	s_add_u32 s24, s28, 0x1000
	v_lshlrev_b64 v[132:133], 2, v[130:131]
	s_addc_u32 s25, s29, 0
	v_lshl_add_u64 v[150:151], s[26:27], 0, v[132:133]
	v_lshl_add_u64 v[146:147], s[24:25], 0, v[132:133]
	s_lshl_b32 s15, s22, 8
	global_load_dwordx4 v[138:141], v[150:151], off offset:16
	global_load_dwordx4 v[134:137], v[150:151], off
	global_load_dwordx4 v[142:145], v[146:147], off
	s_nop 0
	global_load_dwordx4 v[146:149], v[146:147], off offset:16
	s_add_i32 s15, s15, s44
	v_and_or_b32 v152, v152, 15, s15
	v_ashrrev_i32_e32 v153, 31, v152
	v_lshlrev_b64 v[162:163], 10, v[152:153]
	v_lshl_add_u64 v[162:163], v[162:163], 0, v[130:131]
	v_lshl_add_u64 v[200:201], s[28:29], 0, v[132:133]
	v_lshlrev_b64 v[212:213], 1, v[162:163]
	v_readlane_b32 s62, v249, 24
	v_readlane_b32 s63, v249, 25
	global_load_dwordx4 v[154:157], v[200:201], off offset:16
	global_load_dwordx4 v[158:161], v[200:201], off
	v_lshl_add_u64 v[214:215], s[90:91], 0, v[212:213]
	v_mov_b32_e32 v246, v212
	v_lshl_add_u64 v[132:133], s[62:63], 0, v[132:133]
	global_load_dwordx4 v[162:165], v[214:215], off
	global_load_dwordx4 v[230:233], v246, s[90:91] offset:256
	v_add_u32_e32 v247, 0x8000, v246
	global_load_dwordx4 v[234:237], v247, s[90:91]
	v_add_u32_e32 v247, 0x8000, v246
	global_load_dwordx4 v[238:241], v247, s[90:91] offset:256
	v_add_u32_e32 v247, 0x10000, v246
	global_load_dwordx4 v[242:245], v247, s[90:91]
	v_add_u32_e32 v247, 0x10000, v246
	global_load_dwordx4 v[226:229], v247, s[90:91] offset:256
	global_load_dwordx4 v[166:169], v[132:133], off
	global_load_dwordx4 v[170:173], v[132:133], off offset:16
	v_or_b32_e32 v204, 0x80, v130
	v_ashrrev_i32_e32 v205, 31, v204
	global_load_dwordx4 v[180:183], v[132:133], off offset:528
	global_load_dwordx4 v[184:187], v[132:133], off offset:512
	global_load_dwordx4 v[188:191], v[150:151], off offset:528
	global_load_dwordx4 v[192:195], v[150:151], off offset:512
	global_load_dwordx4 v[196:199], v[200:201], off offset:528
	s_nop 0
	global_load_dwordx4 v[200:203], v[200:201], off offset:512
	v_lshl_add_u64 v[132:133], v[204:205], 2, s[24:25]
	global_load_dwordx4 v[204:207], v[132:133], off offset:16
	global_load_dwordx4 v[208:211], v[132:133], off
	s_and_b64 vcc, exec, s[0:1]
	s_mov_b64 s[0:1], -1
	v_readlane_b32 s57, v249, 19
	v_readlane_b32 s58, v249, 20
	v_readlane_b32 s59, v249, 21
	v_readlane_b32 s60, v249, 22
	v_readlane_b32 s61, v249, 23
	v_readlane_b32 s64, v249, 26
	v_readlane_b32 s65, v249, 27
	v_readlane_b32 s66, v249, 28
	v_readlane_b32 s67, v249, 29
	v_readlane_b32 s68, v249, 30
	v_readlane_b32 s69, v249, 31
	v_readlane_b32 s70, v249, 32
	v_readlane_b32 s71, v249, 33
	s_waitcnt vmcnt(0)
	v_pk_add_f32 v[138:139], v[138:139], 1.0 op_sel_hi:[1,0]
	v_pk_add_f32 v[132:133], v[136:137], 1.0 op_sel_hi:[1,0]
	v_pk_add_f32 v[136:137], v[134:135], 1.0 op_sel_hi:[1,0]
	v_pk_add_f32 v[134:135], v[140:141], 1.0 op_sel_hi:[1,0]
	v_add_f32_e32 v140, 1.0, v142
	v_add_f32_e32 v141, 1.0, v143
	v_add_f32_e32 v142, 1.0, v144
	v_add_f32_e32 v143, 1.0, v145
	v_add_f32_e32 v144, 1.0, v146
	v_add_f32_e32 v145, 1.0, v147
	v_add_f32_e32 v146, 1.0, v148
	v_add_f32_e32 v147, 1.0, v149
	v_rcp_f32_e32 v140, v140
	v_rcp_f32_e32 v141, v141
	v_rcp_f32_e32 v142, v142
	v_rcp_f32_e32 v143, v143
	v_rcp_f32_e32 v144, v144
	v_rcp_f32_e32 v145, v145
	v_rcp_f32_e32 v146, v146
	v_rcp_f32_e32 v147, v147
	v_pk_mul_f32 v[140:141], v[140:141], s[12:13] op_sel_hi:[1,0]
	v_pk_mul_f32 v[142:143], v[142:143], s[12:13] op_sel_hi:[1,0]
	v_pk_mul_f32 v[144:145], v[144:145], s[12:13] op_sel_hi:[1,0]
	v_pk_mul_f32 v[146:147], v[146:147], s[12:13] op_sel_hi:[1,0]
	v_pk_mul_f32 v[148:149], v[160:161], v[142:143]
	v_pk_mul_f32 v[150:151], v[158:159], v[140:141]
	v_pk_mul_f32 v[156:157], v[156:157], v[146:147]
	v_pk_mul_f32 v[158:159], v[154:155], v[144:145]
	v_lshlrev_b32_e32 v160, 16, v162
	v_and_b32_e32 v161, 0xffff0000, v162
	v_lshlrev_b32_e32 v162, 16, v163
	v_and_b32_e32 v163, 0xffff0000, v163
	v_lshlrev_b32_e32 v216, 16, v164
	v_and_b32_e32 v217, 0xffff0000, v164
	v_lshlrev_b32_e32 v164, 16, v165
	v_and_b32_e32 v165, 0xffff0000, v165
	v_pk_fma_f32 v[148:149], v[168:169], v[132:133], v[148:149] neg_lo:[0,0,1] neg_hi:[0,0,1]
	v_pk_fma_f32 v[154:155], v[166:167], v[136:137], v[150:151] neg_lo:[0,0,1] neg_hi:[0,0,1]
	v_pk_fma_f32 v[150:151], v[172:173], v[134:135], v[156:157] neg_lo:[0,0,1] neg_hi:[0,0,1]
	v_pk_fma_f32 v[156:157], v[170:171], v[138:139], v[158:159] neg_lo:[0,0,1] neg_hi:[0,0,1]
	v_pk_fma_f32 v[158:159], v[140:141], v[160:161], v[154:155]
	v_pk_fma_f32 v[160:161], v[142:143], v[162:163], v[148:149]
	v_pk_fma_f32 v[162:163], v[144:145], v[216:217], v[156:157]
	v_pk_fma_f32 v[164:165], v[146:147], v[164:165], v[150:151]
	v_pk_fma_f32 v[124:125], v[124:125], v[136:137], v[158:159]
	v_pk_fma_f32 v[126:127], v[126:127], v[132:133], v[160:161]
	v_pk_fma_f32 v[158:159], v[120:121], v[138:139], v[162:163]
	v_pk_fma_f32 v[160:161], v[122:123], v[134:135], v[164:165]
	v_cvt_pk_bf16_f32 v120, v124, v125
	v_cvt_pk_bf16_f32 v121, v126, v127
	v_cvt_pk_bf16_f32 v122, v158, v159
	v_cvt_pk_bf16_f32 v123, v160, v161
	v_lshl_add_u64 v[216:217], s[76:77], 0, v[212:213]
	global_store_dwordx4 v[216:217], v[120:123], off
	v_add_f32_e32 v153, 1.0, v208
	v_add_f32_e32 v159, 1.0, v209
	v_add_f32_e32 v160, 1.0, v210
	v_add_f32_e32 v161, 1.0, v211
	v_add_f32_e32 v162, 1.0, v204
	v_add_f32_e32 v163, 1.0, v205
	v_add_f32_e32 v164, 1.0, v206
	v_add_f32_e32 v165, 1.0, v207
	v_rcp_f32_e32 v158, v153
	v_rcp_f32_e32 v159, v159
	v_rcp_f32_e32 v160, v160
	v_rcp_f32_e32 v161, v161
	v_rcp_f32_e32 v162, v162
	v_rcp_f32_e32 v163, v163
	v_rcp_f32_e32 v168, v164
	v_rcp_f32_e32 v169, v165
	v_or_b32_e32 v120, 16, v152
	v_ashrrev_i32_e32 v121, 31, v120
	v_lshlrev_b64 v[120:121], 10, v[120:121]
	v_lshl_add_u64 v[120:121], v[120:121], 0, v[130:131]
	v_pk_mul_f32 v[166:167], v[158:159], s[12:13] op_sel_hi:[1,0]
	v_pk_mul_f32 v[164:165], v[160:161], s[12:13] op_sel_hi:[1,0]
	v_pk_mul_f32 v[160:161], v[162:163], s[12:13] op_sel_hi:[1,0]
	v_pk_mul_f32 v[158:159], v[168:169], s[12:13] op_sel_hi:[1,0]
	v_lshlrev_b64 v[218:219], 1, v[120:121]
	v_pk_add_f32 v[122:123], v[194:195], 1.0 op_sel_hi:[1,0]
	v_pk_add_f32 v[124:125], v[192:193], 1.0 op_sel_hi:[1,0]
	v_pk_add_f32 v[120:121], v[190:191], 1.0 op_sel_hi:[1,0]
	v_pk_add_f32 v[126:127], v[188:189], 1.0 op_sel_hi:[1,0]
	v_pk_mul_f32 v[162:163], v[202:203], v[164:165]
	v_pk_mul_f32 v[168:169], v[200:201], v[166:167]
	v_pk_mul_f32 v[188:189], v[198:199], v[158:159]
	v_pk_mul_f32 v[190:191], v[196:197], v[160:161]
	v_pk_fma_f32 v[170:171], v[186:187], v[122:123], v[162:163] neg_lo:[0,0,1] neg_hi:[0,0,1]
	v_pk_fma_f32 v[172:173], v[184:185], v[124:125], v[168:169] neg_lo:[0,0,1] neg_hi:[0,0,1]
	v_pk_fma_f32 v[162:163], v[182:183], v[120:121], v[188:189] neg_lo:[0,0,1] neg_hi:[0,0,1]
	v_pk_fma_f32 v[168:169], v[180:181], v[126:127], v[190:191] neg_lo:[0,0,1] neg_hi:[0,0,1]
	v_lshl_add_u64 v[220:221], s[90:91], 0, v[218:219]
	s_waitcnt vmcnt(9)
	v_mov_b32_e32 v212, v230
	v_mov_b32_e32 v213, v231
	v_mov_b32_e32 v214, v232
	v_mov_b32_e32 v215, v233
	v_add_u32_e32 v247, 0x18000, v246
	global_load_dwordx4 v[230:233], v247, s[90:91]
	v_lshlrev_b32_e32 v180, 16, v212
	v_and_b32_e32 v181, 0xffff0000, v212
	v_lshlrev_b32_e32 v182, 16, v213
	v_and_b32_e32 v183, 0xffff0000, v213
	v_lshlrev_b32_e32 v184, 16, v214
	v_and_b32_e32 v185, 0xffff0000, v214
	v_lshlrev_b32_e32 v186, 16, v215
	v_and_b32_e32 v187, 0xffff0000, v215
	v_pk_fma_f32 v[180:181], v[166:167], v[180:181], v[172:173]
	v_pk_fma_f32 v[182:183], v[164:165], v[182:183], v[170:171]
	v_pk_fma_f32 v[184:185], v[160:161], v[184:185], v[168:169]
	v_pk_fma_f32 v[186:187], v[158:159], v[186:187], v[162:163]
	v_pk_fma_f32 v[116:117], v[116:117], v[124:125], v[180:181]
	v_pk_fma_f32 v[118:119], v[118:119], v[122:123], v[182:183]
	v_pk_fma_f32 v[180:181], v[112:113], v[126:127], v[184:185]
	v_pk_fma_f32 v[182:183], v[114:115], v[120:121], v[186:187]
	v_cvt_pk_bf16_f32 v112, v116, v117
	v_cvt_pk_bf16_f32 v113, v118, v119
	v_cvt_pk_bf16_f32 v114, v180, v181
	v_cvt_pk_bf16_f32 v115, v182, v183
	global_store_dwordx4 v[216:217], v[112:115], off offset:256
	v_lshl_add_u64 v[116:117], s[76:77], 0, v[218:219]
	s_waitcnt vmcnt(9)
	v_mov_b32_e32 v112, v234
	v_mov_b32_e32 v113, v235
	v_mov_b32_e32 v114, v236
	v_mov_b32_e32 v115, v237
	v_add_u32_e32 v247, 0x18000, v246
	global_load_dwordx4 v[234:237], v247, s[90:91] offset:256
	v_lshlrev_b32_e32 v118, 16, v112
	v_and_b32_e32 v119, 0xffff0000, v112
	v_lshlrev_b32_e32 v112, 16, v113
	v_and_b32_e32 v113, 0xffff0000, v113
	v_lshlrev_b32_e32 v180, 16, v114
	v_and_b32_e32 v181, 0xffff0000, v114
	v_lshlrev_b32_e32 v114, 16, v115
	v_and_b32_e32 v115, 0xffff0000, v115
	v_pk_fma_f32 v[118:119], v[140:141], v[118:119], v[154:155]
	v_pk_fma_f32 v[112:113], v[142:143], v[112:113], v[148:149]
	v_pk_fma_f32 v[180:181], v[144:145], v[180:181], v[156:157]
	v_pk_fma_f32 v[114:115], v[146:147], v[114:115], v[150:151]
	v_pk_fma_f32 v[108:109], v[108:109], v[136:137], v[118:119]
	v_pk_fma_f32 v[110:111], v[110:111], v[132:133], v[112:113]
	v_pk_fma_f32 v[112:113], v[104:105], v[138:139], v[180:181]
	v_pk_fma_f32 v[114:115], v[106:107], v[134:135], v[114:115]
	v_cvt_pk_bf16_f32 v104, v108, v109
	v_cvt_pk_bf16_f32 v105, v110, v111
	v_cvt_pk_bf16_f32 v106, v112, v113
	v_cvt_pk_bf16_f32 v107, v114, v115
	global_store_dwordx4 v[116:117], v[104:107], off
	v_or_b32_e32 v108, 32, v152
	v_ashrrev_i32_e32 v109, 31, v108
	v_lshlrev_b64 v[108:109], 10, v[108:109]
	v_lshl_add_u64 v[108:109], v[108:109], 0, v[130:131]
	v_lshlrev_b64 v[108:109], 1, v[108:109]
	v_lshl_add_u64 v[110:111], s[90:91], 0, v[108:109]
	s_waitcnt vmcnt(9)
	v_mov_b32_e32 v104, v238
	v_mov_b32_e32 v105, v239
	v_mov_b32_e32 v106, v240
	v_mov_b32_e32 v107, v241
	v_add_u32_e32 v247, 0x40000, v246
	global_load_dwordx4 v[238:241], v247, s[90:91]
	v_lshlrev_b32_e32 v112, 16, v104
	v_and_b32_e32 v113, 0xffff0000, v104
	v_lshlrev_b32_e32 v104, 16, v105
	v_and_b32_e32 v105, 0xffff0000, v105
	v_lshlrev_b32_e32 v114, 16, v106
	v_and_b32_e32 v115, 0xffff0000, v106
	v_lshlrev_b32_e32 v106, 16, v107
	v_and_b32_e32 v107, 0xffff0000, v107
	v_pk_fma_f32 v[112:113], v[166:167], v[112:113], v[172:173]
	v_pk_fma_f32 v[104:105], v[164:165], v[104:105], v[170:171]
	v_pk_fma_f32 v[114:115], v[160:161], v[114:115], v[168:169]
	v_pk_fma_f32 v[106:107], v[158:159], v[106:107], v[162:163]
	v_pk_fma_f32 v[100:101], v[100:101], v[124:125], v[112:113]
	v_pk_fma_f32 v[102:103], v[102:103], v[122:123], v[104:105]
	v_pk_fma_f32 v[104:105], v[96:97], v[126:127], v[114:115]
	v_pk_fma_f32 v[106:107], v[98:99], v[120:121], v[106:107]
	v_cvt_pk_bf16_f32 v96, v100, v101
	v_cvt_pk_bf16_f32 v97, v102, v103
	v_cvt_pk_bf16_f32 v98, v104, v105
	v_cvt_pk_bf16_f32 v99, v106, v107
	global_store_dwordx4 v[116:117], v[96:99], off offset:256
	v_lshl_add_u64 v[100:101], s[76:77], 0, v[108:109]
	s_waitcnt vmcnt(9)
	v_mov_b32_e32 v96, v242
	v_mov_b32_e32 v97, v243
	v_mov_b32_e32 v98, v244
	v_mov_b32_e32 v99, v245
	v_add_u32_e32 v247, 0x40000, v246
	global_load_dwordx4 v[242:245], v247, s[90:91] offset:256
	v_lshlrev_b32_e32 v102, 16, v96
	v_and_b32_e32 v103, 0xffff0000, v96
	v_lshlrev_b32_e32 v96, 16, v97
	v_and_b32_e32 v97, 0xffff0000, v97
	v_lshlrev_b32_e32 v104, 16, v98
	v_and_b32_e32 v105, 0xffff0000, v98
	v_lshlrev_b32_e32 v98, 16, v99
	v_and_b32_e32 v99, 0xffff0000, v99
	v_pk_fma_f32 v[102:103], v[140:141], v[102:103], v[154:155]
	v_pk_fma_f32 v[96:97], v[142:143], v[96:97], v[148:149]
	v_pk_fma_f32 v[104:105], v[144:145], v[104:105], v[156:157]
	v_pk_fma_f32 v[98:99], v[146:147], v[98:99], v[150:151]
	v_pk_fma_f32 v[92:93], v[92:93], v[136:137], v[102:103]
	v_pk_fma_f32 v[94:95], v[94:95], v[132:133], v[96:97]
	v_pk_fma_f32 v[96:97], v[88:89], v[138:139], v[104:105]
	v_pk_fma_f32 v[98:99], v[90:91], v[134:135], v[98:99]
	v_cvt_pk_bf16_f32 v88, v92, v93
	v_cvt_pk_bf16_f32 v89, v94, v95
	v_cvt_pk_bf16_f32 v90, v96, v97
	v_cvt_pk_bf16_f32 v91, v98, v99
	global_store_dwordx4 v[100:101], v[88:91], off
	v_or_b32_e32 v92, 48, v152
	v_ashrrev_i32_e32 v93, 31, v92
	v_lshlrev_b64 v[92:93], 10, v[92:93]
	v_lshl_add_u64 v[92:93], v[92:93], 0, v[130:131]
	v_lshlrev_b64 v[92:93], 1, v[92:93]
	v_lshl_add_u64 v[94:95], s[90:91], 0, v[92:93]
	s_waitcnt vmcnt(9)
	v_mov_b32_e32 v88, v226
	v_mov_b32_e32 v89, v227
	v_mov_b32_e32 v90, v228
	v_mov_b32_e32 v91, v229
	v_add_u32_e32 v247, 0x48000, v246
	global_load_dwordx4 v[226:229], v247, s[90:91]
	v_lshlrev_b32_e32 v96, 16, v88
	v_and_b32_e32 v97, 0xffff0000, v88
	v_lshlrev_b32_e32 v88, 16, v89
	v_and_b32_e32 v89, 0xffff0000, v89
	v_lshlrev_b32_e32 v98, 16, v90
	v_and_b32_e32 v99, 0xffff0000, v90
	v_lshlrev_b32_e32 v90, 16, v91
	v_and_b32_e32 v91, 0xffff0000, v91
	v_pk_fma_f32 v[96:97], v[166:167], v[96:97], v[172:173]
	v_pk_fma_f32 v[88:89], v[164:165], v[88:89], v[170:171]
	v_pk_fma_f32 v[98:99], v[160:161], v[98:99], v[168:169]
	v_pk_fma_f32 v[90:91], v[158:159], v[90:91], v[162:163]
	v_pk_fma_f32 v[84:85], v[84:85], v[124:125], v[96:97]
	v_pk_fma_f32 v[86:87], v[86:87], v[122:123], v[88:89]
	v_pk_fma_f32 v[88:89], v[80:81], v[126:127], v[98:99]
	v_pk_fma_f32 v[90:91], v[82:83], v[120:121], v[90:91]
	v_cvt_pk_bf16_f32 v80, v84, v85
	v_cvt_pk_bf16_f32 v81, v86, v87
	v_cvt_pk_bf16_f32 v82, v88, v89
	v_cvt_pk_bf16_f32 v83, v90, v91
	global_store_dwordx4 v[100:101], v[80:83], off offset:256
	v_lshl_add_u64 v[84:85], s[76:77], 0, v[92:93]
	s_waitcnt vmcnt(9)
	v_mov_b32_e32 v80, v230
	v_mov_b32_e32 v81, v231
	v_mov_b32_e32 v82, v232
	v_mov_b32_e32 v83, v233
	v_add_u32_e32 v247, 0x48000, v246
	global_load_dwordx4 v[230:233], v247, s[90:91] offset:256
	v_lshlrev_b32_e32 v86, 16, v80
	v_and_b32_e32 v87, 0xffff0000, v80
	v_lshlrev_b32_e32 v80, 16, v81
	v_and_b32_e32 v81, 0xffff0000, v81
	v_lshlrev_b32_e32 v88, 16, v82
	v_and_b32_e32 v89, 0xffff0000, v82
	v_lshlrev_b32_e32 v82, 16, v83
	v_and_b32_e32 v83, 0xffff0000, v83
	v_pk_fma_f32 v[86:87], v[140:141], v[86:87], v[154:155]
	v_pk_fma_f32 v[80:81], v[142:143], v[80:81], v[148:149]
	v_pk_fma_f32 v[88:89], v[144:145], v[88:89], v[156:157]
	v_pk_fma_f32 v[82:83], v[146:147], v[82:83], v[150:151]
	v_pk_fma_f32 v[76:77], v[76:77], v[136:137], v[86:87]
	v_pk_fma_f32 v[78:79], v[78:79], v[132:133], v[80:81]
	v_pk_fma_f32 v[80:81], v[72:73], v[138:139], v[88:89]
	v_pk_fma_f32 v[82:83], v[74:75], v[134:135], v[82:83]
	v_cvt_pk_bf16_f32 v72, v76, v77
	v_cvt_pk_bf16_f32 v73, v78, v79
	v_cvt_pk_bf16_f32 v74, v80, v81
	v_cvt_pk_bf16_f32 v75, v82, v83
	global_store_dwordx4 v[84:85], v[72:75], off
	v_add_u32_e32 v76, 0x80, v152
	v_ashrrev_i32_e32 v77, 31, v76
	v_lshlrev_b64 v[76:77], 10, v[76:77]
	v_lshl_add_u64 v[76:77], v[76:77], 0, v[130:131]
	v_lshlrev_b64 v[76:77], 1, v[76:77]
	v_lshl_add_u64 v[78:79], s[90:91], 0, v[76:77]
	s_waitcnt vmcnt(9)
	v_mov_b32_e32 v72, v234
	v_mov_b32_e32 v73, v235
	v_mov_b32_e32 v74, v236
	v_mov_b32_e32 v75, v237
	v_add_u32_e32 v247, 0x50000, v246
	global_load_dwordx4 v[234:237], v247, s[90:91]
	v_lshlrev_b32_e32 v80, 16, v72
	v_and_b32_e32 v81, 0xffff0000, v72
	v_lshlrev_b32_e32 v72, 16, v73
	v_and_b32_e32 v73, 0xffff0000, v73
	v_lshlrev_b32_e32 v82, 16, v74
	v_and_b32_e32 v83, 0xffff0000, v74
	v_lshlrev_b32_e32 v74, 16, v75
	v_and_b32_e32 v75, 0xffff0000, v75
	v_pk_fma_f32 v[80:81], v[166:167], v[80:81], v[172:173]
	v_pk_fma_f32 v[72:73], v[164:165], v[72:73], v[170:171]
	v_pk_fma_f32 v[82:83], v[160:161], v[82:83], v[168:169]
	v_pk_fma_f32 v[74:75], v[158:159], v[74:75], v[162:163]
	v_pk_fma_f32 v[68:69], v[68:69], v[124:125], v[80:81]
	v_pk_fma_f32 v[70:71], v[70:71], v[122:123], v[72:73]
	v_pk_fma_f32 v[72:73], v[64:65], v[126:127], v[82:83]
	v_pk_fma_f32 v[74:75], v[66:67], v[120:121], v[74:75]
	v_cvt_pk_bf16_f32 v64, v68, v69
	v_cvt_pk_bf16_f32 v65, v70, v71
	v_cvt_pk_bf16_f32 v66, v72, v73
	v_cvt_pk_bf16_f32 v67, v74, v75
	global_store_dwordx4 v[84:85], v[64:67], off offset:256
	v_lshl_add_u64 v[68:69], s[76:77], 0, v[76:77]
	s_waitcnt vmcnt(9)
	v_mov_b32_e32 v64, v238
	v_mov_b32_e32 v65, v239
	v_mov_b32_e32 v66, v240
	v_mov_b32_e32 v67, v241
	v_add_u32_e32 v247, 0x50000, v246
	global_load_dwordx4 v[238:241], v247, s[90:91] offset:256
	v_lshlrev_b32_e32 v70, 16, v64
	v_and_b32_e32 v71, 0xffff0000, v64
	v_lshlrev_b32_e32 v64, 16, v65
	v_and_b32_e32 v65, 0xffff0000, v65
	v_lshlrev_b32_e32 v72, 16, v66
	v_and_b32_e32 v73, 0xffff0000, v66
	v_lshlrev_b32_e32 v66, 16, v67
	v_and_b32_e32 v67, 0xffff0000, v67
	v_pk_fma_f32 v[70:71], v[140:141], v[70:71], v[154:155]
	v_pk_fma_f32 v[64:65], v[142:143], v[64:65], v[148:149]
	v_pk_fma_f32 v[72:73], v[144:145], v[72:73], v[156:157]
	v_pk_fma_f32 v[66:67], v[146:147], v[66:67], v[150:151]
	v_pk_fma_f32 v[60:61], v[60:61], v[136:137], v[70:71]
	v_pk_fma_f32 v[62:63], v[62:63], v[132:133], v[64:65]
	v_pk_fma_f32 v[64:65], v[56:57], v[138:139], v[72:73]
	v_pk_fma_f32 v[66:67], v[58:59], v[134:135], v[66:67]
	v_cvt_pk_bf16_f32 v56, v60, v61
	v_cvt_pk_bf16_f32 v57, v62, v63
	v_cvt_pk_bf16_f32 v58, v64, v65
	v_cvt_pk_bf16_f32 v59, v66, v67
	global_store_dwordx4 v[68:69], v[56:59], off
	v_add_u32_e32 v60, 0x90, v152
	v_ashrrev_i32_e32 v61, 31, v60
	v_lshlrev_b64 v[60:61], 10, v[60:61]
	v_lshl_add_u64 v[60:61], v[60:61], 0, v[130:131]
	v_lshlrev_b64 v[60:61], 1, v[60:61]
	v_lshl_add_u64 v[62:63], s[90:91], 0, v[60:61]
	s_waitcnt vmcnt(9)
	v_mov_b32_e32 v56, v242
	v_mov_b32_e32 v57, v243
	v_mov_b32_e32 v58, v244
	v_mov_b32_e32 v59, v245
	v_add_u32_e32 v247, 0x58000, v246
	global_load_dwordx4 v[242:245], v247, s[90:91]
	v_lshlrev_b32_e32 v64, 16, v56
	v_and_b32_e32 v65, 0xffff0000, v56
	v_lshlrev_b32_e32 v56, 16, v57
	v_and_b32_e32 v57, 0xffff0000, v57
	v_lshlrev_b32_e32 v66, 16, v58
	v_and_b32_e32 v67, 0xffff0000, v58
	v_lshlrev_b32_e32 v58, 16, v59
	v_and_b32_e32 v59, 0xffff0000, v59
	v_pk_fma_f32 v[64:65], v[166:167], v[64:65], v[172:173]
	v_pk_fma_f32 v[56:57], v[164:165], v[56:57], v[170:171]
	v_pk_fma_f32 v[66:67], v[160:161], v[66:67], v[168:169]
	v_pk_fma_f32 v[58:59], v[158:159], v[58:59], v[162:163]
	v_pk_fma_f32 v[52:53], v[52:53], v[124:125], v[64:65]
	v_pk_fma_f32 v[54:55], v[54:55], v[122:123], v[56:57]
	v_pk_fma_f32 v[56:57], v[48:49], v[126:127], v[66:67]
	v_pk_fma_f32 v[58:59], v[50:51], v[120:121], v[58:59]
	v_cvt_pk_bf16_f32 v48, v52, v53
	v_cvt_pk_bf16_f32 v49, v54, v55
	v_cvt_pk_bf16_f32 v50, v56, v57
	v_cvt_pk_bf16_f32 v51, v58, v59
	global_store_dwordx4 v[68:69], v[48:51], off offset:256
	v_lshl_add_u64 v[52:53], s[76:77], 0, v[60:61]
	s_waitcnt vmcnt(9)
	v_mov_b32_e32 v48, v226
	v_mov_b32_e32 v49, v227
	v_mov_b32_e32 v50, v228
	v_mov_b32_e32 v51, v229
	v_add_u32_e32 v247, 0x58000, v246
	global_load_dwordx4 v[226:229], v247, s[90:91] offset:256
	v_lshlrev_b32_e32 v54, 16, v48
	v_and_b32_e32 v55, 0xffff0000, v48
	v_lshlrev_b32_e32 v48, 16, v49
	v_and_b32_e32 v49, 0xffff0000, v49
	v_lshlrev_b32_e32 v56, 16, v50
	v_and_b32_e32 v57, 0xffff0000, v50
	v_lshlrev_b32_e32 v50, 16, v51
	v_and_b32_e32 v51, 0xffff0000, v51
	v_pk_fma_f32 v[54:55], v[140:141], v[54:55], v[154:155]
	v_pk_fma_f32 v[48:49], v[142:143], v[48:49], v[148:149]
	v_pk_fma_f32 v[56:57], v[144:145], v[56:57], v[156:157]
	v_pk_fma_f32 v[50:51], v[146:147], v[50:51], v[150:151]
	v_pk_fma_f32 v[44:45], v[44:45], v[136:137], v[54:55]
	v_pk_fma_f32 v[46:47], v[46:47], v[132:133], v[48:49]
	v_pk_fma_f32 v[48:49], v[40:41], v[138:139], v[56:57]
	v_pk_fma_f32 v[50:51], v[42:43], v[134:135], v[50:51]
	v_cvt_pk_bf16_f32 v40, v44, v45
	v_cvt_pk_bf16_f32 v41, v46, v47
	v_cvt_pk_bf16_f32 v42, v48, v49
	v_cvt_pk_bf16_f32 v43, v50, v51
	global_store_dwordx4 v[52:53], v[40:43], off
	v_add_u32_e32 v44, 0xa0, v152
	v_ashrrev_i32_e32 v45, 31, v44
	v_lshlrev_b64 v[44:45], 10, v[44:45]
	v_lshl_add_u64 v[44:45], v[44:45], 0, v[130:131]
	v_lshlrev_b64 v[44:45], 1, v[44:45]
	v_lshl_add_u64 v[46:47], s[90:91], 0, v[44:45]
	s_waitcnt vmcnt(9)
	v_mov_b32_e32 v40, v230
	v_mov_b32_e32 v41, v231
	v_mov_b32_e32 v42, v232
	v_mov_b32_e32 v43, v233
	v_lshlrev_b32_e32 v48, 16, v40
	v_and_b32_e32 v49, 0xffff0000, v40
	v_lshlrev_b32_e32 v40, 16, v41
	v_and_b32_e32 v41, 0xffff0000, v41
	v_lshlrev_b32_e32 v50, 16, v42
	v_and_b32_e32 v51, 0xffff0000, v42
	v_lshlrev_b32_e32 v42, 16, v43
	v_and_b32_e32 v43, 0xffff0000, v43
	v_pk_fma_f32 v[48:49], v[166:167], v[48:49], v[172:173]
	v_pk_fma_f32 v[40:41], v[164:165], v[40:41], v[170:171]
	v_pk_fma_f32 v[50:51], v[160:161], v[50:51], v[168:169]
	v_pk_fma_f32 v[42:43], v[158:159], v[42:43], v[162:163]
	v_pk_fma_f32 v[36:37], v[36:37], v[124:125], v[48:49]
	v_pk_fma_f32 v[38:39], v[38:39], v[122:123], v[40:41]
	v_pk_fma_f32 v[40:41], v[32:33], v[126:127], v[50:51]
	v_pk_fma_f32 v[42:43], v[34:35], v[120:121], v[42:43]
	v_cvt_pk_bf16_f32 v32, v36, v37
	v_cvt_pk_bf16_f32 v33, v38, v39
	v_cvt_pk_bf16_f32 v34, v40, v41
	v_cvt_pk_bf16_f32 v35, v42, v43
	global_store_dwordx4 v[52:53], v[32:35], off offset:256
	v_lshl_add_u64 v[36:37], s[76:77], 0, v[44:45]
	s_waitcnt vmcnt(8)
	v_mov_b32_e32 v32, v234
	v_mov_b32_e32 v33, v235
	v_mov_b32_e32 v34, v236
	v_mov_b32_e32 v35, v237
	v_lshlrev_b32_e32 v38, 16, v32
	v_and_b32_e32 v39, 0xffff0000, v32
	v_lshlrev_b32_e32 v32, 16, v33
	v_and_b32_e32 v33, 0xffff0000, v33
	v_lshlrev_b32_e32 v40, 16, v34
	v_and_b32_e32 v41, 0xffff0000, v34
	v_lshlrev_b32_e32 v34, 16, v35
	v_and_b32_e32 v35, 0xffff0000, v35
	v_pk_fma_f32 v[38:39], v[140:141], v[38:39], v[154:155]
	v_pk_fma_f32 v[32:33], v[142:143], v[32:33], v[148:149]
	v_pk_fma_f32 v[40:41], v[144:145], v[40:41], v[156:157]
	v_pk_fma_f32 v[34:35], v[146:147], v[34:35], v[150:151]
	v_pk_fma_f32 v[28:29], v[28:29], v[136:137], v[38:39]
	v_pk_fma_f32 v[30:31], v[30:31], v[132:133], v[32:33]
	v_pk_fma_f32 v[32:33], v[24:25], v[138:139], v[40:41]
	v_pk_fma_f32 v[34:35], v[26:27], v[134:135], v[34:35]
	v_cvt_pk_bf16_f32 v24, v28, v29
	v_cvt_pk_bf16_f32 v25, v30, v31
	v_cvt_pk_bf16_f32 v26, v32, v33
	v_cvt_pk_bf16_f32 v27, v34, v35
	global_store_dwordx4 v[36:37], v[24:27], off
	v_add_u32_e32 v28, 0xb0, v152
	v_ashrrev_i32_e32 v29, 31, v28
	v_lshlrev_b64 v[28:29], 10, v[28:29]
	v_lshl_add_u64 v[28:29], v[28:29], 0, v[130:131]
	v_lshlrev_b64 v[28:29], 1, v[28:29]
	v_lshl_add_u64 v[30:31], s[90:91], 0, v[28:29]
	s_waitcnt vmcnt(7)
	v_mov_b32_e32 v24, v238
	v_mov_b32_e32 v25, v239
	v_mov_b32_e32 v26, v240
	v_mov_b32_e32 v27, v241
	v_lshlrev_b32_e32 v32, 16, v24
	v_and_b32_e32 v33, 0xffff0000, v24
	v_lshlrev_b32_e32 v24, 16, v25
	v_and_b32_e32 v25, 0xffff0000, v25
	v_lshlrev_b32_e32 v34, 16, v26
	v_and_b32_e32 v35, 0xffff0000, v26
	v_lshlrev_b32_e32 v26, 16, v27
	v_and_b32_e32 v27, 0xffff0000, v27
	v_pk_fma_f32 v[32:33], v[166:167], v[32:33], v[172:173]
	v_pk_fma_f32 v[24:25], v[164:165], v[24:25], v[170:171]
	v_pk_fma_f32 v[34:35], v[160:161], v[34:35], v[168:169]
	v_pk_fma_f32 v[26:27], v[158:159], v[26:27], v[162:163]
	v_pk_fma_f32 v[20:21], v[20:21], v[124:125], v[32:33]
	v_pk_fma_f32 v[22:23], v[22:23], v[122:123], v[24:25]
	v_pk_fma_f32 v[24:25], v[16:17], v[126:127], v[34:35]
	v_pk_fma_f32 v[26:27], v[18:19], v[120:121], v[26:27]
	v_cvt_pk_bf16_f32 v16, v20, v21
	v_cvt_pk_bf16_f32 v17, v22, v23
	v_cvt_pk_bf16_f32 v18, v24, v25
	v_cvt_pk_bf16_f32 v19, v26, v27
	global_store_dwordx4 v[36:37], v[16:19], off offset:256
	v_lshl_add_u64 v[20:21], s[76:77], 0, v[28:29]
	s_waitcnt vmcnt(6)
	v_mov_b32_e32 v16, v242
	v_mov_b32_e32 v17, v243
	v_mov_b32_e32 v18, v244
	v_mov_b32_e32 v19, v245
	v_lshlrev_b32_e32 v22, 16, v16
	v_and_b32_e32 v23, 0xffff0000, v16
	v_lshlrev_b32_e32 v16, 16, v17
	v_and_b32_e32 v17, 0xffff0000, v17
	v_lshlrev_b32_e32 v24, 16, v18
	v_and_b32_e32 v25, 0xffff0000, v18
	v_lshlrev_b32_e32 v18, 16, v19
	v_and_b32_e32 v19, 0xffff0000, v19
	v_pk_fma_f32 v[22:23], v[140:141], v[22:23], v[154:155]
	v_pk_fma_f32 v[16:17], v[142:143], v[16:17], v[148:149]
	v_pk_fma_f32 v[24:25], v[144:145], v[24:25], v[156:157]
	v_pk_fma_f32 v[18:19], v[146:147], v[18:19], v[150:151]
	v_pk_fma_f32 v[12:13], v[12:13], v[136:137], v[22:23]
	v_pk_fma_f32 v[14:15], v[14:15], v[132:133], v[16:17]
	v_pk_fma_f32 v[16:17], v[8:9], v[138:139], v[24:25]
	v_pk_fma_f32 v[18:19], v[10:11], v[134:135], v[18:19]
	v_cvt_pk_bf16_f32 v8, v12, v13
	v_cvt_pk_bf16_f32 v9, v14, v15
	v_cvt_pk_bf16_f32 v10, v16, v17
	v_cvt_pk_bf16_f32 v11, v18, v19
	global_store_dwordx4 v[20:21], v[8:11], off
	s_waitcnt vmcnt(5)
	v_mov_b32_e32 v8, v226
	v_mov_b32_e32 v9, v227
	v_mov_b32_e32 v10, v228
	v_mov_b32_e32 v11, v229
	v_lshlrev_b32_e32 v12, 16, v8
	v_and_b32_e32 v13, 0xffff0000, v8
	v_lshlrev_b32_e32 v8, 16, v9
	v_and_b32_e32 v9, 0xffff0000, v9
	v_lshlrev_b32_e32 v14, 16, v10
	v_and_b32_e32 v15, 0xffff0000, v10
	v_lshlrev_b32_e32 v10, 16, v11
	v_and_b32_e32 v11, 0xffff0000, v11
	v_pk_fma_f32 v[12:13], v[166:167], v[12:13], v[172:173]
	v_pk_fma_f32 v[8:9], v[164:165], v[8:9], v[170:171]
	v_pk_fma_f32 v[14:15], v[160:161], v[14:15], v[168:169]
	v_pk_fma_f32 v[10:11], v[158:159], v[10:11], v[162:163]
	v_pk_fma_f32 v[4:5], v[4:5], v[124:125], v[12:13]
	v_pk_fma_f32 v[6:7], v[6:7], v[122:123], v[8:9]
	v_pk_fma_f32 v[8:9], v[0:1], v[126:127], v[14:15]
	v_pk_fma_f32 v[10:11], v[2:3], v[120:121], v[10:11]
	v_cvt_pk_bf16_f32 v0, v4, v5
	v_cvt_pk_bf16_f32 v1, v6, v7
	v_cvt_pk_bf16_f32 v2, v8, v9
	v_cvt_pk_bf16_f32 v3, v10, v11
	global_store_dwordx4 v[20:21], v[0:3], off offset:256
	s_cbranch_vccnz .LBB0_717
	s_andn2_b64 vcc, exec, s[6:7]
	s_cbranch_vccnz .LBB0_716
	s_barrier
	s_branch .LBB0_716

.LBB0_915:
	s_getpc_b64 s[100:101]
	global_load_dword a0, v250, s[100:101]
	s_and_saveexec_b64 s[20:21], s[0:1]
	s_cbranch_execz .LBB0_901
	v_cndmask_b32_e32 v34, v49, v48, vcc
	v_sub_f32_e32 v35, v48, v34
	v_mul_f32_e32 v36, 0x3fb8aa3b, v35
	v_fma_f32 v37, v35, s30, -v36
	v_rndne_f32_e32 v38, v36
	v_fmac_f32_e32 v37, 0x32a5705f, v35
	v_sub_f32_e32 v36, v36, v38
	v_add_f32_e32 v36, v36, v37
	v_exp_f32_e32 v36, v36
	v_cvt_i32_f32_e32 v37, v38
	v_sub_f32_e32 v38, v45, v34
	v_cmp_ngt_f32_e32 vcc, s31, v35
	v_sub_f32_e32 v32, v32, v34
	v_ldexp_f32 v36, v36, v37
	v_mul_f32_e32 v37, 0x3fb8aa3b, v38
	v_fma_f32 v39, v38, s30, -v37
	v_rndne_f32_e32 v40, v37
	v_fmac_f32_e32 v39, 0x32a5705f, v38
	v_sub_f32_e32 v37, v37, v40
	v_add_f32_e32 v37, v37, v39
	v_exp_f32_e32 v37, v37
	v_cvt_i32_f32_e32 v39, v40
	v_cndmask_b32_e32 v36, 0, v36, vcc
	v_cmp_nlt_f32_e32 vcc, s34, v35
	v_sub_f32_e32 v33, v33, v34
	v_mul_f32_e32 v34, 0x3fb8aa3b, v33
	v_cndmask_b32_e32 v35, v125, v36, vcc
	v_ldexp_f32 v36, v37, v39
	v_mul_f32_e32 v37, 0x3fb8aa3b, v32
	v_fma_f32 v39, v32, s30, -v37
	v_rndne_f32_e32 v40, v37
	v_fmac_f32_e32 v39, 0x32a5705f, v32
	v_sub_f32_e32 v37, v37, v40
	v_add_f32_e32 v37, v37, v39
	v_exp_f32_e32 v37, v37
	v_cvt_i32_f32_e32 v39, v40
	v_cmp_ngt_f32_e32 vcc, s31, v38
	v_lshl_add_u32 v41, s26, 7, v118
	v_ldexp_f32 v37, v37, v39
	v_cndmask_b32_e32 v36, 0, v36, vcc
	v_cmp_nlt_f32_e32 vcc, s34, v38
	v_fma_f32 v38, v33, s30, -v34
	v_rndne_f32_e32 v39, v34
	v_fmac_f32_e32 v38, 0x32a5705f, v33
	v_sub_f32_e32 v34, v34, v39
	v_add_f32_e32 v34, v34, v38
	v_exp_f32_e32 v34, v34
	v_cvt_i32_f32_e32 v38, v39
	v_cndmask_b32_e32 v36, v125, v36, vcc
	v_cmp_ngt_f32_e32 vcc, s31, v32
	v_ldexp_f32 v34, v34, v38
	s_nop 0
	v_cndmask_b32_e32 v37, 0, v37, vcc
	v_cmp_nlt_f32_e32 vcc, s34, v32
	s_nop 1
	v_cndmask_b32_e32 v32, v125, v37, vcc
	v_cmp_ngt_f32_e32 vcc, s31, v33
	v_sub_f32_e32 v37, v57, v64
	v_mul_f32_e32 v38, 0x3fb8aa3b, v37
	v_cndmask_b32_e32 v34, 0, v34, vcc
	v_cmp_nlt_f32_e32 vcc, s34, v33
	v_fma_f32 v39, v37, s30, -v38
	v_rndne_f32_e32 v40, v38
	v_cndmask_b32_e32 v33, v125, v34, vcc
	v_add_f32_e32 v32, v33, v32
	v_add_f32_e32 v32, v36, v32
	v_add_f32_e32 v32, v35, v32
	v_div_scale_f32 v33, s[4:5], v32, v32, 1.0
	v_rcp_f32_e32 v34, v33
	v_fmac_f32_e32 v39, 0x32a5705f, v37
	v_sub_f32_e32 v38, v38, v40
	v_add_f32_e32 v38, v38, v39
	v_fma_f32 v35, -v33, v34, 1.0
	v_fmac_f32_e32 v34, v35, v34
	v_div_scale_f32 v35, vcc, 1.0, v32, 1.0
	v_exp_f32_e32 v38, v38
	v_cvt_i32_f32_e32 v39, v40
	v_mul_f32_e32 v36, v35, v34
	v_fma_f32 v40, -v33, v36, v35
	v_fmac_f32_e32 v36, v40, v34
	v_fma_f32 v33, -v33, v36, v35
	v_ldexp_f32 v35, v38, v39
	v_cmp_ngt_f32_e64 s[4:5], s31, v37
	v_div_fmas_f32 v33, v33, v34, v36
	v_div_fixup_f32 v39, v33, v32, 1.0
	v_cndmask_b32_e64 v35, 0, v35, s[4:5]
	v_cmp_nlt_f32_e64 s[4:5], s34, v37
	s_nop 1
	v_cndmask_b32_e64 v35, v125, v35, s[4:5]
	v_add_f32_e32 v35, 1.0, v35
	v_div_scale_f32 v37, s[4:5], v35, v35, 1.0
	v_rcp_f32_e32 v38, v37
	s_nop 0
	v_fma_f32 v32, -v37, v38, 1.0
	v_fmac_f32_e32 v38, v32, v38
	v_div_scale_f32 v32, vcc, 1.0, v35, 1.0
	v_mul_f32_e32 v33, v32, v38
	v_fma_f32 v34, -v37, v33, v32
	v_fmac_f32_e32 v33, v34, v38
	v_fma_f32 v32, -v37, v33, v32
	v_div_fmas_f32 v32, v32, v38, v33
	v_add_u32_e32 v33, v60, v44
	v_div_fixup_f32 v35, v32, v35, 1.0
	v_add_u32_e32 v37, v55, v44
	v_lshl_add_u32 v32, v33, 2, s35
	ds_add_rtn_u32 v34, v32, v123
	v_lshl_add_u32 v32, v37, 2, s35
	ds_add_rtn_u32 v38, v32, v123
	v_sub_f32_e32 v40, 1.0, v35
	v_lshlrev_b32_e32 v32, 1, v127
	v_mul_f32_e32 v35, v39, v35
	v_or_b32_e32 v36, 1, v32
	v_mul_f32_e32 v39, v39, v40
	s_waitcnt lgkmcnt(1)
	ds_write_b128 v41, v[32:35]
	s_waitcnt lgkmcnt(1)
	ds_write_b128 v41, v[36:39] offset:16
	s_branch .LBB0_901

.LBB0_1086:
	s_getpc_b64 s[100:101]
	global_load_dword a0, v250, s[100:101]
	s_or_b64 exec, exec, s[14:15]
	v_and_b32_e32 v6, 7, v6
	v_cmp_ne_u32_e32 vcc, 0, v6
	s_and_saveexec_b64 s[14:15], vcc
	s_cbranch_execz .LBB0_1089
	v_lshlrev_b32_e32 v7, 2, v9
	v_lshlrev_b32_e32 v8, 2, v5
	v_add3_u32 v7, v7, v8, 0
	v_add_u32_e32 v7, 0x24380, v7
	s_mov_b64 s[16:17], 0

.LBB0_1089:
	s_getpc_b64 s[100:101]
	global_load_dword a0, v250, s[100:101]
	s_or_b64 exec, exec, s[14:15]
	v_and_b32_e32 v1, 0x7ffffffe, v3
	v_cmp_ne_u32_e32 vcc, v3, v1
	s_orn2_b64 s[14:15], vcc, exec

.LBB0_1093:
	s_getpc_b64 s[100:101]
	global_load_dword a0, v250, s[100:101]
	s_or_b64 exec, exec, s[0:1]
	v_cmp_eq_u32_e32 vcc, 31, v2
	s_and_b64 exec, exec, vcc
	s_add_i32 s0, 0, 0x24000
	v_mov_b32_e32 v0, s0
	ds_write_b32 v0, v4

.LBB0_1127:
	s_getpc_b64 s[100:101]
	global_load_dword a0, v250, s[100:101]
	s_mov_b32 s14, 0
	s_lshl_b32 s14, s34, 2
	s_add_i32 s14, s3, s14
	v_mbcnt_lo_u32_b32 v146, -1, 0
	v_mbcnt_hi_u32_b32 v146, -1, v146
	v_mov_b32_e32 v128, s14
	ds_read2_b32 v[128:129], v128 offset0:64 offset1:224
	v_and_b32_e32 v143, 15, v146
	v_or_b32_e32 v144, s41, v143
	v_mov_b32_e32 v147, 0
	s_waitcnt lgkmcnt(0)
	v_lshlrev_b32_e32 v130, 2, v128
	v_add_u32_e32 v130, s3, v130
	ds_read_b32 v145, v130 offset:4
	v_ashrrev_i32_e32 v133, 31, v128
	v_mov_b32_e32 v132, v128
	v_add_u32_e32 v130, v129, v144
	v_lshlrev_b64 v[132:133], 16, v[132:133]
	s_waitcnt lgkmcnt(0)
	v_cmp_lt_i32_e32 vcc, v130, v145
	v_mov_b32_e32 v128, 0
	v_lshl_add_u64 v[132:133], s[10:11], 0, v[132:133]
	v_ashrrev_i32_e32 v131, 31, v130
	v_readlane_b32 s72, v249, 55
	v_readlane_b32 s73, v249, 56
	v_readlane_b32 s74, v249, 57
	v_readlane_b32 s75, v249, 58
	v_readlane_b32 s76, v249, 59
	v_readlane_b32 s77, v249, 60
	v_readlane_b32 s78, v249, 61
	v_readlane_b32 s79, v249, 62
	v_bfe_u32 v148, v146, 4, 2
	s_lshl_b32 s14, s64, 7
	v_lshl_add_u64 v[152:153], v[130:131], 2, v[132:133]
	v_lshl_or_b32 v149, v148, 3, s14
	global_load_dword v154, v[152:153], off
	global_load_dword v155, v[152:153], off offset:64
	global_load_dword v156, v[152:153], off offset:128
	global_load_dword v157, v[152:153], off offset:192
	global_load_dword v158, v[152:153], off offset:512
	global_load_dword v159, v[152:153], off offset:576
	global_load_dword v160, v[152:153], off offset:640
	global_load_dword v161, v[152:153], off offset:704
	s_lshl_b32 s14, s34, 8
	v_or_b32_e32 v149, s42, v149
	v_add_u32_e32 v150, s14, v144
	v_lshl_add_u32 v150, v150, 8, v149
	v_cmp_lt_i32_e32 vcc, v130, v145
	s_waitcnt vmcnt(7)
	v_mul_f32_e32 v163, 0x3c800000, v154
	v_mul_f32_e32 v164, 0xbd38aa3b, v124
	v_mul_f32_e32 v165, 0xbd38aa3b, v125
	v_mul_f32_e32 v166, 0xbd38aa3b, v126
	v_mul_f32_e32 v167, 0xbd38aa3b, v127
	v_mul_f32_e32 v168, 0xbd38aa3b, v116
	v_mul_f32_e32 v169, 0xbd38aa3b, v117
	v_mul_f32_e32 v170, 0xbd38aa3b, v118
	v_mul_f32_e32 v171, 0xbd38aa3b, v119
	v_exp_f32_e32 v164, v164
	v_exp_f32_e32 v165, v165
	v_exp_f32_e32 v166, v166
	v_exp_f32_e32 v167, v167
	v_exp_f32_e32 v168, v168
	v_exp_f32_e32 v169, v169
	v_exp_f32_e32 v170, v170
	v_exp_f32_e32 v171, v171
	v_add_f32_e32 v164, 1.0, v164
	v_add_f32_e32 v165, 1.0, v165
	v_add_f32_e32 v166, 1.0, v166
	v_add_f32_e32 v167, 1.0, v167
	v_add_f32_e32 v168, 1.0, v168
	v_add_f32_e32 v169, 1.0, v169
	v_add_f32_e32 v170, 1.0, v170
	v_add_f32_e32 v171, 1.0, v171
	v_rcp_f32_e32 v164, v164
	v_rcp_f32_e32 v165, v165
	v_rcp_f32_e32 v166, v166
	v_rcp_f32_e32 v167, v167
	v_rcp_f32_e32 v168, v168
	v_rcp_f32_e32 v169, v169
	v_rcp_f32_e32 v170, v170
	v_rcp_f32_e32 v171, v171
	v_mul_f32_e32 v164, v124, v164
	v_mul_f32_e32 v165, v125, v165
	v_mul_f32_e32 v166, v126, v166
	v_mul_f32_e32 v167, v127, v167
	v_mul_f32_e32 v168, v116, v168
	v_mul_f32_e32 v169, v117, v169
	v_mul_f32_e32 v170, v118, v170
	v_mul_f32_e32 v171, v119, v171
	v_mul_f32_e32 v164, v164, v120
	v_mul_f32_e32 v165, v165, v121
	v_mul_f32_e32 v166, v166, v122
	v_mul_f32_e32 v167, v167, v123
	v_mul_f32_e32 v168, v168, v112
	v_mul_f32_e32 v169, v169, v113
	v_mul_f32_e32 v170, v170, v114
	v_mul_f32_e32 v171, v171, v115
	v_mul_f32_e32 v164, v164, v163
	v_mul_f32_e32 v165, v165, v163
	v_mul_f32_e32 v166, v166, v163
	v_mul_f32_e32 v167, v167, v163
	v_mul_f32_e32 v168, v168, v163
	v_mul_f32_e32 v169, v169, v163
	v_mul_f32_e32 v170, v170, v163
	v_mul_f32_e32 v171, v171, v163
	v_max_f32_e32 v164, 0xc3e00000, v164
	v_max_f32_e32 v165, 0xc3e00000, v165
	v_max_f32_e32 v166, 0xc3e00000, v166
	v_max_f32_e32 v167, 0xc3e00000, v167
	v_max_f32_e32 v168, 0xc3e00000, v168
	v_max_f32_e32 v169, 0xc3e00000, v169
	v_max_f32_e32 v170, 0xc3e00000, v170
	v_max_f32_e32 v171, 0xc3e00000, v171
	v_min_f32_e32 v164, 0x43e00000, v164
	v_min_f32_e32 v165, 0x43e00000, v165
	v_min_f32_e32 v166, 0x43e00000, v166
	v_min_f32_e32 v167, 0x43e00000, v167
	v_min_f32_e32 v168, 0x43e00000, v168
	v_min_f32_e32 v169, 0x43e00000, v169
	v_min_f32_e32 v170, 0x43e00000, v170
	v_min_f32_e32 v171, 0x43e00000, v171
	v_cndmask_b32_e32 v164, 0, v164, vcc
	v_cndmask_b32_e32 v165, 0, v165, vcc
	v_cndmask_b32_e32 v166, 0, v166, vcc
	v_cndmask_b32_e32 v167, 0, v167, vcc
	v_cndmask_b32_e32 v168, 0, v168, vcc
	v_cndmask_b32_e32 v169, 0, v169, vcc
	v_cndmask_b32_e32 v170, 0, v170, vcc
	v_cndmask_b32_e32 v171, 0, v171, vcc
	v_mov_b32_e32 v188, 0
	v_mov_b32_e32 v189, 0
	v_cvt_pk_fp8_f32 v188, v164, v165
	v_cvt_pk_fp8_f32 v189, v168, v169
	v_mov_b32_e32 v192, v150
	v_cvt_pk_fp8_f32 v188, v166, v167 op_sel:[0,0,1]
	v_cvt_pk_fp8_f32 v189, v170, v171 op_sel:[0,0,1]
	s_nop 1
	global_store_dwordx2 v192, v[188:189], s[12:13] sc1
	v_add_u32_e32 v162, 0x10, v130
	v_cmp_lt_i32_e32 vcc, v162, v145
	s_waitcnt vmcnt(7)
	v_mul_f32_e32 v163, 0x3c800000, v155
	v_mul_f32_e32 v164, 0xbd38aa3b, v108
	v_mul_f32_e32 v165, 0xbd38aa3b, v109
	v_mul_f32_e32 v166, 0xbd38aa3b, v110
	v_mul_f32_e32 v167, 0xbd38aa3b, v111
	v_mul_f32_e32 v168, 0xbd38aa3b, v100
	v_mul_f32_e32 v169, 0xbd38aa3b, v101
	v_mul_f32_e32 v170, 0xbd38aa3b, v102
	v_mul_f32_e32 v171, 0xbd38aa3b, v103
	v_exp_f32_e32 v164, v164
	v_exp_f32_e32 v165, v165
	v_exp_f32_e32 v166, v166
	v_exp_f32_e32 v167, v167
	v_exp_f32_e32 v168, v168
	v_exp_f32_e32 v169, v169
	v_exp_f32_e32 v170, v170
	v_exp_f32_e32 v171, v171
	v_add_f32_e32 v164, 1.0, v164
	v_add_f32_e32 v165, 1.0, v165
	v_add_f32_e32 v166, 1.0, v166
	v_add_f32_e32 v167, 1.0, v167
	v_add_f32_e32 v168, 1.0, v168
	v_add_f32_e32 v169, 1.0, v169
	v_add_f32_e32 v170, 1.0, v170
	v_add_f32_e32 v171, 1.0, v171
	v_rcp_f32_e32 v164, v164
	v_rcp_f32_e32 v165, v165
	v_rcp_f32_e32 v166, v166
	v_rcp_f32_e32 v167, v167
	v_rcp_f32_e32 v168, v168
	v_rcp_f32_e32 v169, v169
	v_rcp_f32_e32 v170, v170
	v_rcp_f32_e32 v171, v171
	v_mul_f32_e32 v164, v108, v164
	v_mul_f32_e32 v165, v109, v165
	v_mul_f32_e32 v166, v110, v166
	v_mul_f32_e32 v167, v111, v167
	v_mul_f32_e32 v168, v100, v168
	v_mul_f32_e32 v169, v101, v169
	v_mul_f32_e32 v170, v102, v170
	v_mul_f32_e32 v171, v103, v171
	v_mul_f32_e32 v164, v164, v104
	v_mul_f32_e32 v165, v165, v105
	v_mul_f32_e32 v166, v166, v106
	v_mul_f32_e32 v167, v167, v107
	v_mul_f32_e32 v168, v168, v96
	v_mul_f32_e32 v169, v169, v97
	v_mul_f32_e32 v170, v170, v98
	v_mul_f32_e32 v171, v171, v99
	v_mul_f32_e32 v164, v164, v163
	v_mul_f32_e32 v165, v165, v163
	v_mul_f32_e32 v166, v166, v163
	v_mul_f32_e32 v167, v167, v163
	v_mul_f32_e32 v168, v168, v163
	v_mul_f32_e32 v169, v169, v163
	v_mul_f32_e32 v170, v170, v163
	v_mul_f32_e32 v171, v171, v163
	v_max_f32_e32 v164, 0xc3e00000, v164
	v_max_f32_e32 v165, 0xc3e00000, v165
	v_max_f32_e32 v166, 0xc3e00000, v166
	v_max_f32_e32 v167, 0xc3e00000, v167
	v_max_f32_e32 v168, 0xc3e00000, v168
	v_max_f32_e32 v169, 0xc3e00000, v169
	v_max_f32_e32 v170, 0xc3e00000, v170
	v_max_f32_e32 v171, 0xc3e00000, v171
	v_min_f32_e32 v164, 0x43e00000, v164
	v_min_f32_e32 v165, 0x43e00000, v165
	v_min_f32_e32 v166, 0x43e00000, v166
	v_min_f32_e32 v167, 0x43e00000, v167
	v_min_f32_e32 v168, 0x43e00000, v168
	v_min_f32_e32 v169, 0x43e00000, v169
	v_min_f32_e32 v170, 0x43e00000, v170
	v_min_f32_e32 v171, 0x43e00000, v171
	v_cndmask_b32_e32 v164, 0, v164, vcc
	v_cndmask_b32_e32 v165, 0, v165, vcc
	v_cndmask_b32_e32 v166, 0, v166, vcc
	v_cndmask_b32_e32 v167, 0, v167, vcc
	v_cndmask_b32_e32 v168, 0, v168, vcc
	v_cndmask_b32_e32 v169, 0, v169, vcc
	v_cndmask_b32_e32 v170, 0, v170, vcc
	v_cndmask_b32_e32 v171, 0, v171, vcc
	v_mov_b32_e32 v190, 0
	v_mov_b32_e32 v191, 0
	v_cvt_pk_fp8_f32 v190, v164, v165
	v_cvt_pk_fp8_f32 v191, v168, v169
	v_add_u32_e32 v192, 0x1000, v150
	v_cvt_pk_fp8_f32 v190, v166, v167 op_sel:[0,0,1]
	v_cvt_pk_fp8_f32 v191, v170, v171 op_sel:[0,0,1]
	s_nop 1
	global_store_dwordx2 v192, v[190:191], s[12:13] sc1
	v_add_u32_e32 v162, 0x20, v130
	v_cmp_lt_i32_e32 vcc, v162, v145
	s_waitcnt vmcnt(7)
	v_mul_f32_e32 v163, 0x3c800000, v156
	v_mul_f32_e32 v164, 0xbd38aa3b, v92
	v_mul_f32_e32 v165, 0xbd38aa3b, v93
	v_mul_f32_e32 v166, 0xbd38aa3b, v94
	v_mul_f32_e32 v167, 0xbd38aa3b, v95
	v_mul_f32_e32 v168, 0xbd38aa3b, v84
	v_mul_f32_e32 v169, 0xbd38aa3b, v85
	v_mul_f32_e32 v170, 0xbd38aa3b, v86
	v_mul_f32_e32 v171, 0xbd38aa3b, v87
	v_exp_f32_e32 v164, v164
	v_exp_f32_e32 v165, v165
	v_exp_f32_e32 v166, v166
	v_exp_f32_e32 v167, v167
	v_exp_f32_e32 v168, v168
	v_exp_f32_e32 v169, v169
	v_exp_f32_e32 v170, v170
	v_exp_f32_e32 v171, v171
	v_add_f32_e32 v164, 1.0, v164
	v_add_f32_e32 v165, 1.0, v165
	v_add_f32_e32 v166, 1.0, v166
	v_add_f32_e32 v167, 1.0, v167
	v_add_f32_e32 v168, 1.0, v168
	v_add_f32_e32 v169, 1.0, v169
	v_add_f32_e32 v170, 1.0, v170
	v_add_f32_e32 v171, 1.0, v171
	v_rcp_f32_e32 v164, v164
	v_rcp_f32_e32 v165, v165
	v_rcp_f32_e32 v166, v166
	v_rcp_f32_e32 v167, v167
	v_rcp_f32_e32 v168, v168
	v_rcp_f32_e32 v169, v169
	v_rcp_f32_e32 v170, v170
	v_rcp_f32_e32 v171, v171
	v_mul_f32_e32 v164, v92, v164
	v_mul_f32_e32 v165, v93, v165
	v_mul_f32_e32 v166, v94, v166
	v_mul_f32_e32 v167, v95, v167
	v_mul_f32_e32 v168, v84, v168
	v_mul_f32_e32 v169, v85, v169
	v_mul_f32_e32 v170, v86, v170
	v_mul_f32_e32 v171, v87, v171
	v_mul_f32_e32 v164, v164, v88
	v_mul_f32_e32 v165, v165, v89
	v_mul_f32_e32 v166, v166, v90
	v_mul_f32_e32 v167, v167, v91
	v_mul_f32_e32 v168, v168, v80
	v_mul_f32_e32 v169, v169, v81
	v_mul_f32_e32 v170, v170, v82
	v_mul_f32_e32 v171, v171, v83
	v_mul_f32_e32 v164, v164, v163
	v_mul_f32_e32 v165, v165, v163
	v_mul_f32_e32 v166, v166, v163
	v_mul_f32_e32 v167, v167, v163
	v_mul_f32_e32 v168, v168, v163
	v_mul_f32_e32 v169, v169, v163
	v_mul_f32_e32 v170, v170, v163
	v_mul_f32_e32 v171, v171, v163
	v_max_f32_e32 v164, 0xc3e00000, v164
	v_max_f32_e32 v165, 0xc3e00000, v165
	v_max_f32_e32 v166, 0xc3e00000, v166
	v_max_f32_e32 v167, 0xc3e00000, v167
	v_max_f32_e32 v168, 0xc3e00000, v168
	v_max_f32_e32 v169, 0xc3e00000, v169
	v_max_f32_e32 v170, 0xc3e00000, v170
	v_max_f32_e32 v171, 0xc3e00000, v171
	v_min_f32_e32 v164, 0x43e00000, v164
	v_min_f32_e32 v165, 0x43e00000, v165
	v_min_f32_e32 v166, 0x43e00000, v166
	v_min_f32_e32 v167, 0x43e00000, v167
	v_min_f32_e32 v168, 0x43e00000, v168
	v_min_f32_e32 v169, 0x43e00000, v169
	v_min_f32_e32 v170, 0x43e00000, v170
	v_min_f32_e32 v171, 0x43e00000, v171
	v_cndmask_b32_e32 v164, 0, v164, vcc
	v_cndmask_b32_e32 v165, 0, v165, vcc
	v_cndmask_b32_e32 v166, 0, v166, vcc
	v_cndmask_b32_e32 v167, 0, v167, vcc
	v_cndmask_b32_e32 v168, 0, v168, vcc
	v_cndmask_b32_e32 v169, 0, v169, vcc
	v_cndmask_b32_e32 v170, 0, v170, vcc
	v_cndmask_b32_e32 v171, 0, v171, vcc
	v_mov_b32_e32 v188, 0
	v_mov_b32_e32 v189, 0
	v_cvt_pk_fp8_f32 v188, v164, v165
	v_cvt_pk_fp8_f32 v189, v168, v169
	v_add_u32_e32 v192, 0x2000, v150
	v_cvt_pk_fp8_f32 v188, v166, v167 op_sel:[0,0,1]
	v_cvt_pk_fp8_f32 v189, v170, v171 op_sel:[0,0,1]
	s_nop 1
	global_store_dwordx2 v192, v[188:189], s[12:13] sc1
	v_add_u32_e32 v162, 0x30, v130
	v_cmp_lt_i32_e32 vcc, v162, v145
	s_waitcnt vmcnt(7)
	v_mul_f32_e32 v163, 0x3c800000, v157
	v_mul_f32_e32 v164, 0xbd38aa3b, v76
	v_mul_f32_e32 v165, 0xbd38aa3b, v77
	v_mul_f32_e32 v166, 0xbd38aa3b, v78
	v_mul_f32_e32 v167, 0xbd38aa3b, v79
	v_mul_f32_e32 v168, 0xbd38aa3b, v68
	v_mul_f32_e32 v169, 0xbd38aa3b, v69
	v_mul_f32_e32 v170, 0xbd38aa3b, v70
	v_mul_f32_e32 v171, 0xbd38aa3b, v71
	v_exp_f32_e32 v164, v164
	v_exp_f32_e32 v165, v165
	v_exp_f32_e32 v166, v166
	v_exp_f32_e32 v167, v167
	v_exp_f32_e32 v168, v168
	v_exp_f32_e32 v169, v169
	v_exp_f32_e32 v170, v170
	v_exp_f32_e32 v171, v171
	v_add_f32_e32 v164, 1.0, v164
	v_add_f32_e32 v165, 1.0, v165
	v_add_f32_e32 v166, 1.0, v166
	v_add_f32_e32 v167, 1.0, v167
	v_add_f32_e32 v168, 1.0, v168
	v_add_f32_e32 v169, 1.0, v169
	v_add_f32_e32 v170, 1.0, v170
	v_add_f32_e32 v171, 1.0, v171
	v_rcp_f32_e32 v164, v164
	v_rcp_f32_e32 v165, v165
	v_rcp_f32_e32 v166, v166
	v_rcp_f32_e32 v167, v167
	v_rcp_f32_e32 v168, v168
	v_rcp_f32_e32 v169, v169
	v_rcp_f32_e32 v170, v170
	v_rcp_f32_e32 v171, v171
	v_mul_f32_e32 v164, v76, v164
	v_mul_f32_e32 v165, v77, v165
	v_mul_f32_e32 v166, v78, v166
	v_mul_f32_e32 v167, v79, v167
	v_mul_f32_e32 v168, v68, v168
	v_mul_f32_e32 v169, v69, v169
	v_mul_f32_e32 v170, v70, v170
	v_mul_f32_e32 v171, v71, v171
	v_mul_f32_e32 v164, v164, v72
	v_mul_f32_e32 v165, v165, v73
	v_mul_f32_e32 v166, v166, v74
	v_mul_f32_e32 v167, v167, v75
	v_mul_f32_e32 v168, v168, v64
	v_mul_f32_e32 v169, v169, v65
	v_mul_f32_e32 v170, v170, v66
	v_mul_f32_e32 v171, v171, v67
	v_mul_f32_e32 v164, v164, v163
	v_mul_f32_e32 v165, v165, v163
	v_mul_f32_e32 v166, v166, v163
	v_mul_f32_e32 v167, v167, v163
	v_mul_f32_e32 v168, v168, v163
	v_mul_f32_e32 v169, v169, v163
	v_mul_f32_e32 v170, v170, v163
	v_mul_f32_e32 v171, v171, v163
	v_max_f32_e32 v164, 0xc3e00000, v164
	v_max_f32_e32 v165, 0xc3e00000, v165
	v_max_f32_e32 v166, 0xc3e00000, v166
	v_max_f32_e32 v167, 0xc3e00000, v167
	v_max_f32_e32 v168, 0xc3e00000, v168
	v_max_f32_e32 v169, 0xc3e00000, v169
	v_max_f32_e32 v170, 0xc3e00000, v170
	v_max_f32_e32 v171, 0xc3e00000, v171
	v_min_f32_e32 v164, 0x43e00000, v164
	v_min_f32_e32 v165, 0x43e00000, v165
	v_min_f32_e32 v166, 0x43e00000, v166
	v_min_f32_e32 v167, 0x43e00000, v167
	v_min_f32_e32 v168, 0x43e00000, v168
	v_min_f32_e32 v169, 0x43e00000, v169
	v_min_f32_e32 v170, 0x43e00000, v170
	v_min_f32_e32 v171, 0x43e00000, v171
	v_cndmask_b32_e32 v164, 0, v164, vcc
	v_cndmask_b32_e32 v165, 0, v165, vcc
	v_cndmask_b32_e32 v166, 0, v166, vcc
	v_cndmask_b32_e32 v167, 0, v167, vcc
	v_cndmask_b32_e32 v168, 0, v168, vcc
	v_cndmask_b32_e32 v169, 0, v169, vcc
	v_cndmask_b32_e32 v170, 0, v170, vcc
	v_cndmask_b32_e32 v171, 0, v171, vcc
	v_mov_b32_e32 v190, 0
	v_mov_b32_e32 v191, 0
	v_cvt_pk_fp8_f32 v190, v164, v165
	v_cvt_pk_fp8_f32 v191, v168, v169
	v_add_u32_e32 v192, 0x3000, v150
	v_cvt_pk_fp8_f32 v190, v166, v167 op_sel:[0,0,1]
	v_cvt_pk_fp8_f32 v191, v170, v171 op_sel:[0,0,1]
	s_nop 1
	global_store_dwordx2 v192, v[190:191], s[12:13] sc1
	v_add_u32_e32 v162, 0x80, v130
	v_cmp_lt_i32_e32 vcc, v162, v145
	s_waitcnt vmcnt(7)
	v_mul_f32_e32 v163, 0x3c800000, v158
	v_mul_f32_e32 v164, 0xbd38aa3b, v60
	v_mul_f32_e32 v165, 0xbd38aa3b, v61
	v_mul_f32_e32 v166, 0xbd38aa3b, v62
	v_mul_f32_e32 v167, 0xbd38aa3b, v63
	v_mul_f32_e32 v168, 0xbd38aa3b, v52
	v_mul_f32_e32 v169, 0xbd38aa3b, v53
	v_mul_f32_e32 v170, 0xbd38aa3b, v54
	v_mul_f32_e32 v171, 0xbd38aa3b, v55
	v_exp_f32_e32 v164, v164
	v_exp_f32_e32 v165, v165
	v_exp_f32_e32 v166, v166
	v_exp_f32_e32 v167, v167
	v_exp_f32_e32 v168, v168
	v_exp_f32_e32 v169, v169
	v_exp_f32_e32 v170, v170
	v_exp_f32_e32 v171, v171
	v_add_f32_e32 v164, 1.0, v164
	v_add_f32_e32 v165, 1.0, v165
	v_add_f32_e32 v166, 1.0, v166
	v_add_f32_e32 v167, 1.0, v167
	v_add_f32_e32 v168, 1.0, v168
	v_add_f32_e32 v169, 1.0, v169
	v_add_f32_e32 v170, 1.0, v170
	v_add_f32_e32 v171, 1.0, v171
	v_rcp_f32_e32 v164, v164
	v_rcp_f32_e32 v165, v165
	v_rcp_f32_e32 v166, v166
	v_rcp_f32_e32 v167, v167
	v_rcp_f32_e32 v168, v168
	v_rcp_f32_e32 v169, v169
	v_rcp_f32_e32 v170, v170
	v_rcp_f32_e32 v171, v171
	v_mul_f32_e32 v164, v60, v164
	v_mul_f32_e32 v165, v61, v165
	v_mul_f32_e32 v166, v62, v166
	v_mul_f32_e32 v167, v63, v167
	v_mul_f32_e32 v168, v52, v168
	v_mul_f32_e32 v169, v53, v169
	v_mul_f32_e32 v170, v54, v170
	v_mul_f32_e32 v171, v55, v171
	v_mul_f32_e32 v164, v164, v56
	v_mul_f32_e32 v165, v165, v57
	v_mul_f32_e32 v166, v166, v58
	v_mul_f32_e32 v167, v167, v59
	v_mul_f32_e32 v168, v168, v48
	v_mul_f32_e32 v169, v169, v49
	v_mul_f32_e32 v170, v170, v50
	v_mul_f32_e32 v171, v171, v51
	v_mul_f32_e32 v164, v164, v163
	v_mul_f32_e32 v165, v165, v163
	v_mul_f32_e32 v166, v166, v163
	v_mul_f32_e32 v167, v167, v163
	v_mul_f32_e32 v168, v168, v163
	v_mul_f32_e32 v169, v169, v163
	v_mul_f32_e32 v170, v170, v163
	v_mul_f32_e32 v171, v171, v163
	v_max_f32_e32 v164, 0xc3e00000, v164
	v_max_f32_e32 v165, 0xc3e00000, v165
	v_max_f32_e32 v166, 0xc3e00000, v166
	v_max_f32_e32 v167, 0xc3e00000, v167
	v_max_f32_e32 v168, 0xc3e00000, v168
	v_max_f32_e32 v169, 0xc3e00000, v169
	v_max_f32_e32 v170, 0xc3e00000, v170
	v_max_f32_e32 v171, 0xc3e00000, v171
	v_min_f32_e32 v164, 0x43e00000, v164
	v_min_f32_e32 v165, 0x43e00000, v165
	v_min_f32_e32 v166, 0x43e00000, v166
	v_min_f32_e32 v167, 0x43e00000, v167
	v_min_f32_e32 v168, 0x43e00000, v168
	v_min_f32_e32 v169, 0x43e00000, v169
	v_min_f32_e32 v170, 0x43e00000, v170
	v_min_f32_e32 v171, 0x43e00000, v171
	v_cndmask_b32_e32 v164, 0, v164, vcc
	v_cndmask_b32_e32 v165, 0, v165, vcc
	v_cndmask_b32_e32 v166, 0, v166, vcc
	v_cndmask_b32_e32 v167, 0, v167, vcc
	v_cndmask_b32_e32 v168, 0, v168, vcc
	v_cndmask_b32_e32 v169, 0, v169, vcc
	v_cndmask_b32_e32 v170, 0, v170, vcc
	v_cndmask_b32_e32 v171, 0, v171, vcc
	v_mov_b32_e32 v188, 0
	v_mov_b32_e32 v189, 0
	v_cvt_pk_fp8_f32 v188, v164, v165
	v_cvt_pk_fp8_f32 v189, v168, v169
	v_add_u32_e32 v192, 0x8000, v150
	v_cvt_pk_fp8_f32 v188, v166, v167 op_sel:[0,0,1]
	v_cvt_pk_fp8_f32 v189, v170, v171 op_sel:[0,0,1]
	s_nop 1
	global_store_dwordx2 v192, v[188:189], s[12:13] sc1
	v_add_u32_e32 v162, 0x90, v130
	v_cmp_lt_i32_e32 vcc, v162, v145
	s_waitcnt vmcnt(7)
	v_mul_f32_e32 v163, 0x3c800000, v159
	v_mul_f32_e32 v164, 0xbd38aa3b, v44
	v_mul_f32_e32 v165, 0xbd38aa3b, v45
	v_mul_f32_e32 v166, 0xbd38aa3b, v46
	v_mul_f32_e32 v167, 0xbd38aa3b, v47
	v_mul_f32_e32 v168, 0xbd38aa3b, v36
	v_mul_f32_e32 v169, 0xbd38aa3b, v37
	v_mul_f32_e32 v170, 0xbd38aa3b, v38
	v_mul_f32_e32 v171, 0xbd38aa3b, v39
	v_exp_f32_e32 v164, v164
	v_exp_f32_e32 v165, v165
	v_exp_f32_e32 v166, v166
	v_exp_f32_e32 v167, v167
	v_exp_f32_e32 v168, v168
	v_exp_f32_e32 v169, v169
	v_exp_f32_e32 v170, v170
	v_exp_f32_e32 v171, v171
	v_add_f32_e32 v164, 1.0, v164
	v_add_f32_e32 v165, 1.0, v165
	v_add_f32_e32 v166, 1.0, v166
	v_add_f32_e32 v167, 1.0, v167
	v_add_f32_e32 v168, 1.0, v168
	v_add_f32_e32 v169, 1.0, v169
	v_add_f32_e32 v170, 1.0, v170
	v_add_f32_e32 v171, 1.0, v171
	v_rcp_f32_e32 v164, v164
	v_rcp_f32_e32 v165, v165
	v_rcp_f32_e32 v166, v166
	v_rcp_f32_e32 v167, v167
	v_rcp_f32_e32 v168, v168
	v_rcp_f32_e32 v169, v169
	v_rcp_f32_e32 v170, v170
	v_rcp_f32_e32 v171, v171
	v_mul_f32_e32 v164, v44, v164
	v_mul_f32_e32 v165, v45, v165
	v_mul_f32_e32 v166, v46, v166
	v_mul_f32_e32 v167, v47, v167
	v_mul_f32_e32 v168, v36, v168
	v_mul_f32_e32 v169, v37, v169
	v_mul_f32_e32 v170, v38, v170
	v_mul_f32_e32 v171, v39, v171
	v_mul_f32_e32 v164, v164, v40
	v_mul_f32_e32 v165, v165, v41
	v_mul_f32_e32 v166, v166, v42
	v_mul_f32_e32 v167, v167, v43
	v_mul_f32_e32 v168, v168, v32
	v_mul_f32_e32 v169, v169, v33
	v_mul_f32_e32 v170, v170, v34
	v_mul_f32_e32 v171, v171, v35
	v_mul_f32_e32 v164, v164, v163
	v_mul_f32_e32 v165, v165, v163
	v_mul_f32_e32 v166, v166, v163
	v_mul_f32_e32 v167, v167, v163
	v_mul_f32_e32 v168, v168, v163
	v_mul_f32_e32 v169, v169, v163
	v_mul_f32_e32 v170, v170, v163
	v_mul_f32_e32 v171, v171, v163
	v_max_f32_e32 v164, 0xc3e00000, v164
	v_max_f32_e32 v165, 0xc3e00000, v165
	v_max_f32_e32 v166, 0xc3e00000, v166
	v_max_f32_e32 v167, 0xc3e00000, v167
	v_max_f32_e32 v168, 0xc3e00000, v168
	v_max_f32_e32 v169, 0xc3e00000, v169
	v_max_f32_e32 v170, 0xc3e00000, v170
	v_max_f32_e32 v171, 0xc3e00000, v171
	v_min_f32_e32 v164, 0x43e00000, v164
	v_min_f32_e32 v165, 0x43e00000, v165
	v_min_f32_e32 v166, 0x43e00000, v166
	v_min_f32_e32 v167, 0x43e00000, v167
	v_min_f32_e32 v168, 0x43e00000, v168
	v_min_f32_e32 v169, 0x43e00000, v169
	v_min_f32_e32 v170, 0x43e00000, v170
	v_min_f32_e32 v171, 0x43e00000, v171
	v_cndmask_b32_e32 v164, 0, v164, vcc
	v_cndmask_b32_e32 v165, 0, v165, vcc
	v_cndmask_b32_e32 v166, 0, v166, vcc
	v_cndmask_b32_e32 v167, 0, v167, vcc
	v_cndmask_b32_e32 v168, 0, v168, vcc
	v_cndmask_b32_e32 v169, 0, v169, vcc
	v_cndmask_b32_e32 v170, 0, v170, vcc
	v_cndmask_b32_e32 v171, 0, v171, vcc
	v_mov_b32_e32 v190, 0
	v_mov_b32_e32 v191, 0
	v_cvt_pk_fp8_f32 v190, v164, v165
	v_cvt_pk_fp8_f32 v191, v168, v169
	v_add_u32_e32 v192, 0x9000, v150
	v_cvt_pk_fp8_f32 v190, v166, v167 op_sel:[0,0,1]
	v_cvt_pk_fp8_f32 v191, v170, v171 op_sel:[0,0,1]
	s_nop 1
	global_store_dwordx2 v192, v[190:191], s[12:13] sc1
	v_add_u32_e32 v162, 0xa0, v130
	v_cmp_lt_i32_e32 vcc, v162, v145
	s_waitcnt vmcnt(7)
	v_mul_f32_e32 v163, 0x3c800000, v160
	v_mul_f32_e32 v164, 0xbd38aa3b, v28
	v_mul_f32_e32 v165, 0xbd38aa3b, v29
	v_mul_f32_e32 v166, 0xbd38aa3b, v30
	v_mul_f32_e32 v167, 0xbd38aa3b, v31
	v_mul_f32_e32 v168, 0xbd38aa3b, v20
	v_mul_f32_e32 v169, 0xbd38aa3b, v21
	v_mul_f32_e32 v170, 0xbd38aa3b, v22
	v_mul_f32_e32 v171, 0xbd38aa3b, v23
	v_exp_f32_e32 v164, v164
	v_exp_f32_e32 v165, v165
	v_exp_f32_e32 v166, v166
	v_exp_f32_e32 v167, v167
	v_exp_f32_e32 v168, v168
	v_exp_f32_e32 v169, v169
	v_exp_f32_e32 v170, v170
	v_exp_f32_e32 v171, v171
	v_add_f32_e32 v164, 1.0, v164
	v_add_f32_e32 v165, 1.0, v165
	v_add_f32_e32 v166, 1.0, v166
	v_add_f32_e32 v167, 1.0, v167
	v_add_f32_e32 v168, 1.0, v168
	v_add_f32_e32 v169, 1.0, v169
	v_add_f32_e32 v170, 1.0, v170
	v_add_f32_e32 v171, 1.0, v171
	v_rcp_f32_e32 v164, v164
	v_rcp_f32_e32 v165, v165
	v_rcp_f32_e32 v166, v166
	v_rcp_f32_e32 v167, v167
	v_rcp_f32_e32 v168, v168
	v_rcp_f32_e32 v169, v169
	v_rcp_f32_e32 v170, v170
	v_rcp_f32_e32 v171, v171
	v_mul_f32_e32 v164, v28, v164
	v_mul_f32_e32 v165, v29, v165
	v_mul_f32_e32 v166, v30, v166
	v_mul_f32_e32 v167, v31, v167
	v_mul_f32_e32 v168, v20, v168
	v_mul_f32_e32 v169, v21, v169
	v_mul_f32_e32 v170, v22, v170
	v_mul_f32_e32 v171, v23, v171
	v_mul_f32_e32 v164, v164, v24
	v_mul_f32_e32 v165, v165, v25
	v_mul_f32_e32 v166, v166, v26
	v_mul_f32_e32 v167, v167, v27
	v_mul_f32_e32 v168, v168, v16
	v_mul_f32_e32 v169, v169, v17
	v_mul_f32_e32 v170, v170, v18
	v_mul_f32_e32 v171, v171, v19
	v_mul_f32_e32 v164, v164, v163
	v_mul_f32_e32 v165, v165, v163
	v_mul_f32_e32 v166, v166, v163
	v_mul_f32_e32 v167, v167, v163
	v_mul_f32_e32 v168, v168, v163
	v_mul_f32_e32 v169, v169, v163
	v_mul_f32_e32 v170, v170, v163
	v_mul_f32_e32 v171, v171, v163
	v_max_f32_e32 v164, 0xc3e00000, v164
	v_max_f32_e32 v165, 0xc3e00000, v165
	v_max_f32_e32 v166, 0xc3e00000, v166
	v_max_f32_e32 v167, 0xc3e00000, v167
	v_max_f32_e32 v168, 0xc3e00000, v168
	v_max_f32_e32 v169, 0xc3e00000, v169
	v_max_f32_e32 v170, 0xc3e00000, v170
	v_max_f32_e32 v171, 0xc3e00000, v171
	v_min_f32_e32 v164, 0x43e00000, v164
	v_min_f32_e32 v165, 0x43e00000, v165
	v_min_f32_e32 v166, 0x43e00000, v166
	v_min_f32_e32 v167, 0x43e00000, v167
	v_min_f32_e32 v168, 0x43e00000, v168
	v_min_f32_e32 v169, 0x43e00000, v169
	v_min_f32_e32 v170, 0x43e00000, v170
	v_min_f32_e32 v171, 0x43e00000, v171
	v_cndmask_b32_e32 v164, 0, v164, vcc
	v_cndmask_b32_e32 v165, 0, v165, vcc
	v_cndmask_b32_e32 v166, 0, v166, vcc
	v_cndmask_b32_e32 v167, 0, v167, vcc
	v_cndmask_b32_e32 v168, 0, v168, vcc
	v_cndmask_b32_e32 v169, 0, v169, vcc
	v_cndmask_b32_e32 v170, 0, v170, vcc
	v_cndmask_b32_e32 v171, 0, v171, vcc
	v_mov_b32_e32 v188, 0
	v_mov_b32_e32 v189, 0
	v_cvt_pk_fp8_f32 v188, v164, v165
	v_cvt_pk_fp8_f32 v189, v168, v169
	v_add_u32_e32 v192, 0xa000, v150
	v_cvt_pk_fp8_f32 v188, v166, v167 op_sel:[0,0,1]
	v_cvt_pk_fp8_f32 v189, v170, v171 op_sel:[0,0,1]
	s_nop 1
	global_store_dwordx2 v192, v[188:189], s[12:13] sc1
	v_add_u32_e32 v162, 0xb0, v130
	v_cmp_lt_i32_e32 vcc, v162, v145
	s_waitcnt vmcnt(7)
	v_mul_f32_e32 v163, 0x3c800000, v161
	v_mul_f32_e32 v164, 0xbd38aa3b, v12
	v_mul_f32_e32 v165, 0xbd38aa3b, v13
	v_mul_f32_e32 v166, 0xbd38aa3b, v14
	v_mul_f32_e32 v167, 0xbd38aa3b, v15
	v_mul_f32_e32 v168, 0xbd38aa3b, v4
	v_mul_f32_e32 v169, 0xbd38aa3b, v5
	v_mul_f32_e32 v170, 0xbd38aa3b, v6
	v_mul_f32_e32 v171, 0xbd38aa3b, v7
	v_exp_f32_e32 v164, v164
	v_exp_f32_e32 v165, v165
	v_exp_f32_e32 v166, v166
	v_exp_f32_e32 v167, v167
	v_exp_f32_e32 v168, v168
	v_exp_f32_e32 v169, v169
	v_exp_f32_e32 v170, v170
	v_exp_f32_e32 v171, v171
	v_add_f32_e32 v164, 1.0, v164
	v_add_f32_e32 v165, 1.0, v165
	v_add_f32_e32 v166, 1.0, v166
	v_add_f32_e32 v167, 1.0, v167
	v_add_f32_e32 v168, 1.0, v168
	v_add_f32_e32 v169, 1.0, v169
	v_add_f32_e32 v170, 1.0, v170
	v_add_f32_e32 v171, 1.0, v171
	v_rcp_f32_e32 v164, v164
	v_rcp_f32_e32 v165, v165
	v_rcp_f32_e32 v166, v166
	v_rcp_f32_e32 v167, v167
	v_rcp_f32_e32 v168, v168
	v_rcp_f32_e32 v169, v169
	v_rcp_f32_e32 v170, v170
	v_rcp_f32_e32 v171, v171
	v_mul_f32_e32 v164, v12, v164
	v_mul_f32_e32 v165, v13, v165
	v_mul_f32_e32 v166, v14, v166
	v_mul_f32_e32 v167, v15, v167
	v_mul_f32_e32 v168, v4, v168
	v_mul_f32_e32 v169, v5, v169
	v_mul_f32_e32 v170, v6, v170
	v_mul_f32_e32 v171, v7, v171
	v_mul_f32_e32 v164, v164, v8
	v_mul_f32_e32 v165, v165, v9
	v_mul_f32_e32 v166, v166, v10
	v_mul_f32_e32 v167, v167, v11
	v_mul_f32_e32 v168, v168, v0
	v_mul_f32_e32 v169, v169, v1
	v_mul_f32_e32 v170, v170, v2
	v_mul_f32_e32 v171, v171, v3
	v_mul_f32_e32 v164, v164, v163
	v_mul_f32_e32 v165, v165, v163
	v_mul_f32_e32 v166, v166, v163
	v_mul_f32_e32 v167, v167, v163
	v_mul_f32_e32 v168, v168, v163
	v_mul_f32_e32 v169, v169, v163
	v_mul_f32_e32 v170, v170, v163
	v_mul_f32_e32 v171, v171, v163
	v_max_f32_e32 v164, 0xc3e00000, v164
	v_max_f32_e32 v165, 0xc3e00000, v165
	v_max_f32_e32 v166, 0xc3e00000, v166
	v_max_f32_e32 v167, 0xc3e00000, v167
	v_max_f32_e32 v168, 0xc3e00000, v168
	v_max_f32_e32 v169, 0xc3e00000, v169
	v_max_f32_e32 v170, 0xc3e00000, v170
	v_max_f32_e32 v171, 0xc3e00000, v171
	v_min_f32_e32 v164, 0x43e00000, v164
	v_min_f32_e32 v165, 0x43e00000, v165
	v_min_f32_e32 v166, 0x43e00000, v166
	v_min_f32_e32 v167, 0x43e00000, v167
	v_min_f32_e32 v168, 0x43e00000, v168
	v_min_f32_e32 v169, 0x43e00000, v169
	v_min_f32_e32 v170, 0x43e00000, v170
	v_min_f32_e32 v171, 0x43e00000, v171
	v_cndmask_b32_e32 v164, 0, v164, vcc
	v_cndmask_b32_e32 v165, 0, v165, vcc
	v_cndmask_b32_e32 v166, 0, v166, vcc
	v_cndmask_b32_e32 v167, 0, v167, vcc
	v_cndmask_b32_e32 v168, 0, v168, vcc
	v_cndmask_b32_e32 v169, 0, v169, vcc
	v_cndmask_b32_e32 v170, 0, v170, vcc
	v_cndmask_b32_e32 v171, 0, v171, vcc
	v_mov_b32_e32 v190, 0
	v_mov_b32_e32 v191, 0
	v_cvt_pk_fp8_f32 v190, v164, v165
	v_cvt_pk_fp8_f32 v191, v168, v169
	v_add_u32_e32 v192, 0xb000, v150
	v_cvt_pk_fp8_f32 v190, v166, v167 op_sel:[0,0,1]
	v_cvt_pk_fp8_f32 v191, v170, v171 op_sel:[0,0,1]
	s_nop 1
	global_store_dwordx2 v192, v[190:191], s[12:13] sc1
	v_bfe_u32 v114, v146, 4, 2
	s_waitcnt vmcnt(0)
	v_or_b32_e32 v0, v114, v143
	v_cmp_eq_u32_e32 vcc, 0, v0
	s_and_saveexec_b64 s[22:23], vcc
	s_cbranch_execz .LBB0_1274
	s_mov_b64 s[24:25], exec
	v_mbcnt_lo_u32_b32 v0, s24, 0
	v_mbcnt_hi_u32_b32 v0, s25, v0
	v_cmp_eq_u32_e32 vcc, 0, v0
	s_and_b64 s[26:27], exec, vcc
	s_mov_b64 exec, s[26:27]
	s_cbranch_execz .LBB0_1274
	s_lshl_b32 s26, s34, 5
	s_ashr_i32 s27, s26, 31
	s_lshl_b64 s[26:27], s[26:27], 2
	s_add_u32 s26, s29, s26
	s_addc_u32 s27, s50, s27
	s_bcnt1_i32_b64 s14, s[24:25]
	s_lshl_b32 s14, s14, 1
	v_mov_b32_e32 v0, s14
	global_atomic_add v140, v0, s[26:27]

.LBB0_1289:
	s_getpc_b64 s[100:101]
	global_load_dword a0, v250, s[100:101]
	s_lshl_b32 s0, s18, 2
	s_add_i32 s0, s3, s0
	v_mbcnt_lo_u32_b32 v72, -1, 0
	v_mbcnt_hi_u32_b32 v72, -1, v72
	v_mov_b32_e32 v64, s0
	ds_read2_b32 v[64:65], v64 offset0:64 offset1:224
	s_lshl_b32 s0, s20, 7
	v_and_b32_e32 v70, 15, v72
	s_add_i32 s0, s0, s24
	v_or_b32_e32 v71, s0, v70
	s_waitcnt lgkmcnt(0)
	v_ashrrev_i32_e32 v67, 31, v64
	v_mov_b32_e32 v66, v64
	v_lshlrev_b32_e32 v64, 2, v64
	v_add_u32_e32 v64, s3, v64
	ds_read_b32 v64, v64 offset:4
	v_lshlrev_b64 v[68:69], 16, v[66:67]
	v_add_u32_e32 v66, v65, v71
	v_mov_b32_e32 v73, 0
	v_lshl_add_u64 v[68:69], s[10:11], 0, v[68:69]
	s_waitcnt lgkmcnt(0)
	v_cmp_lt_i32_e32 vcc, v66, v64
	v_ashrrev_i32_e32 v67, 31, v66
	v_mov_b32_e32 v74, 0
	v_bfe_u32 v140, v72, 4, 2
	s_lshl_b32 s0, s19, 7
	v_lshl_add_u64 v[144:145], v[66:67], 2, v[68:69]
	v_lshl_or_b32 v141, v140, 3, s0
	global_load_dword v146, v[144:145], off
	global_load_dword v147, v[144:145], off offset:64
	global_load_dword v148, v[144:145], off offset:128
	global_load_dword v149, v[144:145], off offset:192
	s_lshl_b32 s4, s18, 8
	v_or_b32_e32 v141, s21, v141
	v_add_u32_e32 v142, s4, v71
	v_lshl_add_u32 v142, v142, 8, v141
	v_cmp_lt_i32_e32 vcc, v66, v64
	s_waitcnt vmcnt(3)
	v_mul_f32_e32 v155, 0x3c800000, v146
	v_mul_f32_e32 v156, 0xbd38aa3b, v60
	v_mul_f32_e32 v157, 0xbd38aa3b, v61
	v_mul_f32_e32 v158, 0xbd38aa3b, v62
	v_mul_f32_e32 v159, 0xbd38aa3b, v63
	v_mul_f32_e32 v160, 0xbd38aa3b, v52
	v_mul_f32_e32 v161, 0xbd38aa3b, v53
	v_mul_f32_e32 v162, 0xbd38aa3b, v54
	v_mul_f32_e32 v163, 0xbd38aa3b, v55
	v_exp_f32_e32 v156, v156
	v_exp_f32_e32 v157, v157
	v_exp_f32_e32 v158, v158
	v_exp_f32_e32 v159, v159
	v_exp_f32_e32 v160, v160
	v_exp_f32_e32 v161, v161
	v_exp_f32_e32 v162, v162
	v_exp_f32_e32 v163, v163
	v_add_f32_e32 v156, 1.0, v156
	v_add_f32_e32 v157, 1.0, v157
	v_add_f32_e32 v158, 1.0, v158
	v_add_f32_e32 v159, 1.0, v159
	v_add_f32_e32 v160, 1.0, v160
	v_add_f32_e32 v161, 1.0, v161
	v_add_f32_e32 v162, 1.0, v162
	v_add_f32_e32 v163, 1.0, v163
	v_rcp_f32_e32 v156, v156
	v_rcp_f32_e32 v157, v157
	v_rcp_f32_e32 v158, v158
	v_rcp_f32_e32 v159, v159
	v_rcp_f32_e32 v160, v160
	v_rcp_f32_e32 v161, v161
	v_rcp_f32_e32 v162, v162
	v_rcp_f32_e32 v163, v163
	v_mul_f32_e32 v156, v60, v156
	v_mul_f32_e32 v157, v61, v157
	v_mul_f32_e32 v158, v62, v158
	v_mul_f32_e32 v159, v63, v159
	v_mul_f32_e32 v160, v52, v160
	v_mul_f32_e32 v161, v53, v161
	v_mul_f32_e32 v162, v54, v162
	v_mul_f32_e32 v163, v55, v163
	v_mul_f32_e32 v156, v156, v56
	v_mul_f32_e32 v157, v157, v57
	v_mul_f32_e32 v158, v158, v58
	v_mul_f32_e32 v159, v159, v59
	v_mul_f32_e32 v160, v160, v48
	v_mul_f32_e32 v161, v161, v49
	v_mul_f32_e32 v162, v162, v50
	v_mul_f32_e32 v163, v163, v51
	v_mul_f32_e32 v156, v156, v155
	v_mul_f32_e32 v157, v157, v155
	v_mul_f32_e32 v158, v158, v155
	v_mul_f32_e32 v159, v159, v155
	v_mul_f32_e32 v160, v160, v155
	v_mul_f32_e32 v161, v161, v155
	v_mul_f32_e32 v162, v162, v155
	v_mul_f32_e32 v163, v163, v155
	v_max_f32_e32 v156, 0xc3e00000, v156
	v_max_f32_e32 v157, 0xc3e00000, v157
	v_max_f32_e32 v158, 0xc3e00000, v158
	v_max_f32_e32 v159, 0xc3e00000, v159
	v_max_f32_e32 v160, 0xc3e00000, v160
	v_max_f32_e32 v161, 0xc3e00000, v161
	v_max_f32_e32 v162, 0xc3e00000, v162
	v_max_f32_e32 v163, 0xc3e00000, v163
	v_min_f32_e32 v156, 0x43e00000, v156
	v_min_f32_e32 v157, 0x43e00000, v157
	v_min_f32_e32 v158, 0x43e00000, v158
	v_min_f32_e32 v159, 0x43e00000, v159
	v_min_f32_e32 v160, 0x43e00000, v160
	v_min_f32_e32 v161, 0x43e00000, v161
	v_min_f32_e32 v162, 0x43e00000, v162
	v_min_f32_e32 v163, 0x43e00000, v163
	v_cndmask_b32_e32 v156, 0, v156, vcc
	v_cndmask_b32_e32 v157, 0, v157, vcc
	v_cndmask_b32_e32 v158, 0, v158, vcc
	v_cndmask_b32_e32 v159, 0, v159, vcc
	v_cndmask_b32_e32 v160, 0, v160, vcc
	v_cndmask_b32_e32 v161, 0, v161, vcc
	v_cndmask_b32_e32 v162, 0, v162, vcc
	v_cndmask_b32_e32 v163, 0, v163, vcc
	v_mov_b32_e32 v180, 0
	v_mov_b32_e32 v181, 0
	v_cvt_pk_fp8_f32 v180, v156, v157
	v_cvt_pk_fp8_f32 v181, v160, v161
	v_mov_b32_e32 v184, v142
	v_cvt_pk_fp8_f32 v180, v158, v159 op_sel:[0,0,1]
	v_cvt_pk_fp8_f32 v181, v162, v163 op_sel:[0,0,1]
	s_nop 1
	global_store_dwordx2 v184, v[180:181], s[12:13] sc1
	v_add_u32_e32 v154, 0x10, v66
	v_cmp_lt_i32_e32 vcc, v154, v64
	s_waitcnt vmcnt(3)
	v_mul_f32_e32 v155, 0x3c800000, v147
	v_mul_f32_e32 v156, 0xbd38aa3b, v44
	v_mul_f32_e32 v157, 0xbd38aa3b, v45
	v_mul_f32_e32 v158, 0xbd38aa3b, v46
	v_mul_f32_e32 v159, 0xbd38aa3b, v47
	v_mul_f32_e32 v160, 0xbd38aa3b, v36
	v_mul_f32_e32 v161, 0xbd38aa3b, v37
	v_mul_f32_e32 v162, 0xbd38aa3b, v38
	v_mul_f32_e32 v163, 0xbd38aa3b, v39
	v_exp_f32_e32 v156, v156
	v_exp_f32_e32 v157, v157
	v_exp_f32_e32 v158, v158
	v_exp_f32_e32 v159, v159
	v_exp_f32_e32 v160, v160
	v_exp_f32_e32 v161, v161
	v_exp_f32_e32 v162, v162
	v_exp_f32_e32 v163, v163
	v_add_f32_e32 v156, 1.0, v156
	v_add_f32_e32 v157, 1.0, v157
	v_add_f32_e32 v158, 1.0, v158
	v_add_f32_e32 v159, 1.0, v159
	v_add_f32_e32 v160, 1.0, v160
	v_add_f32_e32 v161, 1.0, v161
	v_add_f32_e32 v162, 1.0, v162
	v_add_f32_e32 v163, 1.0, v163
	v_rcp_f32_e32 v156, v156
	v_rcp_f32_e32 v157, v157
	v_rcp_f32_e32 v158, v158
	v_rcp_f32_e32 v159, v159
	v_rcp_f32_e32 v160, v160
	v_rcp_f32_e32 v161, v161
	v_rcp_f32_e32 v162, v162
	v_rcp_f32_e32 v163, v163
	v_mul_f32_e32 v156, v44, v156
	v_mul_f32_e32 v157, v45, v157
	v_mul_f32_e32 v158, v46, v158
	v_mul_f32_e32 v159, v47, v159
	v_mul_f32_e32 v160, v36, v160
	v_mul_f32_e32 v161, v37, v161
	v_mul_f32_e32 v162, v38, v162
	v_mul_f32_e32 v163, v39, v163
	v_mul_f32_e32 v156, v156, v40
	v_mul_f32_e32 v157, v157, v41
	v_mul_f32_e32 v158, v158, v42
	v_mul_f32_e32 v159, v159, v43
	v_mul_f32_e32 v160, v160, v32
	v_mul_f32_e32 v161, v161, v33
	v_mul_f32_e32 v162, v162, v34
	v_mul_f32_e32 v163, v163, v35
	v_mul_f32_e32 v156, v156, v155
	v_mul_f32_e32 v157, v157, v155
	v_mul_f32_e32 v158, v158, v155
	v_mul_f32_e32 v159, v159, v155
	v_mul_f32_e32 v160, v160, v155
	v_mul_f32_e32 v161, v161, v155
	v_mul_f32_e32 v162, v162, v155
	v_mul_f32_e32 v163, v163, v155
	v_max_f32_e32 v156, 0xc3e00000, v156
	v_max_f32_e32 v157, 0xc3e00000, v157
	v_max_f32_e32 v158, 0xc3e00000, v158
	v_max_f32_e32 v159, 0xc3e00000, v159
	v_max_f32_e32 v160, 0xc3e00000, v160
	v_max_f32_e32 v161, 0xc3e00000, v161
	v_max_f32_e32 v162, 0xc3e00000, v162
	v_max_f32_e32 v163, 0xc3e00000, v163
	v_min_f32_e32 v156, 0x43e00000, v156
	v_min_f32_e32 v157, 0x43e00000, v157
	v_min_f32_e32 v158, 0x43e00000, v158
	v_min_f32_e32 v159, 0x43e00000, v159
	v_min_f32_e32 v160, 0x43e00000, v160
	v_min_f32_e32 v161, 0x43e00000, v161
	v_min_f32_e32 v162, 0x43e00000, v162
	v_min_f32_e32 v163, 0x43e00000, v163
	v_cndmask_b32_e32 v156, 0, v156, vcc
	v_cndmask_b32_e32 v157, 0, v157, vcc
	v_cndmask_b32_e32 v158, 0, v158, vcc
	v_cndmask_b32_e32 v159, 0, v159, vcc
	v_cndmask_b32_e32 v160, 0, v160, vcc
	v_cndmask_b32_e32 v161, 0, v161, vcc
	v_cndmask_b32_e32 v162, 0, v162, vcc
	v_cndmask_b32_e32 v163, 0, v163, vcc
	v_mov_b32_e32 v182, 0
	v_mov_b32_e32 v183, 0
	v_cvt_pk_fp8_f32 v182, v156, v157
	v_cvt_pk_fp8_f32 v183, v160, v161
	v_add_u32_e32 v184, 0x1000, v142
	v_cvt_pk_fp8_f32 v182, v158, v159 op_sel:[0,0,1]
	v_cvt_pk_fp8_f32 v183, v162, v163 op_sel:[0,0,1]
	s_nop 1
	global_store_dwordx2 v184, v[182:183], s[12:13] sc1
	v_add_u32_e32 v154, 0x20, v66
	v_cmp_lt_i32_e32 vcc, v154, v64
	s_waitcnt vmcnt(3)
	v_mul_f32_e32 v155, 0x3c800000, v148
	v_mul_f32_e32 v156, 0xbd38aa3b, v28
	v_mul_f32_e32 v157, 0xbd38aa3b, v29
	v_mul_f32_e32 v158, 0xbd38aa3b, v30
	v_mul_f32_e32 v159, 0xbd38aa3b, v31
	v_mul_f32_e32 v160, 0xbd38aa3b, v20
	v_mul_f32_e32 v161, 0xbd38aa3b, v21
	v_mul_f32_e32 v162, 0xbd38aa3b, v22
	v_mul_f32_e32 v163, 0xbd38aa3b, v23
	v_exp_f32_e32 v156, v156
	v_exp_f32_e32 v157, v157
	v_exp_f32_e32 v158, v158
	v_exp_f32_e32 v159, v159
	v_exp_f32_e32 v160, v160
	v_exp_f32_e32 v161, v161
	v_exp_f32_e32 v162, v162
	v_exp_f32_e32 v163, v163
	v_add_f32_e32 v156, 1.0, v156
	v_add_f32_e32 v157, 1.0, v157
	v_add_f32_e32 v158, 1.0, v158
	v_add_f32_e32 v159, 1.0, v159
	v_add_f32_e32 v160, 1.0, v160
	v_add_f32_e32 v161, 1.0, v161
	v_add_f32_e32 v162, 1.0, v162
	v_add_f32_e32 v163, 1.0, v163
	v_rcp_f32_e32 v156, v156
	v_rcp_f32_e32 v157, v157
	v_rcp_f32_e32 v158, v158
	v_rcp_f32_e32 v159, v159
	v_rcp_f32_e32 v160, v160
	v_rcp_f32_e32 v161, v161
	v_rcp_f32_e32 v162, v162
	v_rcp_f32_e32 v163, v163
	v_mul_f32_e32 v156, v28, v156
	v_mul_f32_e32 v157, v29, v157
	v_mul_f32_e32 v158, v30, v158
	v_mul_f32_e32 v159, v31, v159
	v_mul_f32_e32 v160, v20, v160
	v_mul_f32_e32 v161, v21, v161
	v_mul_f32_e32 v162, v22, v162
	v_mul_f32_e32 v163, v23, v163
	v_mul_f32_e32 v156, v156, v24
	v_mul_f32_e32 v157, v157, v25
	v_mul_f32_e32 v158, v158, v26
	v_mul_f32_e32 v159, v159, v27
	v_mul_f32_e32 v160, v160, v16
	v_mul_f32_e32 v161, v161, v17
	v_mul_f32_e32 v162, v162, v18
	v_mul_f32_e32 v163, v163, v19
	v_mul_f32_e32 v156, v156, v155
	v_mul_f32_e32 v157, v157, v155
	v_mul_f32_e32 v158, v158, v155
	v_mul_f32_e32 v159, v159, v155
	v_mul_f32_e32 v160, v160, v155
	v_mul_f32_e32 v161, v161, v155
	v_mul_f32_e32 v162, v162, v155
	v_mul_f32_e32 v163, v163, v155
	v_max_f32_e32 v156, 0xc3e00000, v156
	v_max_f32_e32 v157, 0xc3e00000, v157
	v_max_f32_e32 v158, 0xc3e00000, v158
	v_max_f32_e32 v159, 0xc3e00000, v159
	v_max_f32_e32 v160, 0xc3e00000, v160
	v_max_f32_e32 v161, 0xc3e00000, v161
	v_max_f32_e32 v162, 0xc3e00000, v162
	v_max_f32_e32 v163, 0xc3e00000, v163
	v_min_f32_e32 v156, 0x43e00000, v156
	v_min_f32_e32 v157, 0x43e00000, v157
	v_min_f32_e32 v158, 0x43e00000, v158
	v_min_f32_e32 v159, 0x43e00000, v159
	v_min_f32_e32 v160, 0x43e00000, v160
	v_min_f32_e32 v161, 0x43e00000, v161
	v_min_f32_e32 v162, 0x43e00000, v162
	v_min_f32_e32 v163, 0x43e00000, v163
	v_cndmask_b32_e32 v156, 0, v156, vcc
	v_cndmask_b32_e32 v157, 0, v157, vcc
	v_cndmask_b32_e32 v158, 0, v158, vcc
	v_cndmask_b32_e32 v159, 0, v159, vcc
	v_cndmask_b32_e32 v160, 0, v160, vcc
	v_cndmask_b32_e32 v161, 0, v161, vcc
	v_cndmask_b32_e32 v162, 0, v162, vcc
	v_cndmask_b32_e32 v163, 0, v163, vcc
	v_mov_b32_e32 v180, 0
	v_mov_b32_e32 v181, 0
	v_cvt_pk_fp8_f32 v180, v156, v157
	v_cvt_pk_fp8_f32 v181, v160, v161
	v_add_u32_e32 v184, 0x2000, v142
	v_cvt_pk_fp8_f32 v180, v158, v159 op_sel:[0,0,1]
	v_cvt_pk_fp8_f32 v181, v162, v163 op_sel:[0,0,1]
	s_nop 1
	global_store_dwordx2 v184, v[180:181], s[12:13] sc1
	v_add_u32_e32 v154, 0x30, v66
	v_cmp_lt_i32_e32 vcc, v154, v64
	s_waitcnt vmcnt(3)
	v_mul_f32_e32 v155, 0x3c800000, v149
	v_mul_f32_e32 v156, 0xbd38aa3b, v12
	v_mul_f32_e32 v157, 0xbd38aa3b, v13
	v_mul_f32_e32 v158, 0xbd38aa3b, v14
	v_mul_f32_e32 v159, 0xbd38aa3b, v15
	v_mul_f32_e32 v160, 0xbd38aa3b, v4
	v_mul_f32_e32 v161, 0xbd38aa3b, v5
	v_mul_f32_e32 v162, 0xbd38aa3b, v6
	v_mul_f32_e32 v163, 0xbd38aa3b, v7
	v_exp_f32_e32 v156, v156
	v_exp_f32_e32 v157, v157
	v_exp_f32_e32 v158, v158
	v_exp_f32_e32 v159, v159
	v_exp_f32_e32 v160, v160
	v_exp_f32_e32 v161, v161
	v_exp_f32_e32 v162, v162
	v_exp_f32_e32 v163, v163
	v_add_f32_e32 v156, 1.0, v156
	v_add_f32_e32 v157, 1.0, v157
	v_add_f32_e32 v158, 1.0, v158
	v_add_f32_e32 v159, 1.0, v159
	v_add_f32_e32 v160, 1.0, v160
	v_add_f32_e32 v161, 1.0, v161
	v_add_f32_e32 v162, 1.0, v162
	v_add_f32_e32 v163, 1.0, v163
	v_rcp_f32_e32 v156, v156
	v_rcp_f32_e32 v157, v157
	v_rcp_f32_e32 v158, v158
	v_rcp_f32_e32 v159, v159
	v_rcp_f32_e32 v160, v160
	v_rcp_f32_e32 v161, v161
	v_rcp_f32_e32 v162, v162
	v_rcp_f32_e32 v163, v163
	v_mul_f32_e32 v156, v12, v156
	v_mul_f32_e32 v157, v13, v157
	v_mul_f32_e32 v158, v14, v158
	v_mul_f32_e32 v159, v15, v159
	v_mul_f32_e32 v160, v4, v160
	v_mul_f32_e32 v161, v5, v161
	v_mul_f32_e32 v162, v6, v162
	v_mul_f32_e32 v163, v7, v163
	v_mul_f32_e32 v156, v156, v8
	v_mul_f32_e32 v157, v157, v9
	v_mul_f32_e32 v158, v158, v10
	v_mul_f32_e32 v159, v159, v11
	v_mul_f32_e32 v160, v160, v0
	v_mul_f32_e32 v161, v161, v1
	v_mul_f32_e32 v162, v162, v2
	v_mul_f32_e32 v163, v163, v3
	v_mul_f32_e32 v156, v156, v155
	v_mul_f32_e32 v157, v157, v155
	v_mul_f32_e32 v158, v158, v155
	v_mul_f32_e32 v159, v159, v155
	v_mul_f32_e32 v160, v160, v155
	v_mul_f32_e32 v161, v161, v155
	v_mul_f32_e32 v162, v162, v155
	v_mul_f32_e32 v163, v163, v155
	v_max_f32_e32 v156, 0xc3e00000, v156
	v_max_f32_e32 v157, 0xc3e00000, v157
	v_max_f32_e32 v158, 0xc3e00000, v158
	v_max_f32_e32 v159, 0xc3e00000, v159
	v_max_f32_e32 v160, 0xc3e00000, v160
	v_max_f32_e32 v161, 0xc3e00000, v161
	v_max_f32_e32 v162, 0xc3e00000, v162
	v_max_f32_e32 v163, 0xc3e00000, v163
	v_min_f32_e32 v156, 0x43e00000, v156
	v_min_f32_e32 v157, 0x43e00000, v157
	v_min_f32_e32 v158, 0x43e00000, v158
	v_min_f32_e32 v159, 0x43e00000, v159
	v_min_f32_e32 v160, 0x43e00000, v160
	v_min_f32_e32 v161, 0x43e00000, v161
	v_min_f32_e32 v162, 0x43e00000, v162
	v_min_f32_e32 v163, 0x43e00000, v163
	v_cndmask_b32_e32 v156, 0, v156, vcc
	v_cndmask_b32_e32 v157, 0, v157, vcc
	v_cndmask_b32_e32 v158, 0, v158, vcc
	v_cndmask_b32_e32 v159, 0, v159, vcc
	v_cndmask_b32_e32 v160, 0, v160, vcc
	v_cndmask_b32_e32 v161, 0, v161, vcc
	v_cndmask_b32_e32 v162, 0, v162, vcc
	v_cndmask_b32_e32 v163, 0, v163, vcc
	v_mov_b32_e32 v182, 0
	v_mov_b32_e32 v183, 0
	v_cvt_pk_fp8_f32 v182, v156, v157
	v_cvt_pk_fp8_f32 v183, v160, v161
	v_add_u32_e32 v184, 0x3000, v142
	v_cvt_pk_fp8_f32 v182, v158, v159 op_sel:[0,0,1]
	v_cvt_pk_fp8_f32 v183, v162, v163 op_sel:[0,0,1]
	s_nop 1
	global_store_dwordx2 v184, v[182:183], s[12:13] sc1
	v_bfe_u32 v50, v72, 4, 2
	s_waitcnt vmcnt(0)
	v_or_b32_e32 v0, v50, v70
	v_cmp_eq_u32_e32 vcc, 0, v0
	s_and_saveexec_b64 s[0:1], vcc
	s_cbranch_execz .LBB0_1364
	s_mov_b64 s[4:5], exec
	v_mbcnt_lo_u32_b32 v0, s4, 0
	v_mbcnt_hi_u32_b32 v0, s5, v0
	v_cmp_eq_u32_e32 vcc, 0, v0
	s_and_b64 s[10:11], exec, vcc
	s_mov_b64 exec, s[10:11]
	s_cbranch_execz .LBB0_1364
	s_lshl_b32 s10, s18, 5
	s_ashr_i32 s11, s10, 31
	s_lshl_b64 s[10:11], s[10:11], 2
	s_add_u32 s10, s29, s10
	s_addc_u32 s11, s50, s11
	s_bcnt1_i32_b64 s4, s[4:5]
	v_mov_b32_e32 v0, 0
	v_mov_b32_e32 v1, s4
	global_atomic_add v0, v1, s[10:11]

.LBB0_1381:
	s_getpc_b64 s[100:101]
	global_load_dword a0, v250, s[100:101]
	v_bfe_i32 v3, v0, 27, 1
	v_lshlrev_b32_e32 v1, 4, v0
	v_lshrrev_b32_e32 v3, 22, v3
	v_add_u32_e32 v3, v1, v3
	v_and_b32_e32 v3, 0xfffffc00, v3
	v_ashrrev_i32_e32 v2, 31, v0
	v_sub_u32_e32 v1, v1, v3
	v_lshrrev_b32_e32 v2, 26, v2
	v_lshrrev_b32_e32 v3, 4, v1
	v_add_u32_e32 v2, v0, v2
	v_bitop3_b32 v3, v3, v1, 32 bitop3:0x6c
	v_ashrrev_i32_e32 v1, 31, v1
	v_ashrrev_i32_e32 v2, 6, v2
	v_lshrrev_b32_e32 v1, 26, v1
	v_lshlrev_b32_e32 v4, 3, v2
	v_add_u32_e32 v1, v3, v1
	s_add_u32 s14, s78, 0x6500000
	v_and_b32_e32 v4, -16, v4
	v_ashrrev_i32_e32 v1, 6, v1
	v_lshlrev_b32_e32 v2, 5, v2
	s_addc_u32 s15, s79, 0
	s_ashr_i32 s4, s21, 6
	v_add_u32_e32 v4, v1, v4
	v_and_b32_e32 v5, 32, v2
	v_mul_i32_i24_e32 v2, 64, v1
	v_and_b32_e32 v1, 3, v1
	s_mov_b32 s16, 0xffffe0
	s_ashr_i32 s41, s40, 31
	s_ashr_i32 s5, s21, 8
	v_and_or_b32 v1, v4, s16, v1
	s_lshl_b32 s51, s4, 10
	s_lshl_b64 s[16:17], s[40:41], 16
	v_sub_u32_e32 v2, v3, v2
	v_mov_b32_e32 v3, 1
	s_add_u32 s42, s12, s16
	v_ashrrev_i16_sdwa v2, v3, sext(v2) dst_sel:DWORD dst_unused:UNUSED_PAD src0_sel:DWORD src1_sel:BYTE_0
	s_addc_u32 s43, s13, s17
	s_lshl_b32 s16, s40, 2
	v_bfe_i32 v3, v2, 0, 16
	v_lshlrev_b32_e32 v2, 1, v4
	s_add_i32 s16, s16, 0
	v_and_b32_e32 v6, 24, v2
	v_lshrrev_b32_e32 v2, 2, v4
	s_add_i32 s16, s16, 0x24100
	v_and_b32_e32 v7, 4, v2
	s_barrier
	v_mov_b32_e32 v2, s16
	ds_read_b32 v2, v2
	v_or3_b32 v1, v1, v7, v6
	v_add_lshl_u32 v3, v5, v3, 1
	v_lshl_add_u32 v194, v1, 8, v3
	v_lshl_add_u32 v195, v4, 8, v3
	s_waitcnt lgkmcnt(0)
	v_ashrrev_i32_e32 v3, 31, v2
	v_lshlrev_b64 v[2:3], 18, v[2:3]
	s_ashr_i32 s39, s38, 31
	v_lshl_add_u64 v[2:3], s[14:15], 0, v[2:3]
	s_lshl_b64 s[16:17], s[38:39], 16
	v_lshl_add_u64 v[2:3], v[2:3], 0, s[16:17]
	s_add_i32 s52, s51, 0
	v_readfirstlane_b32 s17, v3
	v_readfirstlane_b32 s16, v2
	s_mov_b64 s[18:19], s[16:17]
	s_add_i32 m0, s52, 0x10000
	s_mov_b32 s64, 0
	global_load_lds_dwordx4 v194, s[18:19]
	s_add_u32 s18, s16, 0x4000
	s_addc_u32 s19, s17, 0
	s_add_i32 m0, s52, 0x12000
	s_nop 0
	global_load_lds_dwordx4 v194, s[18:19]
	s_add_i32 m0, s52, 0x14000
	s_add_u32 s18, s16, 0x8000
	s_addc_u32 s19, s17, 0
	s_nop 0
	global_load_lds_dwordx4 v194, s[18:19]
	s_add_u32 s18, s16, 0xc000
	s_addc_u32 s19, s17, 0
	s_add_i32 m0, s52, 0x16000
	s_nop 0
	global_load_lds_dwordx4 v194, s[18:19]
	v_mov_b32_e32 v1, v195
	s_mov_b64 s[18:19], s[42:43]
	s_mov_b32 m0, s52
	s_nop 0
	global_load_lds_dwordx4 v1, s[18:19] sc1
	s_add_u32 s18, s42, 0x4000
	v_mov_b32_e32 v1, v195
	s_addc_u32 s19, s43, 0
	s_add_i32 s53, s52, 0x2000
	s_mov_b32 m0, s53
	s_add_i32 s60, s52, 0x4000
	global_load_lds_dwordx4 v1, s[18:19] sc1
	s_add_u32 s18, s42, 0x8000
	v_mov_b32_e32 v1, v195
	s_addc_u32 s19, s43, 0
	s_mov_b32 m0, s60
	s_nop 0
	global_load_lds_dwordx4 v1, s[18:19] sc1
	s_add_u32 s18, s42, 0xc000
	s_addc_u32 s19, s43, 0
	s_add_i32 s61, s52, 0x6000
	v_mov_b32_e32 v1, v195
	s_mov_b32 m0, s61
	s_cmp_eq_u32 s5, 1
	global_load_lds_dwordx4 v1, s[18:19] sc1
	s_cselect_b64 s[18:19], -1, 0
	s_cmp_lg_u32 s5, 1
	s_cbranch_scc1 .LBB0_1383
	s_barrier

.LBB0_1401:
	s_getpc_b64 s[100:101]
	global_load_dword a0, v250, s[100:101]
	s_barrier

.LBB0_1602:
	s_getpc_b64 s[100:101]
	global_load_dword a0, v250, s[100:101]
	s_or_b64 exec, exec, s[10:11]

.LBB0_1772:
	s_getpc_b64 s[100:101]
	global_load_dword a0, v250, s[100:101]
	s_mov_b32 s5, 0
	v_mbcnt_lo_u32_b32 v147, -1, 0
	v_mbcnt_hi_u32_b32 v147, -1, v147
	s_lshl_b32 s5, s4, 8
	v_readlane_b32 s80, v249, 18
	v_bfe_u32 v58, v147, 4, 2
	v_lshlrev_b32_e32 v146, 3, v58
	v_or_b32_e32 v56, s41, v146
	v_or_b32_e32 v56, s5, v56
	v_ashrrev_i32_e32 v57, 31, v56
	v_readlane_b32 s90, v249, 28
	v_readlane_b32 s91, v249, 29
	v_cmp_eq_u32_e64 s[6:7], 0, v58
	s_add_i32 s51, s5, 0xfffff800
	v_lshl_add_u64 v[60:61], v[56:57], 2, s[90:91]
	global_load_dwordx4 v[76:79], v[60:61], off
	global_load_dwordx4 v[68:71], v[60:61], off offset:16
	global_load_dwordx4 v[56:59], v[60:61], off offset:528
	s_nop 0
	global_load_dwordx4 v[60:63], v[60:61], off offset:512
	s_cmp_gt_i32 s4, 7
	v_readlane_b32 s81, v249, 19
	v_readlane_b32 s82, v249, 20
	v_readlane_b32 s83, v249, 21
	v_readlane_b32 s84, v249, 22
	v_readlane_b32 s85, v249, 23
	v_readlane_b32 s86, v249, 24
	v_readlane_b32 s87, v249, 25
	s_cselect_b64 s[70:71], -1, 0
	s_and_b64 s[72:73], s[70:71], exec
	s_mov_b32 s53, 0x16500000
	v_readlane_b32 s80, v249, 55
	s_cselect_b32 s53, s53, 0x12500000
	v_readlane_b32 s86, v249, 61
	s_cselect_b32 s5, s51, s5
	v_readlane_b32 s87, v249, 62
	s_add_u32 s72, s86, s53
	s_addc_u32 s73, s87, 0
	s_lshl_b32 s51, s68, 8
	s_or_b32 s5, s41, s5
	s_add_i32 s51, s51, s39
	v_or_b32_e32 v146, s5, v146
	v_and_or_b32 v148, v147, 15, s51
	v_ashrrev_i32_e32 v147, 31, v146
	v_ashrrev_i32_e32 v149, 31, v148
	v_lshl_add_u64 v[146:147], v[146:147], 1, s[72:73]
	v_lshlrev_b64 v[160:161], 12, v[148:149]
	v_lshl_add_u64 v[164:165], v[146:147], 0, v[160:161]
	v_mov_b64_e32 v[150:151], s[24:25]
	s_lshl_b32 s53, s4, 2
	s_sub_i32 s68, s53, 32
	s_ashr_i32 s69, s68, 31
	s_or_b64 s[68:69], s[68:69], s[14:15]
	s_cmp_lt_i32 s4, 8
	v_readlane_b32 s88, v249, 26
	v_readlane_b32 s89, v249, 27
	v_readlane_b32 s92, v249, 30
	v_readlane_b32 s93, v249, 31
	v_readlane_b32 s94, v249, 32
	v_readlane_b32 s95, v249, 33
	v_readlane_b32 s81, v249, 56
	v_readlane_b32 s82, v249, 57
	v_readlane_b32 s83, v249, 58
	v_readlane_b32 s84, v249, 59
	v_readlane_b32 s85, v249, 60
	s_waitcnt vmcnt(0)
	v_readlane_b32 s90, v249, 63
	v_readlane_b32 s91, v248, 0
	s_mov_b64 s[94:95], s[46:47]
	v_mov_b32_e32 v192, v148
	v_ashrrev_i32_e32 v193, 31, v192
	v_lshlrev_b64 v[194:195], 12, v[192:193]
	v_lshl_add_u64 v[196:197], v[146:147], 0, v[194:195]
	v_pk_add_f32 v[140:141], v[140:141], v[76:77]
	v_pk_add_f32 v[142:143], v[142:143], v[78:79]
	v_pk_add_f32 v[136:137], v[136:137], v[68:69]
	v_pk_add_f32 v[138:139], v[138:139], v[70:71]
	v_med3_f32 v160, v140, s78, v158
	v_med3_f32 v161, v141, s78, v158
	v_med3_f32 v162, v142, s78, v158
	v_med3_f32 v163, v143, s78, v158
	v_med3_f32 v164, v136, s78, v158
	v_med3_f32 v165, v137, s78, v158
	v_med3_f32 v166, v138, s78, v158
	v_med3_f32 v167, v139, s78, v158
	v_pk_mul_f32 v[168:169], v[160:161], v[160:161]
	v_pk_mul_f32 v[170:171], v[162:163], v[162:163]
	v_pk_mul_f32 v[172:173], v[164:165], v[164:165]
	v_pk_mul_f32 v[174:175], v[166:167], v[166:167]
	v_pk_fma_f32 v[168:169], v[168:169], s[20:21], -1.0 op_sel_hi:[1,0,0]
	v_pk_fma_f32 v[170:171], v[170:171], s[20:21], -1.0 op_sel_hi:[1,0,0]
	v_pk_fma_f32 v[172:173], v[172:173], s[20:21], -1.0 op_sel_hi:[1,0,0]
	v_pk_fma_f32 v[174:175], v[174:175], s[20:21], -1.0 op_sel_hi:[1,0,0]
	v_pk_fma_f32 v[176:177], v[168:169], s[22:23], v[150:151] op_sel_hi:[1,0,0] neg_lo:[1,0,0] neg_hi:[1,0,0]
	v_pk_fma_f32 v[178:179], v[170:171], s[22:23], v[150:151] op_sel_hi:[1,0,0] neg_lo:[1,0,0] neg_hi:[1,0,0]
	v_pk_fma_f32 v[180:181], v[172:173], s[22:23], v[150:151] op_sel_hi:[1,0,0] neg_lo:[1,0,0] neg_hi:[1,0,0]
	v_pk_fma_f32 v[182:183], v[174:175], s[22:23], v[150:151] op_sel_hi:[1,0,0] neg_lo:[1,0,0] neg_hi:[1,0,0]
	v_pk_fma_f32 v[176:177], v[168:169], v[176:177], s[26:27] op_sel_hi:[1,1,0]
	v_pk_fma_f32 v[178:179], v[170:171], v[178:179], s[26:27] op_sel_hi:[1,1,0]
	v_pk_fma_f32 v[180:181], v[172:173], v[180:181], s[26:27] op_sel_hi:[1,1,0]
	v_pk_fma_f32 v[182:183], v[174:175], v[182:183], s[26:27] op_sel_hi:[1,1,0]
	v_pk_fma_f32 v[176:177], v[168:169], v[176:177], s[28:29] op_sel_hi:[1,1,0]
	v_pk_fma_f32 v[178:179], v[170:171], v[178:179], s[28:29] op_sel_hi:[1,1,0]
	v_pk_fma_f32 v[180:181], v[172:173], v[180:181], s[28:29] op_sel_hi:[1,1,0]
	v_pk_fma_f32 v[182:183], v[174:175], v[182:183], s[28:29] op_sel_hi:[1,1,0]
	v_pk_fma_f32 v[176:177], v[168:169], v[176:177], s[30:31] op_sel_hi:[1,1,0]
	v_pk_fma_f32 v[178:179], v[170:171], v[178:179], s[30:31] op_sel_hi:[1,1,0]
	v_pk_fma_f32 v[180:181], v[172:173], v[180:181], s[30:31] op_sel_hi:[1,1,0]
	v_pk_fma_f32 v[182:183], v[174:175], v[182:183], s[30:31] op_sel_hi:[1,1,0]
	v_pk_fma_f32 v[176:177], v[168:169], v[176:177], s[34:35] op_sel_hi:[1,1,0]
	v_pk_fma_f32 v[178:179], v[170:171], v[178:179], s[34:35] op_sel_hi:[1,1,0]
	v_pk_fma_f32 v[180:181], v[172:173], v[180:181], s[34:35] op_sel_hi:[1,1,0]
	v_pk_fma_f32 v[182:183], v[174:175], v[182:183], s[34:35] op_sel_hi:[1,1,0]
	v_pk_fma_f32 v[176:177], v[168:169], v[176:177], s[36:37] op_sel_hi:[1,1,0]
	v_pk_fma_f32 v[178:179], v[170:171], v[178:179], s[36:37] op_sel_hi:[1,1,0]
	v_pk_fma_f32 v[180:181], v[172:173], v[180:181], s[36:37] op_sel_hi:[1,1,0]
	v_pk_fma_f32 v[182:183], v[174:175], v[182:183], s[36:37] op_sel_hi:[1,1,0]
	v_pk_fma_f32 v[176:177], v[168:169], v[176:177], s[38:39] op_sel_hi:[1,1,0]
	v_pk_fma_f32 v[178:179], v[170:171], v[178:179], s[38:39] op_sel_hi:[1,1,0]
	v_pk_fma_f32 v[180:181], v[172:173], v[180:181], s[38:39] op_sel_hi:[1,1,0]
	v_pk_fma_f32 v[182:183], v[174:175], v[182:183], s[38:39] op_sel_hi:[1,1,0]
	v_pk_fma_f32 v[176:177], v[168:169], v[176:177], s[40:41] op_sel_hi:[1,1,0]
	v_pk_fma_f32 v[178:179], v[170:171], v[178:179], s[40:41] op_sel_hi:[1,1,0]
	v_pk_fma_f32 v[180:181], v[172:173], v[180:181], s[40:41] op_sel_hi:[1,1,0]
	v_pk_fma_f32 v[182:183], v[174:175], v[182:183], s[40:41] op_sel_hi:[1,1,0]
	v_pk_fma_f32 v[176:177], v[168:169], v[176:177], s[42:43] op_sel_hi:[1,1,0]
	v_pk_fma_f32 v[178:179], v[170:171], v[178:179], s[42:43] op_sel_hi:[1,1,0]
	v_pk_fma_f32 v[180:181], v[172:173], v[180:181], s[42:43] op_sel_hi:[1,1,0]
	v_pk_fma_f32 v[182:183], v[174:175], v[182:183], s[42:43] op_sel_hi:[1,1,0]
	v_pk_fma_f32 v[176:177], v[168:169], v[176:177], s[44:45] op_sel_hi:[1,1,0]
	v_pk_fma_f32 v[178:179], v[170:171], v[178:179], s[44:45] op_sel_hi:[1,1,0]
	v_pk_fma_f32 v[180:181], v[172:173], v[180:181], s[44:45] op_sel_hi:[1,1,0]
	v_pk_fma_f32 v[182:183], v[174:175], v[182:183], s[44:45] op_sel_hi:[1,1,0]
	v_pk_fma_f32 v[168:169], v[168:169], v[176:177], s[48:49] op_sel_hi:[1,1,0]
	v_pk_fma_f32 v[170:171], v[170:171], v[178:179], s[48:49] op_sel_hi:[1,1,0]
	v_pk_fma_f32 v[172:173], v[172:173], v[180:181], s[48:49] op_sel_hi:[1,1,0]
	v_pk_fma_f32 v[174:175], v[174:175], v[182:183], s[48:49] op_sel_hi:[1,1,0]
	v_pk_fma_f32 v[160:161], v[160:161], v[168:169], 0.5 op_sel_hi:[1,1,0]
	v_pk_fma_f32 v[162:163], v[162:163], v[170:171], 0.5 op_sel_hi:[1,1,0]
	v_pk_fma_f32 v[164:165], v[164:165], v[172:173], 0.5 op_sel_hi:[1,1,0]
	v_pk_fma_f32 v[166:167], v[166:167], v[174:175], 0.5 op_sel_hi:[1,1,0]
	v_pk_mul_f32 v[140:141], v[140:141], v[160:161]
	v_pk_mul_f32 v[142:143], v[142:143], v[162:163]
	v_pk_mul_f32 v[136:137], v[136:137], v[164:165]
	v_pk_mul_f32 v[138:139], v[138:139], v[166:167]
	v_cvt_pk_bf16_f32 v184, v140, v141
	v_cvt_pk_bf16_f32 v185, v142, v143
	v_cvt_pk_bf16_f32 v186, v136, v137
	v_cvt_pk_bf16_f32 v187, v138, v139
	global_store_dwordx4 v[196:197], v[184:187], off
	v_pk_add_f32 v[132:133], v[132:133], v[60:61]
	v_pk_add_f32 v[134:135], v[134:135], v[62:63]
	v_pk_add_f32 v[128:129], v[128:129], v[56:57]
	v_pk_add_f32 v[130:131], v[130:131], v[58:59]
	v_med3_f32 v160, v132, s78, v158
	v_med3_f32 v161, v133, s78, v158
	v_med3_f32 v162, v134, s78, v158
	v_med3_f32 v163, v135, s78, v158
	v_med3_f32 v164, v128, s78, v158
	v_med3_f32 v165, v129, s78, v158
	v_med3_f32 v166, v130, s78, v158
	v_med3_f32 v167, v131, s78, v158
	v_pk_mul_f32 v[168:169], v[160:161], v[160:161]
	v_pk_mul_f32 v[170:171], v[162:163], v[162:163]
	v_pk_mul_f32 v[172:173], v[164:165], v[164:165]
	v_pk_mul_f32 v[174:175], v[166:167], v[166:167]
	v_pk_fma_f32 v[168:169], v[168:169], s[20:21], -1.0 op_sel_hi:[1,0,0]
	v_pk_fma_f32 v[170:171], v[170:171], s[20:21], -1.0 op_sel_hi:[1,0,0]
	v_pk_fma_f32 v[172:173], v[172:173], s[20:21], -1.0 op_sel_hi:[1,0,0]
	v_pk_fma_f32 v[174:175], v[174:175], s[20:21], -1.0 op_sel_hi:[1,0,0]
	v_pk_fma_f32 v[176:177], v[168:169], s[22:23], v[150:151] op_sel_hi:[1,0,0] neg_lo:[1,0,0] neg_hi:[1,0,0]
	v_pk_fma_f32 v[178:179], v[170:171], s[22:23], v[150:151] op_sel_hi:[1,0,0] neg_lo:[1,0,0] neg_hi:[1,0,0]
	v_pk_fma_f32 v[180:181], v[172:173], s[22:23], v[150:151] op_sel_hi:[1,0,0] neg_lo:[1,0,0] neg_hi:[1,0,0]
	v_pk_fma_f32 v[182:183], v[174:175], s[22:23], v[150:151] op_sel_hi:[1,0,0] neg_lo:[1,0,0] neg_hi:[1,0,0]
	v_pk_fma_f32 v[176:177], v[168:169], v[176:177], s[26:27] op_sel_hi:[1,1,0]
	v_pk_fma_f32 v[178:179], v[170:171], v[178:179], s[26:27] op_sel_hi:[1,1,0]
	v_pk_fma_f32 v[180:181], v[172:173], v[180:181], s[26:27] op_sel_hi:[1,1,0]
	v_pk_fma_f32 v[182:183], v[174:175], v[182:183], s[26:27] op_sel_hi:[1,1,0]
	v_pk_fma_f32 v[176:177], v[168:169], v[176:177], s[28:29] op_sel_hi:[1,1,0]
	v_pk_fma_f32 v[178:179], v[170:171], v[178:179], s[28:29] op_sel_hi:[1,1,0]
	v_pk_fma_f32 v[180:181], v[172:173], v[180:181], s[28:29] op_sel_hi:[1,1,0]
	v_pk_fma_f32 v[182:183], v[174:175], v[182:183], s[28:29] op_sel_hi:[1,1,0]
	v_pk_fma_f32 v[176:177], v[168:169], v[176:177], s[30:31] op_sel_hi:[1,1,0]
	v_pk_fma_f32 v[178:179], v[170:171], v[178:179], s[30:31] op_sel_hi:[1,1,0]
	v_pk_fma_f32 v[180:181], v[172:173], v[180:181], s[30:31] op_sel_hi:[1,1,0]
	v_pk_fma_f32 v[182:183], v[174:175], v[182:183], s[30:31] op_sel_hi:[1,1,0]
	v_pk_fma_f32 v[176:177], v[168:169], v[176:177], s[34:35] op_sel_hi:[1,1,0]
	v_pk_fma_f32 v[178:179], v[170:171], v[178:179], s[34:35] op_sel_hi:[1,1,0]
	v_pk_fma_f32 v[180:181], v[172:173], v[180:181], s[34:35] op_sel_hi:[1,1,0]
	v_pk_fma_f32 v[182:183], v[174:175], v[182:183], s[34:35] op_sel_hi:[1,1,0]
	v_pk_fma_f32 v[176:177], v[168:169], v[176:177], s[36:37] op_sel_hi:[1,1,0]
	v_pk_fma_f32 v[178:179], v[170:171], v[178:179], s[36:37] op_sel_hi:[1,1,0]
	v_pk_fma_f32 v[180:181], v[172:173], v[180:181], s[36:37] op_sel_hi:[1,1,0]
	v_pk_fma_f32 v[182:183], v[174:175], v[182:183], s[36:37] op_sel_hi:[1,1,0]
	v_pk_fma_f32 v[176:177], v[168:169], v[176:177], s[38:39] op_sel_hi:[1,1,0]
	v_pk_fma_f32 v[178:179], v[170:171], v[178:179], s[38:39] op_sel_hi:[1,1,0]
	v_pk_fma_f32 v[180:181], v[172:173], v[180:181], s[38:39] op_sel_hi:[1,1,0]
	v_pk_fma_f32 v[182:183], v[174:175], v[182:183], s[38:39] op_sel_hi:[1,1,0]
	v_pk_fma_f32 v[176:177], v[168:169], v[176:177], s[40:41] op_sel_hi:[1,1,0]
	v_pk_fma_f32 v[178:179], v[170:171], v[178:179], s[40:41] op_sel_hi:[1,1,0]
	v_pk_fma_f32 v[180:181], v[172:173], v[180:181], s[40:41] op_sel_hi:[1,1,0]
	v_pk_fma_f32 v[182:183], v[174:175], v[182:183], s[40:41] op_sel_hi:[1,1,0]
	v_pk_fma_f32 v[176:177], v[168:169], v[176:177], s[42:43] op_sel_hi:[1,1,0]
	v_pk_fma_f32 v[178:179], v[170:171], v[178:179], s[42:43] op_sel_hi:[1,1,0]
	v_pk_fma_f32 v[180:181], v[172:173], v[180:181], s[42:43] op_sel_hi:[1,1,0]
	v_pk_fma_f32 v[182:183], v[174:175], v[182:183], s[42:43] op_sel_hi:[1,1,0]
	v_pk_fma_f32 v[176:177], v[168:169], v[176:177], s[44:45] op_sel_hi:[1,1,0]
	v_pk_fma_f32 v[178:179], v[170:171], v[178:179], s[44:45] op_sel_hi:[1,1,0]
	v_pk_fma_f32 v[180:181], v[172:173], v[180:181], s[44:45] op_sel_hi:[1,1,0]
	v_pk_fma_f32 v[182:183], v[174:175], v[182:183], s[44:45] op_sel_hi:[1,1,0]
	v_pk_fma_f32 v[168:169], v[168:169], v[176:177], s[48:49] op_sel_hi:[1,1,0]
	v_pk_fma_f32 v[170:171], v[170:171], v[178:179], s[48:49] op_sel_hi:[1,1,0]
	v_pk_fma_f32 v[172:173], v[172:173], v[180:181], s[48:49] op_sel_hi:[1,1,0]
	v_pk_fma_f32 v[174:175], v[174:175], v[182:183], s[48:49] op_sel_hi:[1,1,0]
	v_pk_fma_f32 v[160:161], v[160:161], v[168:169], 0.5 op_sel_hi:[1,1,0]
	v_pk_fma_f32 v[162:163], v[162:163], v[170:171], 0.5 op_sel_hi:[1,1,0]
	v_pk_fma_f32 v[164:165], v[164:165], v[172:173], 0.5 op_sel_hi:[1,1,0]
	v_pk_fma_f32 v[166:167], v[166:167], v[174:175], 0.5 op_sel_hi:[1,1,0]
	v_pk_mul_f32 v[132:133], v[132:133], v[160:161]
	v_pk_mul_f32 v[134:135], v[134:135], v[162:163]
	v_pk_mul_f32 v[128:129], v[128:129], v[164:165]
	v_pk_mul_f32 v[130:131], v[130:131], v[166:167]
	v_cvt_pk_bf16_f32 v188, v132, v133
	v_cvt_pk_bf16_f32 v189, v134, v135
	v_cvt_pk_bf16_f32 v190, v128, v129
	v_cvt_pk_bf16_f32 v191, v130, v131
	global_store_dwordx4 v[196:197], v[188:191], off offset:256
	s_and_b64 vcc, exec, s[70:71]
	s_cbranch_vccz .Lg9_nostat_0
	v_pk_add_f32 v[160:161], v[140:141], v[142:143]
	v_pk_add_f32 v[162:163], v[136:137], v[138:139]
	v_pk_add_f32 v[164:165], v[132:133], v[134:135]
	v_pk_add_f32 v[166:167], v[128:129], v[130:131]
	v_pk_mul_f32 v[168:169], v[140:141], v[140:141]
	v_pk_mul_f32 v[170:171], v[132:133], v[132:133]
	v_pk_add_f32 v[160:161], v[160:161], v[162:163]
	v_pk_add_f32 v[164:165], v[164:165], v[166:167]
	v_pk_fma_f32 v[168:169], v[142:143], v[142:143], v[168:169]
	v_pk_fma_f32 v[170:171], v[134:135], v[134:135], v[170:171]
	v_pk_fma_f32 v[168:169], v[136:137], v[136:137], v[168:169]
	v_pk_fma_f32 v[170:171], v[128:129], v[128:129], v[170:171]
	v_pk_fma_f32 v[168:169], v[138:139], v[138:139], v[168:169]
	v_pk_fma_f32 v[170:171], v[130:131], v[130:131], v[170:171]
	v_pk_add_f32 v[160:161], v[160:161], v[164:165]
	v_pk_add_f32 v[168:169], v[168:169], v[170:171]
	s_nop 0
	v_add_f32_e32 v198, v160, v161
	v_add_f32_e32 v200, v168, v169
	v_mov_b32_e32 v199, v198
	s_nop 1
	v_permlane16_swap_b32 v199, v198
	s_nop 1
	v_add_f32_e32 v198, v199, v198
	v_mov_b32_e32 v202, v198
	v_mov_b32_e32 v201, v200
	s_nop 1
	v_permlane32_swap_b32 v202, v198
	s_nop 1
	s_nop 1
	v_permlane16_swap_b32 v201, v200
	s_nop 1
	v_add_f32_e32 v199, v201, v200
	v_mov_b32_e32 v203, v199
	s_nop 1
	v_permlane32_swap_b32 v203, v199
	s_nop 1
	s_and_saveexec_b64 s[4:5], s[6:7]
	v_lshlrev_b64 v[194:195], 8, v[192:193]
	v_lshl_add_u64 v[194:195], s[16:17], 0, v[194:195]
	v_lshl_add_u64 v[194:195], s[68:69], 3, v[194:195]
	v_pk_add_f32 v[200:201], v[202:203], v[198:199]
	global_store_dwordx2 v[194:195], v[200:201], off
	s_or_b64 exec, exec, s[4:5]

.LBB0_1972:
	s_getpc_b64 s[100:101]
	global_load_dword a0, v250, s[100:101]
	s_waitcnt vmcnt(0)
	s_barrier

.LBB0_2140:
	s_getpc_b64 s[100:101]
	global_load_dword a0, v250, s[100:101]
	s_mov_b32 s19, 0
	v_mbcnt_lo_u32_b32 v162, -1, 0
	v_mbcnt_hi_u32_b32 v162, -1, v162
	s_lshl_b32 s19, s64, 8
	v_readlane_b32 s64, v249, 35
	v_lshrrev_b32_e32 v8, 1, v162
	v_and_or_b32 v8, v8, 24, s19
	s_lshr_b32 s19, s26, 5
	s_mul_i32 s28, s19, 0x1800
	s_ashr_i32 s29, s28, 31
	v_or_b32_e32 v8, s52, v8
	s_lshl_b64 s[28:29], s[28:29], 2
	s_add_u32 s30, s48, s28
	v_ashrrev_i32_e32 v9, 31, v8
	s_addc_u32 s31, s49, s29
	v_lshlrev_b64 v[14:15], 2, v[8:9]
	v_lshl_add_u64 v[146:147], s[30:31], 0, v[14:15]
	s_add_u32 s30, s44, s28
	s_addc_u32 s31, s45, s29
	s_add_u32 s28, s30, 0x1000
	s_addc_u32 s29, s31, 0
	v_lshl_add_u64 v[148:149], s[28:29], 0, v[14:15]
	s_lshl_b32 s19, s26, 8
	global_load_dwordx4 v[10:13], v[146:147], off
	global_load_dwordx4 v[136:139], v[146:147], off offset:16
	global_load_dwordx4 v[140:143], v[148:149], off
	global_load_dwordx4 v[150:153], v[148:149], off offset:16
	s_add_i32 s19, s19, s51
	v_and_or_b32 v148, v162, 15, s19
	v_ashrrev_i32_e32 v149, 31, v148
	v_lshlrev_b64 v[162:163], 10, v[148:149]
	v_lshl_add_u64 v[162:163], v[162:163], 0, v[8:9]
	v_lshl_add_u64 v[200:201], s[30:31], 0, v[14:15]
	v_lshlrev_b64 v[212:213], 1, v[162:163]
	v_readlane_b32 s70, v249, 41
	v_readlane_b32 s71, v249, 42
	global_load_dwordx4 v[154:157], v[200:201], off offset:16
	global_load_dwordx4 v[158:161], v[200:201], off
	v_lshl_add_u64 v[214:215], s[90:91], 0, v[212:213]
	v_mov_b32_e32 v246, v212
	v_lshl_add_u64 v[14:15], s[70:71], 0, v[14:15]
	global_load_dwordx4 v[162:165], v[214:215], off
	global_load_dwordx4 v[230:233], v246, s[90:91] offset:256
	v_add_u32_e32 v247, 0x8000, v246
	global_load_dwordx4 v[234:237], v247, s[90:91]
	v_add_u32_e32 v247, 0x8000, v246
	global_load_dwordx4 v[238:241], v247, s[90:91] offset:256
	v_add_u32_e32 v247, 0x10000, v246
	global_load_dwordx4 v[242:245], v247, s[90:91]
	v_add_u32_e32 v247, 0x10000, v246
	global_load_dwordx4 v[226:229], v247, s[90:91] offset:256
	global_load_dwordx4 v[166:169], v[14:15], off
	global_load_dwordx4 v[170:173], v[14:15], off offset:16
	global_load_dwordx4 v[180:183], v[14:15], off offset:528
	global_load_dwordx4 v[184:187], v[14:15], off offset:512
	global_load_dwordx4 v[188:191], v[146:147], off offset:528
	global_load_dwordx4 v[192:195], v[146:147], off offset:512
	global_load_dwordx4 v[196:199], v[200:201], off offset:528
	s_nop 0
	global_load_dwordx4 v[200:203], v[200:201], off offset:512
	v_or_b32_e32 v204, 0x80, v8
	v_ashrrev_i32_e32 v205, 31, v204
	v_lshl_add_u64 v[14:15], v[204:205], 2, s[28:29]
	global_load_dwordx4 v[204:207], v[14:15], off offset:16
	global_load_dwordx4 v[208:211], v[14:15], off
	v_readlane_b32 s72, v249, 43
	v_readlane_b32 s73, v249, 44
	v_readlane_b32 s74, v249, 45
	v_readlane_b32 s75, v249, 46
	v_readlane_b32 s76, v249, 47
	v_readlane_b32 s77, v249, 48
	v_readlane_b32 s78, v249, 49
	v_readlane_b32 s79, v249, 50
	v_readlane_b32 s72, v249, 55
	v_readlane_b32 s76, v249, 59
	v_readlane_b32 s77, v249, 60
	v_readlane_b32 s73, v249, 56
	v_readlane_b32 s74, v249, 57
	v_readlane_b32 s75, v249, 58
	v_readlane_b32 s78, v249, 61
	v_readlane_b32 s79, v249, 62
	s_and_b64 vcc, exec, s[0:1]
	s_mov_b64 s[0:1], -1
	v_readlane_b32 s65, v249, 36
	v_readlane_b32 s66, v249, 37
	v_readlane_b32 s67, v249, 38
	v_readlane_b32 s68, v249, 39
	v_readlane_b32 s69, v249, 40
	s_waitcnt vmcnt(0)
	v_pk_add_f32 v[216:217], v[12:13], 1.0 op_sel_hi:[1,0]
	v_pk_add_f32 v[220:221], v[138:139], 1.0 op_sel_hi:[1,0]
	v_add_f32_e32 v138, 1.0, v140
	v_add_f32_e32 v139, 1.0, v141
	v_add_f32_e32 v140, 1.0, v142
	v_add_f32_e32 v141, 1.0, v143
	v_add_f32_e32 v142, 1.0, v150
	v_add_f32_e32 v143, 1.0, v151
	v_add_f32_e32 v146, 1.0, v152
	v_add_f32_e32 v147, 1.0, v153
	v_rcp_f32_e32 v138, v138
	v_rcp_f32_e32 v139, v139
	v_rcp_f32_e32 v140, v140
	v_rcp_f32_e32 v141, v141
	v_rcp_f32_e32 v142, v142
	v_rcp_f32_e32 v143, v143
	v_rcp_f32_e32 v146, v146
	v_rcp_f32_e32 v147, v147
	v_pk_mul_f32 v[138:139], v[138:139], s[14:15] op_sel_hi:[1,0]
	v_pk_mul_f32 v[140:141], v[140:141], s[14:15] op_sel_hi:[1,0]
	v_pk_mul_f32 v[142:143], v[142:143], s[14:15] op_sel_hi:[1,0]
	v_pk_mul_f32 v[146:147], v[146:147], s[14:15] op_sel_hi:[1,0]
	v_pk_add_f32 v[218:219], v[10:11], 1.0 op_sel_hi:[1,0]
	v_pk_add_f32 v[222:223], v[136:137], 1.0 op_sel_hi:[1,0]
	v_pk_mul_f32 v[150:151], v[160:161], v[140:141]
	v_pk_mul_f32 v[152:153], v[158:159], v[138:139]
	v_pk_mul_f32 v[156:157], v[156:157], v[146:147]
	v_pk_mul_f32 v[158:159], v[154:155], v[142:143]
	v_lshlrev_b32_e32 v160, 16, v162
	v_and_b32_e32 v161, 0xffff0000, v162
	v_lshlrev_b32_e32 v162, 16, v163
	v_and_b32_e32 v163, 0xffff0000, v163
	v_lshlrev_b32_e32 v224, 16, v164
	v_and_b32_e32 v225, 0xffff0000, v164
	v_lshlrev_b32_e32 v164, 16, v165
	v_and_b32_e32 v165, 0xffff0000, v165
	v_pk_fma_f32 v[150:151], v[168:169], v[216:217], v[150:151] neg_lo:[0,0,1] neg_hi:[0,0,1]
	v_pk_fma_f32 v[154:155], v[166:167], v[218:219], v[152:153] neg_lo:[0,0,1] neg_hi:[0,0,1]
	v_pk_fma_f32 v[152:153], v[172:173], v[220:221], v[156:157] neg_lo:[0,0,1] neg_hi:[0,0,1]
	v_pk_fma_f32 v[156:157], v[170:171], v[222:223], v[158:159] neg_lo:[0,0,1] neg_hi:[0,0,1]
	v_pk_mul_f32 v[10:11], v[216:217], s[16:17] op_sel_hi:[1,0]
	v_pk_mul_f32 v[14:15], v[218:219], s[16:17] op_sel_hi:[1,0]
	v_pk_mul_f32 v[12:13], v[220:221], s[16:17] op_sel_hi:[1,0]
	v_pk_mul_f32 v[136:137], v[222:223], s[16:17] op_sel_hi:[1,0]
	v_pk_fma_f32 v[158:159], v[138:139], v[160:161], v[154:155]
	v_pk_fma_f32 v[160:161], v[140:141], v[162:163], v[150:151]
	v_pk_fma_f32 v[162:163], v[142:143], v[224:225], v[156:157]
	v_pk_fma_f32 v[164:165], v[146:147], v[164:165], v[152:153]
	v_pk_fma_f32 v[132:133], v[132:133], v[14:15], v[158:159]
	v_pk_fma_f32 v[134:135], v[134:135], v[10:11], v[160:161]
	v_pk_fma_f32 v[158:159], v[128:129], v[136:137], v[162:163]
	v_pk_fma_f32 v[160:161], v[130:131], v[12:13], v[164:165]
	v_cvt_pk_bf16_f32 v128, v132, v133
	v_cvt_pk_bf16_f32 v129, v134, v135
	v_cvt_pk_bf16_f32 v130, v158, v159
	v_cvt_pk_bf16_f32 v131, v160, v161
	v_lshl_add_u64 v[216:217], s[76:77], 0, v[212:213]
	global_store_dwordx4 v[216:217], v[128:131], off
	v_add_f32_e32 v149, 1.0, v208
	v_add_f32_e32 v159, 1.0, v209
	v_add_f32_e32 v160, 1.0, v210
	v_add_f32_e32 v161, 1.0, v211
	v_add_f32_e32 v164, 1.0, v204
	v_add_f32_e32 v165, 1.0, v205
	v_add_f32_e32 v166, 1.0, v206
	v_add_f32_e32 v167, 1.0, v207
	v_rcp_f32_e32 v158, v149
	v_rcp_f32_e32 v159, v159
	v_rcp_f32_e32 v160, v160
	v_rcp_f32_e32 v161, v161
	v_rcp_f32_e32 v170, v164
	v_rcp_f32_e32 v171, v165
	v_rcp_f32_e32 v172, v166
	v_rcp_f32_e32 v173, v167
	v_or_b32_e32 v128, 16, v148
	v_ashrrev_i32_e32 v129, 31, v128
	v_pk_mul_f32 v[166:167], v[158:159], s[14:15] op_sel_hi:[1,0]
	v_pk_mul_f32 v[164:165], v[160:161], s[14:15] op_sel_hi:[1,0]
	v_pk_mul_f32 v[160:161], v[170:171], s[14:15] op_sel_hi:[1,0]
	v_pk_mul_f32 v[158:159], v[172:173], s[14:15] op_sel_hi:[1,0]
	v_lshlrev_b64 v[128:129], 10, v[128:129]
	v_pk_add_f32 v[162:163], v[194:195], 1.0 op_sel_hi:[1,0]
	v_pk_add_f32 v[168:169], v[192:193], 1.0 op_sel_hi:[1,0]
	v_pk_add_f32 v[190:191], v[190:191], 1.0 op_sel_hi:[1,0]
	v_pk_add_f32 v[188:189], v[188:189], 1.0 op_sel_hi:[1,0]
	v_pk_mul_f32 v[170:171], v[202:203], v[164:165]
	v_pk_mul_f32 v[172:173], v[200:201], v[166:167]
	v_pk_mul_f32 v[192:193], v[198:199], v[158:159]
	v_pk_mul_f32 v[194:195], v[196:197], v[160:161]
	v_lshl_add_u64 v[128:129], v[128:129], 0, v[8:9]
	v_pk_mul_f32 v[130:131], v[162:163], s[16:17] op_sel_hi:[1,0]
	v_pk_mul_f32 v[132:133], v[168:169], s[16:17] op_sel_hi:[1,0]
	v_pk_fma_f32 v[170:171], v[186:187], v[162:163], v[170:171] neg_lo:[0,0,1] neg_hi:[0,0,1]
	v_pk_fma_f32 v[172:173], v[184:185], v[168:169], v[172:173] neg_lo:[0,0,1] neg_hi:[0,0,1]
	v_pk_fma_f32 v[162:163], v[182:183], v[190:191], v[192:193] neg_lo:[0,0,1] neg_hi:[0,0,1]
	v_pk_fma_f32 v[168:169], v[180:181], v[188:189], v[194:195] neg_lo:[0,0,1] neg_hi:[0,0,1]
	v_lshlrev_b64 v[218:219], 1, v[128:129]
	v_pk_mul_f32 v[128:129], v[190:191], s[16:17] op_sel_hi:[1,0]
	v_pk_mul_f32 v[134:135], v[188:189], s[16:17] op_sel_hi:[1,0]
	v_lshl_add_u64 v[220:221], s[90:91], 0, v[218:219]
	s_waitcnt vmcnt(9)
	v_mov_b32_e32 v212, v230
	v_mov_b32_e32 v213, v231
	v_mov_b32_e32 v214, v232
	v_mov_b32_e32 v215, v233
	v_add_u32_e32 v247, 0x18000, v246
	global_load_dwordx4 v[230:233], v247, s[90:91]
	v_lshlrev_b32_e32 v180, 16, v212
	v_and_b32_e32 v181, 0xffff0000, v212
	v_lshlrev_b32_e32 v182, 16, v213
	v_and_b32_e32 v183, 0xffff0000, v213
	v_lshlrev_b32_e32 v184, 16, v214
	v_and_b32_e32 v185, 0xffff0000, v214
	v_lshlrev_b32_e32 v186, 16, v215
	v_and_b32_e32 v187, 0xffff0000, v215
	v_pk_fma_f32 v[180:181], v[166:167], v[180:181], v[172:173]
	v_pk_fma_f32 v[182:183], v[164:165], v[182:183], v[170:171]
	v_pk_fma_f32 v[184:185], v[160:161], v[184:185], v[168:169]
	v_pk_fma_f32 v[186:187], v[158:159], v[186:187], v[162:163]
	v_pk_fma_f32 v[124:125], v[124:125], v[132:133], v[180:181]
	v_pk_fma_f32 v[126:127], v[126:127], v[130:131], v[182:183]
	v_pk_fma_f32 v[180:181], v[120:121], v[134:135], v[184:185]
	v_pk_fma_f32 v[182:183], v[122:123], v[128:129], v[186:187]
	v_cvt_pk_bf16_f32 v120, v124, v125
	v_cvt_pk_bf16_f32 v121, v126, v127
	v_cvt_pk_bf16_f32 v122, v180, v181
	v_cvt_pk_bf16_f32 v123, v182, v183
	global_store_dwordx4 v[216:217], v[120:123], off offset:256
	v_lshl_add_u64 v[124:125], s[76:77], 0, v[218:219]
	s_waitcnt vmcnt(9)
	v_mov_b32_e32 v120, v234
	v_mov_b32_e32 v121, v235
	v_mov_b32_e32 v122, v236
	v_mov_b32_e32 v123, v237
	v_add_u32_e32 v247, 0x18000, v246
	global_load_dwordx4 v[234:237], v247, s[90:91] offset:256
	v_lshlrev_b32_e32 v126, 16, v120
	v_and_b32_e32 v127, 0xffff0000, v120
	v_lshlrev_b32_e32 v120, 16, v121
	v_and_b32_e32 v121, 0xffff0000, v121
	v_lshlrev_b32_e32 v180, 16, v122
	v_and_b32_e32 v181, 0xffff0000, v122
	v_lshlrev_b32_e32 v122, 16, v123
	v_and_b32_e32 v123, 0xffff0000, v123
	v_pk_fma_f32 v[126:127], v[138:139], v[126:127], v[154:155]
	v_pk_fma_f32 v[120:121], v[140:141], v[120:121], v[150:151]
	v_pk_fma_f32 v[180:181], v[142:143], v[180:181], v[156:157]
	v_pk_fma_f32 v[122:123], v[146:147], v[122:123], v[152:153]
	v_pk_fma_f32 v[116:117], v[116:117], v[14:15], v[126:127]
	v_pk_fma_f32 v[118:119], v[118:119], v[10:11], v[120:121]
	v_pk_fma_f32 v[120:121], v[112:113], v[136:137], v[180:181]
	v_pk_fma_f32 v[122:123], v[114:115], v[12:13], v[122:123]
	v_cvt_pk_bf16_f32 v112, v116, v117
	v_cvt_pk_bf16_f32 v113, v118, v119
	v_cvt_pk_bf16_f32 v114, v120, v121
	v_cvt_pk_bf16_f32 v115, v122, v123
	global_store_dwordx4 v[124:125], v[112:115], off
	v_or_b32_e32 v116, 32, v148
	v_ashrrev_i32_e32 v117, 31, v116
	v_lshlrev_b64 v[116:117], 10, v[116:117]
	v_lshl_add_u64 v[116:117], v[116:117], 0, v[8:9]
	v_lshlrev_b64 v[116:117], 1, v[116:117]
	v_lshl_add_u64 v[118:119], s[90:91], 0, v[116:117]
	s_waitcnt vmcnt(9)
	v_mov_b32_e32 v112, v238
	v_mov_b32_e32 v113, v239
	v_mov_b32_e32 v114, v240
	v_mov_b32_e32 v115, v241
	v_add_u32_e32 v247, 0x40000, v246
	global_load_dwordx4 v[238:241], v247, s[90:91]
	v_lshlrev_b32_e32 v120, 16, v112
	v_and_b32_e32 v121, 0xffff0000, v112
	v_lshlrev_b32_e32 v112, 16, v113
	v_and_b32_e32 v113, 0xffff0000, v113
	v_lshlrev_b32_e32 v122, 16, v114
	v_and_b32_e32 v123, 0xffff0000, v114
	v_lshlrev_b32_e32 v114, 16, v115
	v_and_b32_e32 v115, 0xffff0000, v115
	v_pk_fma_f32 v[120:121], v[166:167], v[120:121], v[172:173]
	v_pk_fma_f32 v[112:113], v[164:165], v[112:113], v[170:171]
	v_pk_fma_f32 v[122:123], v[160:161], v[122:123], v[168:169]
	v_pk_fma_f32 v[114:115], v[158:159], v[114:115], v[162:163]
	v_pk_fma_f32 v[108:109], v[108:109], v[132:133], v[120:121]
	v_pk_fma_f32 v[110:111], v[110:111], v[130:131], v[112:113]
	v_pk_fma_f32 v[112:113], v[104:105], v[134:135], v[122:123]
	v_pk_fma_f32 v[114:115], v[106:107], v[128:129], v[114:115]
	v_cvt_pk_bf16_f32 v104, v108, v109
	v_cvt_pk_bf16_f32 v105, v110, v111
	v_cvt_pk_bf16_f32 v106, v112, v113
	v_cvt_pk_bf16_f32 v107, v114, v115
	global_store_dwordx4 v[124:125], v[104:107], off offset:256
	v_lshl_add_u64 v[108:109], s[76:77], 0, v[116:117]
	s_waitcnt vmcnt(9)
	v_mov_b32_e32 v104, v242
	v_mov_b32_e32 v105, v243
	v_mov_b32_e32 v106, v244
	v_mov_b32_e32 v107, v245
	v_add_u32_e32 v247, 0x40000, v246
	global_load_dwordx4 v[242:245], v247, s[90:91] offset:256
	v_lshlrev_b32_e32 v110, 16, v104
	v_and_b32_e32 v111, 0xffff0000, v104
	v_lshlrev_b32_e32 v104, 16, v105
	v_and_b32_e32 v105, 0xffff0000, v105
	v_lshlrev_b32_e32 v112, 16, v106
	v_and_b32_e32 v113, 0xffff0000, v106
	v_lshlrev_b32_e32 v106, 16, v107
	v_and_b32_e32 v107, 0xffff0000, v107
	v_pk_fma_f32 v[110:111], v[138:139], v[110:111], v[154:155]
	v_pk_fma_f32 v[104:105], v[140:141], v[104:105], v[150:151]
	v_pk_fma_f32 v[112:113], v[142:143], v[112:113], v[156:157]
	v_pk_fma_f32 v[106:107], v[146:147], v[106:107], v[152:153]
	v_pk_fma_f32 v[100:101], v[100:101], v[14:15], v[110:111]
	v_pk_fma_f32 v[102:103], v[102:103], v[10:11], v[104:105]
	v_pk_fma_f32 v[104:105], v[96:97], v[136:137], v[112:113]
	v_pk_fma_f32 v[106:107], v[98:99], v[12:13], v[106:107]
	v_cvt_pk_bf16_f32 v96, v100, v101
	v_cvt_pk_bf16_f32 v97, v102, v103
	v_cvt_pk_bf16_f32 v98, v104, v105
	v_cvt_pk_bf16_f32 v99, v106, v107
	global_store_dwordx4 v[108:109], v[96:99], off
	v_or_b32_e32 v100, 48, v148
	v_ashrrev_i32_e32 v101, 31, v100
	v_lshlrev_b64 v[100:101], 10, v[100:101]
	v_lshl_add_u64 v[100:101], v[100:101], 0, v[8:9]
	v_lshlrev_b64 v[100:101], 1, v[100:101]
	v_lshl_add_u64 v[102:103], s[90:91], 0, v[100:101]
	s_waitcnt vmcnt(9)
	v_mov_b32_e32 v96, v226
	v_mov_b32_e32 v97, v227
	v_mov_b32_e32 v98, v228
	v_mov_b32_e32 v99, v229
	v_add_u32_e32 v247, 0x48000, v246
	global_load_dwordx4 v[226:229], v247, s[90:91]
	v_lshlrev_b32_e32 v104, 16, v96
	v_and_b32_e32 v105, 0xffff0000, v96
	v_lshlrev_b32_e32 v96, 16, v97
	v_and_b32_e32 v97, 0xffff0000, v97
	v_lshlrev_b32_e32 v106, 16, v98
	v_and_b32_e32 v107, 0xffff0000, v98
	v_lshlrev_b32_e32 v98, 16, v99
	v_and_b32_e32 v99, 0xffff0000, v99
	v_pk_fma_f32 v[104:105], v[166:167], v[104:105], v[172:173]
	v_pk_fma_f32 v[96:97], v[164:165], v[96:97], v[170:171]
	v_pk_fma_f32 v[106:107], v[160:161], v[106:107], v[168:169]
	v_pk_fma_f32 v[98:99], v[158:159], v[98:99], v[162:163]
	v_pk_fma_f32 v[92:93], v[92:93], v[132:133], v[104:105]
	v_pk_fma_f32 v[94:95], v[94:95], v[130:131], v[96:97]
	v_pk_fma_f32 v[96:97], v[88:89], v[134:135], v[106:107]
	v_pk_fma_f32 v[98:99], v[90:91], v[128:129], v[98:99]
	v_cvt_pk_bf16_f32 v88, v92, v93
	v_cvt_pk_bf16_f32 v89, v94, v95
	v_cvt_pk_bf16_f32 v90, v96, v97
	v_cvt_pk_bf16_f32 v91, v98, v99
	global_store_dwordx4 v[108:109], v[88:91], off offset:256
	v_lshl_add_u64 v[92:93], s[76:77], 0, v[100:101]
	s_waitcnt vmcnt(9)
	v_mov_b32_e32 v88, v230
	v_mov_b32_e32 v89, v231
	v_mov_b32_e32 v90, v232
	v_mov_b32_e32 v91, v233
	v_add_u32_e32 v247, 0x48000, v246
	global_load_dwordx4 v[230:233], v247, s[90:91] offset:256
	v_lshlrev_b32_e32 v94, 16, v88
	v_and_b32_e32 v95, 0xffff0000, v88
	v_lshlrev_b32_e32 v88, 16, v89
	v_and_b32_e32 v89, 0xffff0000, v89
	v_lshlrev_b32_e32 v96, 16, v90
	v_and_b32_e32 v97, 0xffff0000, v90
	v_lshlrev_b32_e32 v90, 16, v91
	v_and_b32_e32 v91, 0xffff0000, v91
	v_pk_fma_f32 v[94:95], v[138:139], v[94:95], v[154:155]
	v_pk_fma_f32 v[88:89], v[140:141], v[88:89], v[150:151]
	v_pk_fma_f32 v[96:97], v[142:143], v[96:97], v[156:157]
	v_pk_fma_f32 v[90:91], v[146:147], v[90:91], v[152:153]
	v_pk_fma_f32 v[84:85], v[84:85], v[14:15], v[94:95]
	v_pk_fma_f32 v[86:87], v[86:87], v[10:11], v[88:89]
	v_pk_fma_f32 v[88:89], v[80:81], v[136:137], v[96:97]
	v_pk_fma_f32 v[90:91], v[82:83], v[12:13], v[90:91]
	v_cvt_pk_bf16_f32 v80, v84, v85
	v_cvt_pk_bf16_f32 v81, v86, v87
	v_cvt_pk_bf16_f32 v82, v88, v89
	v_cvt_pk_bf16_f32 v83, v90, v91
	global_store_dwordx4 v[92:93], v[80:83], off
	v_add_u32_e32 v84, 0x80, v148
	v_ashrrev_i32_e32 v85, 31, v84
	v_lshlrev_b64 v[84:85], 10, v[84:85]
	v_lshl_add_u64 v[84:85], v[84:85], 0, v[8:9]
	v_lshlrev_b64 v[84:85], 1, v[84:85]
	v_lshl_add_u64 v[86:87], s[90:91], 0, v[84:85]
	s_waitcnt vmcnt(9)
	v_mov_b32_e32 v80, v234
	v_mov_b32_e32 v81, v235
	v_mov_b32_e32 v82, v236
	v_mov_b32_e32 v83, v237
	v_add_u32_e32 v247, 0x50000, v246
	global_load_dwordx4 v[234:237], v247, s[90:91]
	v_lshlrev_b32_e32 v88, 16, v80
	v_and_b32_e32 v89, 0xffff0000, v80
	v_lshlrev_b32_e32 v80, 16, v81
	v_and_b32_e32 v81, 0xffff0000, v81
	v_lshlrev_b32_e32 v90, 16, v82
	v_and_b32_e32 v91, 0xffff0000, v82
	v_lshlrev_b32_e32 v82, 16, v83
	v_and_b32_e32 v83, 0xffff0000, v83
	v_pk_fma_f32 v[88:89], v[166:167], v[88:89], v[172:173]
	v_pk_fma_f32 v[80:81], v[164:165], v[80:81], v[170:171]
	v_pk_fma_f32 v[90:91], v[160:161], v[90:91], v[168:169]
	v_pk_fma_f32 v[82:83], v[158:159], v[82:83], v[162:163]
	v_pk_fma_f32 v[76:77], v[76:77], v[132:133], v[88:89]
	v_pk_fma_f32 v[78:79], v[78:79], v[130:131], v[80:81]
	v_pk_fma_f32 v[80:81], v[72:73], v[134:135], v[90:91]
	v_pk_fma_f32 v[82:83], v[74:75], v[128:129], v[82:83]
	v_cvt_pk_bf16_f32 v72, v76, v77
	v_cvt_pk_bf16_f32 v73, v78, v79
	v_cvt_pk_bf16_f32 v74, v80, v81
	v_cvt_pk_bf16_f32 v75, v82, v83
	global_store_dwordx4 v[92:93], v[72:75], off offset:256
	v_lshl_add_u64 v[76:77], s[76:77], 0, v[84:85]
	s_waitcnt vmcnt(9)
	v_mov_b32_e32 v72, v238
	v_mov_b32_e32 v73, v239
	v_mov_b32_e32 v74, v240
	v_mov_b32_e32 v75, v241
	v_add_u32_e32 v247, 0x50000, v246
	global_load_dwordx4 v[238:241], v247, s[90:91] offset:256
	v_lshlrev_b32_e32 v78, 16, v72
	v_and_b32_e32 v79, 0xffff0000, v72
	v_lshlrev_b32_e32 v72, 16, v73
	v_and_b32_e32 v73, 0xffff0000, v73
	v_lshlrev_b32_e32 v80, 16, v74
	v_and_b32_e32 v81, 0xffff0000, v74
	v_lshlrev_b32_e32 v74, 16, v75
	v_and_b32_e32 v75, 0xffff0000, v75
	v_pk_fma_f32 v[78:79], v[138:139], v[78:79], v[154:155]
	v_pk_fma_f32 v[72:73], v[140:141], v[72:73], v[150:151]
	v_pk_fma_f32 v[80:81], v[142:143], v[80:81], v[156:157]
	v_pk_fma_f32 v[74:75], v[146:147], v[74:75], v[152:153]
	v_pk_fma_f32 v[68:69], v[68:69], v[14:15], v[78:79]
	v_pk_fma_f32 v[70:71], v[70:71], v[10:11], v[72:73]
	v_pk_fma_f32 v[72:73], v[64:65], v[136:137], v[80:81]
	v_pk_fma_f32 v[74:75], v[66:67], v[12:13], v[74:75]
	v_cvt_pk_bf16_f32 v64, v68, v69
	v_cvt_pk_bf16_f32 v65, v70, v71
	v_cvt_pk_bf16_f32 v66, v72, v73
	v_cvt_pk_bf16_f32 v67, v74, v75
	global_store_dwordx4 v[76:77], v[64:67], off
	v_add_u32_e32 v68, 0x90, v148
	v_ashrrev_i32_e32 v69, 31, v68
	v_lshlrev_b64 v[68:69], 10, v[68:69]
	v_lshl_add_u64 v[68:69], v[68:69], 0, v[8:9]
	v_lshlrev_b64 v[68:69], 1, v[68:69]
	v_lshl_add_u64 v[70:71], s[90:91], 0, v[68:69]
	s_waitcnt vmcnt(9)
	v_mov_b32_e32 v64, v242
	v_mov_b32_e32 v65, v243
	v_mov_b32_e32 v66, v244
	v_mov_b32_e32 v67, v245
	v_add_u32_e32 v247, 0x58000, v246
	global_load_dwordx4 v[242:245], v247, s[90:91]
	v_lshlrev_b32_e32 v72, 16, v64
	v_and_b32_e32 v73, 0xffff0000, v64
	v_lshlrev_b32_e32 v64, 16, v65
	v_and_b32_e32 v65, 0xffff0000, v65
	v_lshlrev_b32_e32 v74, 16, v66
	v_and_b32_e32 v75, 0xffff0000, v66
	v_lshlrev_b32_e32 v66, 16, v67
	v_and_b32_e32 v67, 0xffff0000, v67
	v_pk_fma_f32 v[72:73], v[166:167], v[72:73], v[172:173]
	v_pk_fma_f32 v[64:65], v[164:165], v[64:65], v[170:171]
	v_pk_fma_f32 v[74:75], v[160:161], v[74:75], v[168:169]
	v_pk_fma_f32 v[66:67], v[158:159], v[66:67], v[162:163]
	v_pk_fma_f32 v[60:61], v[60:61], v[132:133], v[72:73]
	v_pk_fma_f32 v[62:63], v[62:63], v[130:131], v[64:65]
	v_pk_fma_f32 v[64:65], v[56:57], v[134:135], v[74:75]
	v_pk_fma_f32 v[66:67], v[58:59], v[128:129], v[66:67]
	v_cvt_pk_bf16_f32 v56, v60, v61
	v_cvt_pk_bf16_f32 v57, v62, v63
	v_cvt_pk_bf16_f32 v58, v64, v65
	v_cvt_pk_bf16_f32 v59, v66, v67
	global_store_dwordx4 v[76:77], v[56:59], off offset:256
	v_lshl_add_u64 v[60:61], s[76:77], 0, v[68:69]
	s_waitcnt vmcnt(9)
	v_mov_b32_e32 v56, v226
	v_mov_b32_e32 v57, v227
	v_mov_b32_e32 v58, v228
	v_mov_b32_e32 v59, v229
	v_add_u32_e32 v247, 0x58000, v246
	global_load_dwordx4 v[226:229], v247, s[90:91] offset:256
	v_lshlrev_b32_e32 v62, 16, v56
	v_and_b32_e32 v63, 0xffff0000, v56
	v_lshlrev_b32_e32 v56, 16, v57
	v_and_b32_e32 v57, 0xffff0000, v57
	v_lshlrev_b32_e32 v64, 16, v58
	v_and_b32_e32 v65, 0xffff0000, v58
	v_lshlrev_b32_e32 v58, 16, v59
	v_and_b32_e32 v59, 0xffff0000, v59
	v_pk_fma_f32 v[62:63], v[138:139], v[62:63], v[154:155]
	v_pk_fma_f32 v[56:57], v[140:141], v[56:57], v[150:151]
	v_pk_fma_f32 v[64:65], v[142:143], v[64:65], v[156:157]
	v_pk_fma_f32 v[58:59], v[146:147], v[58:59], v[152:153]
	v_pk_fma_f32 v[52:53], v[52:53], v[14:15], v[62:63]
	v_pk_fma_f32 v[54:55], v[54:55], v[10:11], v[56:57]
	v_pk_fma_f32 v[56:57], v[48:49], v[136:137], v[64:65]
	v_pk_fma_f32 v[58:59], v[50:51], v[12:13], v[58:59]
	v_cvt_pk_bf16_f32 v48, v52, v53
	v_cvt_pk_bf16_f32 v49, v54, v55
	v_cvt_pk_bf16_f32 v50, v56, v57
	v_cvt_pk_bf16_f32 v51, v58, v59
	global_store_dwordx4 v[60:61], v[48:51], off
	v_add_u32_e32 v52, 0xa0, v148
	v_ashrrev_i32_e32 v53, 31, v52
	v_lshlrev_b64 v[52:53], 10, v[52:53]
	v_lshl_add_u64 v[52:53], v[52:53], 0, v[8:9]
	v_lshlrev_b64 v[52:53], 1, v[52:53]
	v_lshl_add_u64 v[54:55], s[90:91], 0, v[52:53]
	s_waitcnt vmcnt(9)
	v_mov_b32_e32 v48, v230
	v_mov_b32_e32 v49, v231
	v_mov_b32_e32 v50, v232
	v_mov_b32_e32 v51, v233
	v_lshlrev_b32_e32 v56, 16, v48
	v_and_b32_e32 v57, 0xffff0000, v48
	v_lshlrev_b32_e32 v48, 16, v49
	v_and_b32_e32 v49, 0xffff0000, v49
	v_lshlrev_b32_e32 v58, 16, v50
	v_and_b32_e32 v59, 0xffff0000, v50
	v_lshlrev_b32_e32 v50, 16, v51
	v_and_b32_e32 v51, 0xffff0000, v51
	v_pk_fma_f32 v[56:57], v[166:167], v[56:57], v[172:173]
	v_pk_fma_f32 v[48:49], v[164:165], v[48:49], v[170:171]
	v_pk_fma_f32 v[58:59], v[160:161], v[58:59], v[168:169]
	v_pk_fma_f32 v[50:51], v[158:159], v[50:51], v[162:163]
	v_pk_fma_f32 v[44:45], v[44:45], v[132:133], v[56:57]
	v_pk_fma_f32 v[46:47], v[46:47], v[130:131], v[48:49]
	v_pk_fma_f32 v[48:49], v[40:41], v[134:135], v[58:59]
	v_pk_fma_f32 v[50:51], v[42:43], v[128:129], v[50:51]
	v_cvt_pk_bf16_f32 v40, v44, v45
	v_cvt_pk_bf16_f32 v41, v46, v47
	v_cvt_pk_bf16_f32 v42, v48, v49
	v_cvt_pk_bf16_f32 v43, v50, v51
	global_store_dwordx4 v[60:61], v[40:43], off offset:256
	v_lshl_add_u64 v[44:45], s[76:77], 0, v[52:53]
	s_waitcnt vmcnt(8)
	v_mov_b32_e32 v40, v234
	v_mov_b32_e32 v41, v235
	v_mov_b32_e32 v42, v236
	v_mov_b32_e32 v43, v237
	v_lshlrev_b32_e32 v46, 16, v40
	v_and_b32_e32 v47, 0xffff0000, v40
	v_lshlrev_b32_e32 v40, 16, v41
	v_and_b32_e32 v41, 0xffff0000, v41
	v_lshlrev_b32_e32 v48, 16, v42
	v_and_b32_e32 v49, 0xffff0000, v42
	v_lshlrev_b32_e32 v42, 16, v43
	v_and_b32_e32 v43, 0xffff0000, v43
	v_pk_fma_f32 v[46:47], v[138:139], v[46:47], v[154:155]
	v_pk_fma_f32 v[40:41], v[140:141], v[40:41], v[150:151]
	v_pk_fma_f32 v[48:49], v[142:143], v[48:49], v[156:157]
	v_pk_fma_f32 v[42:43], v[146:147], v[42:43], v[152:153]
	v_pk_fma_f32 v[36:37], v[36:37], v[14:15], v[46:47]
	v_pk_fma_f32 v[38:39], v[38:39], v[10:11], v[40:41]
	v_pk_fma_f32 v[40:41], v[32:33], v[136:137], v[48:49]
	v_pk_fma_f32 v[42:43], v[34:35], v[12:13], v[42:43]
	v_cvt_pk_bf16_f32 v32, v36, v37
	v_cvt_pk_bf16_f32 v33, v38, v39
	v_cvt_pk_bf16_f32 v34, v40, v41
	v_cvt_pk_bf16_f32 v35, v42, v43
	global_store_dwordx4 v[44:45], v[32:35], off
	v_add_u32_e32 v36, 0xb0, v148
	v_ashrrev_i32_e32 v37, 31, v36
	v_lshlrev_b64 v[36:37], 10, v[36:37]
	v_lshl_add_u64 v[8:9], v[36:37], 0, v[8:9]
	v_lshlrev_b64 v[8:9], 1, v[8:9]
	v_lshl_add_u64 v[36:37], s[90:91], 0, v[8:9]
	s_waitcnt vmcnt(7)
	v_mov_b32_e32 v32, v238
	v_mov_b32_e32 v33, v239
	v_mov_b32_e32 v34, v240
	v_mov_b32_e32 v35, v241
	v_lshlrev_b32_e32 v38, 16, v32
	v_and_b32_e32 v39, 0xffff0000, v32
	v_lshlrev_b32_e32 v32, 16, v33
	v_and_b32_e32 v33, 0xffff0000, v33
	v_lshlrev_b32_e32 v40, 16, v34
	v_and_b32_e32 v41, 0xffff0000, v34
	v_lshlrev_b32_e32 v34, 16, v35
	v_and_b32_e32 v35, 0xffff0000, v35
	v_pk_fma_f32 v[38:39], v[166:167], v[38:39], v[172:173]
	v_pk_fma_f32 v[32:33], v[164:165], v[32:33], v[170:171]
	v_pk_fma_f32 v[40:41], v[160:161], v[40:41], v[168:169]
	v_pk_fma_f32 v[34:35], v[158:159], v[34:35], v[162:163]
	v_pk_fma_f32 v[28:29], v[28:29], v[132:133], v[38:39]
	v_pk_fma_f32 v[30:31], v[30:31], v[130:131], v[32:33]
	v_pk_fma_f32 v[32:33], v[24:25], v[134:135], v[40:41]
	v_pk_fma_f32 v[34:35], v[26:27], v[128:129], v[34:35]
	v_cvt_pk_bf16_f32 v24, v28, v29
	v_cvt_pk_bf16_f32 v25, v30, v31
	v_cvt_pk_bf16_f32 v26, v32, v33
	v_cvt_pk_bf16_f32 v27, v34, v35
	global_store_dwordx4 v[44:45], v[24:27], off offset:256
	v_lshl_add_u64 v[28:29], s[76:77], 0, v[8:9]
	s_waitcnt vmcnt(6)
	v_mov_b32_e32 v24, v242
	v_mov_b32_e32 v25, v243
	v_mov_b32_e32 v26, v244
	v_mov_b32_e32 v27, v245
	v_lshlrev_b32_e32 v8, 16, v24
	v_and_b32_e32 v9, 0xffff0000, v24
	v_lshlrev_b32_e32 v24, 16, v25
	v_and_b32_e32 v25, 0xffff0000, v25
	v_lshlrev_b32_e32 v30, 16, v26
	v_and_b32_e32 v31, 0xffff0000, v26
	v_lshlrev_b32_e32 v26, 16, v27
	v_and_b32_e32 v27, 0xffff0000, v27
	v_pk_fma_f32 v[8:9], v[138:139], v[8:9], v[154:155]
	v_pk_fma_f32 v[24:25], v[140:141], v[24:25], v[150:151]
	v_pk_fma_f32 v[30:31], v[142:143], v[30:31], v[156:157]
	v_pk_fma_f32 v[26:27], v[146:147], v[26:27], v[152:153]
	v_pk_fma_f32 v[8:9], v[20:21], v[14:15], v[8:9]
	v_pk_fma_f32 v[10:11], v[22:23], v[10:11], v[24:25]
	v_pk_fma_f32 v[14:15], v[16:17], v[136:137], v[30:31]
	v_pk_fma_f32 v[12:13], v[18:19], v[12:13], v[26:27]
	v_cvt_pk_bf16_f32 v8, v8, v9
	v_cvt_pk_bf16_f32 v9, v10, v11
	v_cvt_pk_bf16_f32 v10, v14, v15
	v_cvt_pk_bf16_f32 v11, v12, v13
	global_store_dwordx4 v[28:29], v[8:11], off
	s_waitcnt vmcnt(5)
	v_mov_b32_e32 v8, v226
	v_mov_b32_e32 v9, v227
	v_mov_b32_e32 v10, v228
	v_mov_b32_e32 v11, v229
	v_lshlrev_b32_e32 v12, 16, v8
	v_and_b32_e32 v13, 0xffff0000, v8
	v_lshlrev_b32_e32 v8, 16, v9
	v_and_b32_e32 v9, 0xffff0000, v9
	v_lshlrev_b32_e32 v14, 16, v10
	v_and_b32_e32 v15, 0xffff0000, v10
	v_lshlrev_b32_e32 v10, 16, v11
	v_and_b32_e32 v11, 0xffff0000, v11
	v_pk_fma_f32 v[12:13], v[166:167], v[12:13], v[172:173]
	v_pk_fma_f32 v[8:9], v[164:165], v[8:9], v[170:171]
	v_pk_fma_f32 v[14:15], v[160:161], v[14:15], v[168:169]
	v_pk_fma_f32 v[10:11], v[158:159], v[10:11], v[162:163]
	v_pk_fma_f32 v[4:5], v[4:5], v[132:133], v[12:13]
	v_pk_fma_f32 v[6:7], v[6:7], v[130:131], v[8:9]
	v_pk_fma_f32 v[8:9], v[0:1], v[134:135], v[14:15]
	v_pk_fma_f32 v[10:11], v[2:3], v[128:129], v[10:11]
	v_cvt_pk_bf16_f32 v0, v4, v5
	v_cvt_pk_bf16_f32 v1, v6, v7
	v_cvt_pk_bf16_f32 v2, v8, v9
	v_cvt_pk_bf16_f32 v3, v10, v11
	global_store_dwordx4 v[28:29], v[0:3], off offset:256
	s_cbranch_vccnz .LBB0_2129
	s_andn2_b64 vcc, exec, s[6:7]
	s_cbranch_vccnz .LBB0_2128
	s_barrier
	s_branch .LBB0_2128

.LBB0_2144:
	s_cmp_gt_i32 s49, 12
	s_cselect_b64 s[12:13], -1, 0
	s_and_b64 s[0:1], s[10:11], s[12:13]
	s_andn2_b64 vcc, exec, s[0:1]
	s_cbranch_vccnz .LBB0_2302
	s_waitcnt vmcnt(0)
	s_waitcnt vmcnt(0) lgkmcnt(0)
	s_barrier
	s_cmp_lt_u32 s98, 4
	s_cbranch_scc1 .Lipf_a41
	s_getpc_b64 s[100:101]
	v_lshlrev_b32_e32 v251, 1, v250
	v_add_u32_e32 v251, 0xffff8000, v251
	v_min_u32_e32 v251, 0xdb80, v251
	global_load_dword a0, v251, s[100:101]

.LBB0_2335:
	s_cmp_gt_i32 s49, 13
	s_cselect_b64 s[4:5], -1, 0
	s_and_b64 s[0:1], s[14:15], s[4:5]
	s_andn2_b64 vcc, exec, s[0:1]
	s_cbranch_vccnz .LBB0_2397
	s_waitcnt vmcnt(0)
	s_waitcnt vmcnt(0) lgkmcnt(0)
	s_barrier
	s_cmp_lt_u32 s98, 4
	s_cbranch_scc1 .Lipf_a44
	s_getpc_b64 s[100:101]
	v_lshlrev_b32_e32 v251, 1, v250
	v_add_u32_e32 v251, 0xffff8000, v251
	v_min_u32_e32 v251, 0x8800, v251
	global_load_dword a0, v251, s[100:101]

.LBB0_2408:
	s_getpc_b64 s[100:101]
	v_min_u32_e32 v251, 0x7900, v250
	global_load_dword a0, v251, s[100:101]
	s_or_b64 exec, exec, s[14:15]
	v_and_b32_e32 v6, 7, v6
	v_cmp_ne_u32_e32 vcc, 0, v6
	s_and_saveexec_b64 s[14:15], vcc
	s_cbranch_execz .LBB0_2411
	v_lshlrev_b32_e32 v7, 2, v9
	v_lshlrev_b32_e32 v8, 2, v5
	v_add3_u32 v7, v7, v8, 0
	v_add_u32_e32 v7, 0x24380, v7
	s_mov_b64 s[16:17], 0

.LBB0_2411:
	s_getpc_b64 s[100:101]
	v_min_u32_e32 v251, 0x7880, v250
	global_load_dword a0, v251, s[100:101]
	s_or_b64 exec, exec, s[14:15]
	v_and_b32_e32 v1, 0x7ffffffe, v3
	v_cmp_ne_u32_e32 vcc, v3, v1
	s_orn2_b64 s[14:15], vcc, exec

.LBB0_2415:
	s_getpc_b64 s[100:101]
	v_min_u32_e32 v251, 0x7800, v250
	global_load_dword a0, v251, s[100:101]
	s_or_b64 exec, exec, s[0:1]
	v_cmp_eq_u32_e32 vcc, 31, v2
	s_and_b64 exec, exec, vcc
	s_add_i32 s0, 0, 0x24000
	v_mov_b32_e32 v0, s0
	ds_write_b32 v0, v4

.LBB0_2449:
	s_getpc_b64 s[100:101]
	v_min_u32_e32 v251, 0x6880, v250
	global_load_dword a0, v251, s[100:101]
	s_mov_b32 s14, 0
	s_lshl_b32 s14, s31, 2
	s_add_i32 s14, s3, s14
	v_mbcnt_lo_u32_b32 v146, -1, 0
	v_mbcnt_hi_u32_b32 v146, -1, v146
	v_mov_b32_e32 v128, s14
	ds_read2_b32 v[128:129], v128 offset0:64 offset1:224
	v_and_b32_e32 v143, 15, v146
	v_or_b32_e32 v144, s40, v143
	v_mov_b32_e32 v147, 0
	s_waitcnt lgkmcnt(0)
	v_lshlrev_b32_e32 v130, 2, v128
	v_add_u32_e32 v130, s3, v130
	ds_read_b32 v145, v130 offset:4
	v_ashrrev_i32_e32 v133, 31, v128
	v_mov_b32_e32 v132, v128
	v_add_u32_e32 v130, v129, v144
	v_lshlrev_b64 v[132:133], 16, v[132:133]
	s_waitcnt lgkmcnt(0)
	v_cmp_lt_i32_e32 vcc, v130, v145
	v_mov_b32_e32 v128, 0
	v_lshl_add_u64 v[132:133], s[10:11], 0, v[132:133]
	v_ashrrev_i32_e32 v131, 31, v130
	v_bfe_u32 v148, v146, 4, 2
	s_lshl_b32 s14, s56, 7
	v_lshl_add_u64 v[152:153], v[130:131], 2, v[132:133]
	v_lshl_or_b32 v149, v148, 3, s14
	global_load_dword v154, v[152:153], off
	global_load_dword v155, v[152:153], off offset:64
	global_load_dword v156, v[152:153], off offset:128
	global_load_dword v157, v[152:153], off offset:192
	global_load_dword v158, v[152:153], off offset:512
	global_load_dword v159, v[152:153], off offset:576
	global_load_dword v160, v[152:153], off offset:640
	global_load_dword v161, v[152:153], off offset:704
	s_lshl_b32 s14, s31, 8
	v_or_b32_e32 v149, s41, v149
	v_add_u32_e32 v150, s14, v144
	v_lshl_add_u32 v150, v150, 8, v149
	v_cmp_lt_i32_e32 vcc, v130, v145
	s_waitcnt vmcnt(7)
	v_mul_f32_e32 v163, 0x3c800000, v154
	v_mul_f32_e32 v164, 0xbd38aa3b, v124
	v_mul_f32_e32 v165, 0xbd38aa3b, v125
	v_mul_f32_e32 v166, 0xbd38aa3b, v126
	v_mul_f32_e32 v167, 0xbd38aa3b, v127
	v_mul_f32_e32 v168, 0xbd38aa3b, v116
	v_mul_f32_e32 v169, 0xbd38aa3b, v117
	v_mul_f32_e32 v170, 0xbd38aa3b, v118
	v_mul_f32_e32 v171, 0xbd38aa3b, v119
	v_exp_f32_e32 v164, v164
	v_exp_f32_e32 v165, v165
	v_exp_f32_e32 v166, v166
	v_exp_f32_e32 v167, v167
	v_exp_f32_e32 v168, v168
	v_exp_f32_e32 v169, v169
	v_exp_f32_e32 v170, v170
	v_exp_f32_e32 v171, v171
	v_add_f32_e32 v164, 1.0, v164
	v_add_f32_e32 v165, 1.0, v165
	v_add_f32_e32 v166, 1.0, v166
	v_add_f32_e32 v167, 1.0, v167
	v_add_f32_e32 v168, 1.0, v168
	v_add_f32_e32 v169, 1.0, v169
	v_add_f32_e32 v170, 1.0, v170
	v_add_f32_e32 v171, 1.0, v171
	v_rcp_f32_e32 v164, v164
	v_rcp_f32_e32 v165, v165
	v_rcp_f32_e32 v166, v166
	v_rcp_f32_e32 v167, v167
	v_rcp_f32_e32 v168, v168
	v_rcp_f32_e32 v169, v169
	v_rcp_f32_e32 v170, v170
	v_rcp_f32_e32 v171, v171
	v_mul_f32_e32 v164, v124, v164
	v_mul_f32_e32 v165, v125, v165
	v_mul_f32_e32 v166, v126, v166
	v_mul_f32_e32 v167, v127, v167
	v_mul_f32_e32 v168, v116, v168
	v_mul_f32_e32 v169, v117, v169
	v_mul_f32_e32 v170, v118, v170
	v_mul_f32_e32 v171, v119, v171
	v_mul_f32_e32 v164, v164, v120
	v_mul_f32_e32 v165, v165, v121
	v_mul_f32_e32 v166, v166, v122
	v_mul_f32_e32 v167, v167, v123
	v_mul_f32_e32 v168, v168, v112
	v_mul_f32_e32 v169, v169, v113
	v_mul_f32_e32 v170, v170, v114
	v_mul_f32_e32 v171, v171, v115
	v_mul_f32_e32 v164, v164, v163
	v_mul_f32_e32 v165, v165, v163
	v_mul_f32_e32 v166, v166, v163
	v_mul_f32_e32 v167, v167, v163
	v_mul_f32_e32 v168, v168, v163
	v_mul_f32_e32 v169, v169, v163
	v_mul_f32_e32 v170, v170, v163
	v_mul_f32_e32 v171, v171, v163
	v_max_f32_e32 v164, 0xc3e00000, v164
	v_max_f32_e32 v165, 0xc3e00000, v165
	v_max_f32_e32 v166, 0xc3e00000, v166
	v_max_f32_e32 v167, 0xc3e00000, v167
	v_max_f32_e32 v168, 0xc3e00000, v168
	v_max_f32_e32 v169, 0xc3e00000, v169
	v_max_f32_e32 v170, 0xc3e00000, v170
	v_max_f32_e32 v171, 0xc3e00000, v171
	v_min_f32_e32 v164, 0x43e00000, v164
	v_min_f32_e32 v165, 0x43e00000, v165
	v_min_f32_e32 v166, 0x43e00000, v166
	v_min_f32_e32 v167, 0x43e00000, v167
	v_min_f32_e32 v168, 0x43e00000, v168
	v_min_f32_e32 v169, 0x43e00000, v169
	v_min_f32_e32 v170, 0x43e00000, v170
	v_min_f32_e32 v171, 0x43e00000, v171
	v_cndmask_b32_e32 v164, 0, v164, vcc
	v_cndmask_b32_e32 v165, 0, v165, vcc
	v_cndmask_b32_e32 v166, 0, v166, vcc
	v_cndmask_b32_e32 v167, 0, v167, vcc
	v_cndmask_b32_e32 v168, 0, v168, vcc
	v_cndmask_b32_e32 v169, 0, v169, vcc
	v_cndmask_b32_e32 v170, 0, v170, vcc
	v_cndmask_b32_e32 v171, 0, v171, vcc
	v_mov_b32_e32 v188, 0
	v_mov_b32_e32 v189, 0
	v_cvt_pk_fp8_f32 v188, v164, v165
	v_cvt_pk_fp8_f32 v189, v168, v169
	v_mov_b32_e32 v192, v150
	v_cvt_pk_fp8_f32 v188, v166, v167 op_sel:[0,0,1]
	v_cvt_pk_fp8_f32 v189, v170, v171 op_sel:[0,0,1]
	s_nop 1
	global_store_dwordx2 v192, v[188:189], s[12:13] sc1
	v_add_u32_e32 v162, 0x10, v130
	v_cmp_lt_i32_e32 vcc, v162, v145
	s_waitcnt vmcnt(7)
	v_mul_f32_e32 v163, 0x3c800000, v155
	v_mul_f32_e32 v164, 0xbd38aa3b, v108
	v_mul_f32_e32 v165, 0xbd38aa3b, v109
	v_mul_f32_e32 v166, 0xbd38aa3b, v110
	v_mul_f32_e32 v167, 0xbd38aa3b, v111
	v_mul_f32_e32 v168, 0xbd38aa3b, v100
	v_mul_f32_e32 v169, 0xbd38aa3b, v101
	v_mul_f32_e32 v170, 0xbd38aa3b, v102
	v_mul_f32_e32 v171, 0xbd38aa3b, v103
	v_exp_f32_e32 v164, v164
	v_exp_f32_e32 v165, v165
	v_exp_f32_e32 v166, v166
	v_exp_f32_e32 v167, v167
	v_exp_f32_e32 v168, v168
	v_exp_f32_e32 v169, v169
	v_exp_f32_e32 v170, v170
	v_exp_f32_e32 v171, v171
	v_add_f32_e32 v164, 1.0, v164
	v_add_f32_e32 v165, 1.0, v165
	v_add_f32_e32 v166, 1.0, v166
	v_add_f32_e32 v167, 1.0, v167
	v_add_f32_e32 v168, 1.0, v168
	v_add_f32_e32 v169, 1.0, v169
	v_add_f32_e32 v170, 1.0, v170
	v_add_f32_e32 v171, 1.0, v171
	v_rcp_f32_e32 v164, v164
	v_rcp_f32_e32 v165, v165
	v_rcp_f32_e32 v166, v166
	v_rcp_f32_e32 v167, v167
	v_rcp_f32_e32 v168, v168
	v_rcp_f32_e32 v169, v169
	v_rcp_f32_e32 v170, v170
	v_rcp_f32_e32 v171, v171
	v_mul_f32_e32 v164, v108, v164
	v_mul_f32_e32 v165, v109, v165
	v_mul_f32_e32 v166, v110, v166
	v_mul_f32_e32 v167, v111, v167
	v_mul_f32_e32 v168, v100, v168
	v_mul_f32_e32 v169, v101, v169
	v_mul_f32_e32 v170, v102, v170
	v_mul_f32_e32 v171, v103, v171
	v_mul_f32_e32 v164, v164, v104
	v_mul_f32_e32 v165, v165, v105
	v_mul_f32_e32 v166, v166, v106
	v_mul_f32_e32 v167, v167, v107
	v_mul_f32_e32 v168, v168, v96
	v_mul_f32_e32 v169, v169, v97
	v_mul_f32_e32 v170, v170, v98
	v_mul_f32_e32 v171, v171, v99
	v_mul_f32_e32 v164, v164, v163
	v_mul_f32_e32 v165, v165, v163
	v_mul_f32_e32 v166, v166, v163
	v_mul_f32_e32 v167, v167, v163
	v_mul_f32_e32 v168, v168, v163
	v_mul_f32_e32 v169, v169, v163
	v_mul_f32_e32 v170, v170, v163
	v_mul_f32_e32 v171, v171, v163
	v_max_f32_e32 v164, 0xc3e00000, v164
	v_max_f32_e32 v165, 0xc3e00000, v165
	v_max_f32_e32 v166, 0xc3e00000, v166
	v_max_f32_e32 v167, 0xc3e00000, v167
	v_max_f32_e32 v168, 0xc3e00000, v168
	v_max_f32_e32 v169, 0xc3e00000, v169
	v_max_f32_e32 v170, 0xc3e00000, v170
	v_max_f32_e32 v171, 0xc3e00000, v171
	v_min_f32_e32 v164, 0x43e00000, v164
	v_min_f32_e32 v165, 0x43e00000, v165
	v_min_f32_e32 v166, 0x43e00000, v166
	v_min_f32_e32 v167, 0x43e00000, v167
	v_min_f32_e32 v168, 0x43e00000, v168
	v_min_f32_e32 v169, 0x43e00000, v169
	v_min_f32_e32 v170, 0x43e00000, v170
	v_min_f32_e32 v171, 0x43e00000, v171
	v_cndmask_b32_e32 v164, 0, v164, vcc
	v_cndmask_b32_e32 v165, 0, v165, vcc
	v_cndmask_b32_e32 v166, 0, v166, vcc
	v_cndmask_b32_e32 v167, 0, v167, vcc
	v_cndmask_b32_e32 v168, 0, v168, vcc
	v_cndmask_b32_e32 v169, 0, v169, vcc
	v_cndmask_b32_e32 v170, 0, v170, vcc
	v_cndmask_b32_e32 v171, 0, v171, vcc
	v_mov_b32_e32 v190, 0
	v_mov_b32_e32 v191, 0
	v_cvt_pk_fp8_f32 v190, v164, v165
	v_cvt_pk_fp8_f32 v191, v168, v169
	v_add_u32_e32 v192, 0x1000, v150
	v_cvt_pk_fp8_f32 v190, v166, v167 op_sel:[0,0,1]
	v_cvt_pk_fp8_f32 v191, v170, v171 op_sel:[0,0,1]
	s_nop 1
	global_store_dwordx2 v192, v[190:191], s[12:13] sc1
	v_add_u32_e32 v162, 0x20, v130
	v_cmp_lt_i32_e32 vcc, v162, v145
	s_waitcnt vmcnt(7)
	v_mul_f32_e32 v163, 0x3c800000, v156
	v_mul_f32_e32 v164, 0xbd38aa3b, v92
	v_mul_f32_e32 v165, 0xbd38aa3b, v93
	v_mul_f32_e32 v166, 0xbd38aa3b, v94
	v_mul_f32_e32 v167, 0xbd38aa3b, v95
	v_mul_f32_e32 v168, 0xbd38aa3b, v84
	v_mul_f32_e32 v169, 0xbd38aa3b, v85
	v_mul_f32_e32 v170, 0xbd38aa3b, v86
	v_mul_f32_e32 v171, 0xbd38aa3b, v87
	v_exp_f32_e32 v164, v164
	v_exp_f32_e32 v165, v165
	v_exp_f32_e32 v166, v166
	v_exp_f32_e32 v167, v167
	v_exp_f32_e32 v168, v168
	v_exp_f32_e32 v169, v169
	v_exp_f32_e32 v170, v170
	v_exp_f32_e32 v171, v171
	v_add_f32_e32 v164, 1.0, v164
	v_add_f32_e32 v165, 1.0, v165
	v_add_f32_e32 v166, 1.0, v166
	v_add_f32_e32 v167, 1.0, v167
	v_add_f32_e32 v168, 1.0, v168
	v_add_f32_e32 v169, 1.0, v169
	v_add_f32_e32 v170, 1.0, v170
	v_add_f32_e32 v171, 1.0, v171
	v_rcp_f32_e32 v164, v164
	v_rcp_f32_e32 v165, v165
	v_rcp_f32_e32 v166, v166
	v_rcp_f32_e32 v167, v167
	v_rcp_f32_e32 v168, v168
	v_rcp_f32_e32 v169, v169
	v_rcp_f32_e32 v170, v170
	v_rcp_f32_e32 v171, v171
	v_mul_f32_e32 v164, v92, v164
	v_mul_f32_e32 v165, v93, v165
	v_mul_f32_e32 v166, v94, v166
	v_mul_f32_e32 v167, v95, v167
	v_mul_f32_e32 v168, v84, v168
	v_mul_f32_e32 v169, v85, v169
	v_mul_f32_e32 v170, v86, v170
	v_mul_f32_e32 v171, v87, v171
	v_mul_f32_e32 v164, v164, v88
	v_mul_f32_e32 v165, v165, v89
	v_mul_f32_e32 v166, v166, v90
	v_mul_f32_e32 v167, v167, v91
	v_mul_f32_e32 v168, v168, v80
	v_mul_f32_e32 v169, v169, v81
	v_mul_f32_e32 v170, v170, v82
	v_mul_f32_e32 v171, v171, v83
	v_mul_f32_e32 v164, v164, v163
	v_mul_f32_e32 v165, v165, v163
	v_mul_f32_e32 v166, v166, v163
	v_mul_f32_e32 v167, v167, v163
	v_mul_f32_e32 v168, v168, v163
	v_mul_f32_e32 v169, v169, v163
	v_mul_f32_e32 v170, v170, v163
	v_mul_f32_e32 v171, v171, v163
	v_max_f32_e32 v164, 0xc3e00000, v164
	v_max_f32_e32 v165, 0xc3e00000, v165
	v_max_f32_e32 v166, 0xc3e00000, v166
	v_max_f32_e32 v167, 0xc3e00000, v167
	v_max_f32_e32 v168, 0xc3e00000, v168
	v_max_f32_e32 v169, 0xc3e00000, v169
	v_max_f32_e32 v170, 0xc3e00000, v170
	v_max_f32_e32 v171, 0xc3e00000, v171
	v_min_f32_e32 v164, 0x43e00000, v164
	v_min_f32_e32 v165, 0x43e00000, v165
	v_min_f32_e32 v166, 0x43e00000, v166
	v_min_f32_e32 v167, 0x43e00000, v167
	v_min_f32_e32 v168, 0x43e00000, v168
	v_min_f32_e32 v169, 0x43e00000, v169
	v_min_f32_e32 v170, 0x43e00000, v170
	v_min_f32_e32 v171, 0x43e00000, v171
	v_cndmask_b32_e32 v164, 0, v164, vcc
	v_cndmask_b32_e32 v165, 0, v165, vcc
	v_cndmask_b32_e32 v166, 0, v166, vcc
	v_cndmask_b32_e32 v167, 0, v167, vcc
	v_cndmask_b32_e32 v168, 0, v168, vcc
	v_cndmask_b32_e32 v169, 0, v169, vcc
	v_cndmask_b32_e32 v170, 0, v170, vcc
	v_cndmask_b32_e32 v171, 0, v171, vcc
	v_mov_b32_e32 v188, 0
	v_mov_b32_e32 v189, 0
	v_cvt_pk_fp8_f32 v188, v164, v165
	v_cvt_pk_fp8_f32 v189, v168, v169
	v_add_u32_e32 v192, 0x2000, v150
	v_cvt_pk_fp8_f32 v188, v166, v167 op_sel:[0,0,1]
	v_cvt_pk_fp8_f32 v189, v170, v171 op_sel:[0,0,1]
	s_nop 1
	global_store_dwordx2 v192, v[188:189], s[12:13] sc1
	v_add_u32_e32 v162, 0x30, v130
	v_cmp_lt_i32_e32 vcc, v162, v145
	s_waitcnt vmcnt(7)
	v_mul_f32_e32 v163, 0x3c800000, v157
	v_mul_f32_e32 v164, 0xbd38aa3b, v76
	v_mul_f32_e32 v165, 0xbd38aa3b, v77
	v_mul_f32_e32 v166, 0xbd38aa3b, v78
	v_mul_f32_e32 v167, 0xbd38aa3b, v79
	v_mul_f32_e32 v168, 0xbd38aa3b, v68
	v_mul_f32_e32 v169, 0xbd38aa3b, v69
	v_mul_f32_e32 v170, 0xbd38aa3b, v70
	v_mul_f32_e32 v171, 0xbd38aa3b, v71
	v_exp_f32_e32 v164, v164
	v_exp_f32_e32 v165, v165
	v_exp_f32_e32 v166, v166
	v_exp_f32_e32 v167, v167
	v_exp_f32_e32 v168, v168
	v_exp_f32_e32 v169, v169
	v_exp_f32_e32 v170, v170
	v_exp_f32_e32 v171, v171
	v_add_f32_e32 v164, 1.0, v164
	v_add_f32_e32 v165, 1.0, v165
	v_add_f32_e32 v166, 1.0, v166
	v_add_f32_e32 v167, 1.0, v167
	v_add_f32_e32 v168, 1.0, v168
	v_add_f32_e32 v169, 1.0, v169
	v_add_f32_e32 v170, 1.0, v170
	v_add_f32_e32 v171, 1.0, v171
	v_rcp_f32_e32 v164, v164
	v_rcp_f32_e32 v165, v165
	v_rcp_f32_e32 v166, v166
	v_rcp_f32_e32 v167, v167
	v_rcp_f32_e32 v168, v168
	v_rcp_f32_e32 v169, v169
	v_rcp_f32_e32 v170, v170
	v_rcp_f32_e32 v171, v171
	v_mul_f32_e32 v164, v76, v164
	v_mul_f32_e32 v165, v77, v165
	v_mul_f32_e32 v166, v78, v166
	v_mul_f32_e32 v167, v79, v167
	v_mul_f32_e32 v168, v68, v168
	v_mul_f32_e32 v169, v69, v169
	v_mul_f32_e32 v170, v70, v170
	v_mul_f32_e32 v171, v71, v171
	v_mul_f32_e32 v164, v164, v72
	v_mul_f32_e32 v165, v165, v73
	v_mul_f32_e32 v166, v166, v74
	v_mul_f32_e32 v167, v167, v75
	v_mul_f32_e32 v168, v168, v64
	v_mul_f32_e32 v169, v169, v65
	v_mul_f32_e32 v170, v170, v66
	v_mul_f32_e32 v171, v171, v67
	v_mul_f32_e32 v164, v164, v163
	v_mul_f32_e32 v165, v165, v163
	v_mul_f32_e32 v166, v166, v163
	v_mul_f32_e32 v167, v167, v163
	v_mul_f32_e32 v168, v168, v163
	v_mul_f32_e32 v169, v169, v163
	v_mul_f32_e32 v170, v170, v163
	v_mul_f32_e32 v171, v171, v163
	v_max_f32_e32 v164, 0xc3e00000, v164
	v_max_f32_e32 v165, 0xc3e00000, v165
	v_max_f32_e32 v166, 0xc3e00000, v166
	v_max_f32_e32 v167, 0xc3e00000, v167
	v_max_f32_e32 v168, 0xc3e00000, v168
	v_max_f32_e32 v169, 0xc3e00000, v169
	v_max_f32_e32 v170, 0xc3e00000, v170
	v_max_f32_e32 v171, 0xc3e00000, v171
	v_min_f32_e32 v164, 0x43e00000, v164
	v_min_f32_e32 v165, 0x43e00000, v165
	v_min_f32_e32 v166, 0x43e00000, v166
	v_min_f32_e32 v167, 0x43e00000, v167
	v_min_f32_e32 v168, 0x43e00000, v168
	v_min_f32_e32 v169, 0x43e00000, v169
	v_min_f32_e32 v170, 0x43e00000, v170
	v_min_f32_e32 v171, 0x43e00000, v171
	v_cndmask_b32_e32 v164, 0, v164, vcc
	v_cndmask_b32_e32 v165, 0, v165, vcc
	v_cndmask_b32_e32 v166, 0, v166, vcc
	v_cndmask_b32_e32 v167, 0, v167, vcc
	v_cndmask_b32_e32 v168, 0, v168, vcc
	v_cndmask_b32_e32 v169, 0, v169, vcc
	v_cndmask_b32_e32 v170, 0, v170, vcc
	v_cndmask_b32_e32 v171, 0, v171, vcc
	v_mov_b32_e32 v190, 0
	v_mov_b32_e32 v191, 0
	v_cvt_pk_fp8_f32 v190, v164, v165
	v_cvt_pk_fp8_f32 v191, v168, v169
	v_add_u32_e32 v192, 0x3000, v150
	v_cvt_pk_fp8_f32 v190, v166, v167 op_sel:[0,0,1]
	v_cvt_pk_fp8_f32 v191, v170, v171 op_sel:[0,0,1]
	s_nop 1
	global_store_dwordx2 v192, v[190:191], s[12:13] sc1
	v_add_u32_e32 v162, 0x80, v130
	v_cmp_lt_i32_e32 vcc, v162, v145
	s_waitcnt vmcnt(7)
	v_mul_f32_e32 v163, 0x3c800000, v158
	v_mul_f32_e32 v164, 0xbd38aa3b, v60
	v_mul_f32_e32 v165, 0xbd38aa3b, v61
	v_mul_f32_e32 v166, 0xbd38aa3b, v62
	v_mul_f32_e32 v167, 0xbd38aa3b, v63
	v_mul_f32_e32 v168, 0xbd38aa3b, v52
	v_mul_f32_e32 v169, 0xbd38aa3b, v53
	v_mul_f32_e32 v170, 0xbd38aa3b, v54
	v_mul_f32_e32 v171, 0xbd38aa3b, v55
	v_exp_f32_e32 v164, v164
	v_exp_f32_e32 v165, v165
	v_exp_f32_e32 v166, v166
	v_exp_f32_e32 v167, v167
	v_exp_f32_e32 v168, v168
	v_exp_f32_e32 v169, v169
	v_exp_f32_e32 v170, v170
	v_exp_f32_e32 v171, v171
	v_add_f32_e32 v164, 1.0, v164
	v_add_f32_e32 v165, 1.0, v165
	v_add_f32_e32 v166, 1.0, v166
	v_add_f32_e32 v167, 1.0, v167
	v_add_f32_e32 v168, 1.0, v168
	v_add_f32_e32 v169, 1.0, v169
	v_add_f32_e32 v170, 1.0, v170
	v_add_f32_e32 v171, 1.0, v171
	v_rcp_f32_e32 v164, v164
	v_rcp_f32_e32 v165, v165
	v_rcp_f32_e32 v166, v166
	v_rcp_f32_e32 v167, v167
	v_rcp_f32_e32 v168, v168
	v_rcp_f32_e32 v169, v169
	v_rcp_f32_e32 v170, v170
	v_rcp_f32_e32 v171, v171
	v_mul_f32_e32 v164, v60, v164
	v_mul_f32_e32 v165, v61, v165
	v_mul_f32_e32 v166, v62, v166
	v_mul_f32_e32 v167, v63, v167
	v_mul_f32_e32 v168, v52, v168
	v_mul_f32_e32 v169, v53, v169
	v_mul_f32_e32 v170, v54, v170
	v_mul_f32_e32 v171, v55, v171
	v_mul_f32_e32 v164, v164, v56
	v_mul_f32_e32 v165, v165, v57
	v_mul_f32_e32 v166, v166, v58
	v_mul_f32_e32 v167, v167, v59
	v_mul_f32_e32 v168, v168, v48
	v_mul_f32_e32 v169, v169, v49
	v_mul_f32_e32 v170, v170, v50
	v_mul_f32_e32 v171, v171, v51
	v_mul_f32_e32 v164, v164, v163
	v_mul_f32_e32 v165, v165, v163
	v_mul_f32_e32 v166, v166, v163
	v_mul_f32_e32 v167, v167, v163
	v_mul_f32_e32 v168, v168, v163
	v_mul_f32_e32 v169, v169, v163
	v_mul_f32_e32 v170, v170, v163
	v_mul_f32_e32 v171, v171, v163
	v_max_f32_e32 v164, 0xc3e00000, v164
	v_max_f32_e32 v165, 0xc3e00000, v165
	v_max_f32_e32 v166, 0xc3e00000, v166
	v_max_f32_e32 v167, 0xc3e00000, v167
	v_max_f32_e32 v168, 0xc3e00000, v168
	v_max_f32_e32 v169, 0xc3e00000, v169
	v_max_f32_e32 v170, 0xc3e00000, v170
	v_max_f32_e32 v171, 0xc3e00000, v171
	v_min_f32_e32 v164, 0x43e00000, v164
	v_min_f32_e32 v165, 0x43e00000, v165
	v_min_f32_e32 v166, 0x43e00000, v166
	v_min_f32_e32 v167, 0x43e00000, v167
	v_min_f32_e32 v168, 0x43e00000, v168
	v_min_f32_e32 v169, 0x43e00000, v169
	v_min_f32_e32 v170, 0x43e00000, v170
	v_min_f32_e32 v171, 0x43e00000, v171
	v_cndmask_b32_e32 v164, 0, v164, vcc
	v_cndmask_b32_e32 v165, 0, v165, vcc
	v_cndmask_b32_e32 v166, 0, v166, vcc
	v_cndmask_b32_e32 v167, 0, v167, vcc
	v_cndmask_b32_e32 v168, 0, v168, vcc
	v_cndmask_b32_e32 v169, 0, v169, vcc
	v_cndmask_b32_e32 v170, 0, v170, vcc
	v_cndmask_b32_e32 v171, 0, v171, vcc
	v_mov_b32_e32 v188, 0
	v_mov_b32_e32 v189, 0
	v_cvt_pk_fp8_f32 v188, v164, v165
	v_cvt_pk_fp8_f32 v189, v168, v169
	v_add_u32_e32 v192, 0x8000, v150
	v_cvt_pk_fp8_f32 v188, v166, v167 op_sel:[0,0,1]
	v_cvt_pk_fp8_f32 v189, v170, v171 op_sel:[0,0,1]
	s_nop 1
	global_store_dwordx2 v192, v[188:189], s[12:13] sc1
	v_add_u32_e32 v162, 0x90, v130
	v_cmp_lt_i32_e32 vcc, v162, v145
	s_waitcnt vmcnt(7)
	v_mul_f32_e32 v163, 0x3c800000, v159
	v_mul_f32_e32 v164, 0xbd38aa3b, v44
	v_mul_f32_e32 v165, 0xbd38aa3b, v45
	v_mul_f32_e32 v166, 0xbd38aa3b, v46
	v_mul_f32_e32 v167, 0xbd38aa3b, v47
	v_mul_f32_e32 v168, 0xbd38aa3b, v36
	v_mul_f32_e32 v169, 0xbd38aa3b, v37
	v_mul_f32_e32 v170, 0xbd38aa3b, v38
	v_mul_f32_e32 v171, 0xbd38aa3b, v39
	v_exp_f32_e32 v164, v164
	v_exp_f32_e32 v165, v165
	v_exp_f32_e32 v166, v166
	v_exp_f32_e32 v167, v167
	v_exp_f32_e32 v168, v168
	v_exp_f32_e32 v169, v169
	v_exp_f32_e32 v170, v170
	v_exp_f32_e32 v171, v171
	v_add_f32_e32 v164, 1.0, v164
	v_add_f32_e32 v165, 1.0, v165
	v_add_f32_e32 v166, 1.0, v166
	v_add_f32_e32 v167, 1.0, v167
	v_add_f32_e32 v168, 1.0, v168
	v_add_f32_e32 v169, 1.0, v169
	v_add_f32_e32 v170, 1.0, v170
	v_add_f32_e32 v171, 1.0, v171
	v_rcp_f32_e32 v164, v164
	v_rcp_f32_e32 v165, v165
	v_rcp_f32_e32 v166, v166
	v_rcp_f32_e32 v167, v167
	v_rcp_f32_e32 v168, v168
	v_rcp_f32_e32 v169, v169
	v_rcp_f32_e32 v170, v170
	v_rcp_f32_e32 v171, v171
	v_mul_f32_e32 v164, v44, v164
	v_mul_f32_e32 v165, v45, v165
	v_mul_f32_e32 v166, v46, v166
	v_mul_f32_e32 v167, v47, v167
	v_mul_f32_e32 v168, v36, v168
	v_mul_f32_e32 v169, v37, v169
	v_mul_f32_e32 v170, v38, v170
	v_mul_f32_e32 v171, v39, v171
	v_mul_f32_e32 v164, v164, v40
	v_mul_f32_e32 v165, v165, v41
	v_mul_f32_e32 v166, v166, v42
	v_mul_f32_e32 v167, v167, v43
	v_mul_f32_e32 v168, v168, v32
	v_mul_f32_e32 v169, v169, v33
	v_mul_f32_e32 v170, v170, v34
	v_mul_f32_e32 v171, v171, v35
	v_mul_f32_e32 v164, v164, v163
	v_mul_f32_e32 v165, v165, v163
	v_mul_f32_e32 v166, v166, v163
	v_mul_f32_e32 v167, v167, v163
	v_mul_f32_e32 v168, v168, v163
	v_mul_f32_e32 v169, v169, v163
	v_mul_f32_e32 v170, v170, v163
	v_mul_f32_e32 v171, v171, v163
	v_max_f32_e32 v164, 0xc3e00000, v164
	v_max_f32_e32 v165, 0xc3e00000, v165
	v_max_f32_e32 v166, 0xc3e00000, v166
	v_max_f32_e32 v167, 0xc3e00000, v167
	v_max_f32_e32 v168, 0xc3e00000, v168
	v_max_f32_e32 v169, 0xc3e00000, v169
	v_max_f32_e32 v170, 0xc3e00000, v170
	v_max_f32_e32 v171, 0xc3e00000, v171
	v_min_f32_e32 v164, 0x43e00000, v164
	v_min_f32_e32 v165, 0x43e00000, v165
	v_min_f32_e32 v166, 0x43e00000, v166
	v_min_f32_e32 v167, 0x43e00000, v167
	v_min_f32_e32 v168, 0x43e00000, v168
	v_min_f32_e32 v169, 0x43e00000, v169
	v_min_f32_e32 v170, 0x43e00000, v170
	v_min_f32_e32 v171, 0x43e00000, v171
	v_cndmask_b32_e32 v164, 0, v164, vcc
	v_cndmask_b32_e32 v165, 0, v165, vcc
	v_cndmask_b32_e32 v166, 0, v166, vcc
	v_cndmask_b32_e32 v167, 0, v167, vcc
	v_cndmask_b32_e32 v168, 0, v168, vcc
	v_cndmask_b32_e32 v169, 0, v169, vcc
	v_cndmask_b32_e32 v170, 0, v170, vcc
	v_cndmask_b32_e32 v171, 0, v171, vcc
	v_mov_b32_e32 v190, 0
	v_mov_b32_e32 v191, 0
	v_cvt_pk_fp8_f32 v190, v164, v165
	v_cvt_pk_fp8_f32 v191, v168, v169
	v_add_u32_e32 v192, 0x9000, v150
	v_cvt_pk_fp8_f32 v190, v166, v167 op_sel:[0,0,1]
	v_cvt_pk_fp8_f32 v191, v170, v171 op_sel:[0,0,1]
	s_nop 1
	global_store_dwordx2 v192, v[190:191], s[12:13] sc1
	v_add_u32_e32 v162, 0xa0, v130
	v_cmp_lt_i32_e32 vcc, v162, v145
	s_waitcnt vmcnt(7)
	v_mul_f32_e32 v163, 0x3c800000, v160
	v_mul_f32_e32 v164, 0xbd38aa3b, v28
	v_mul_f32_e32 v165, 0xbd38aa3b, v29
	v_mul_f32_e32 v166, 0xbd38aa3b, v30
	v_mul_f32_e32 v167, 0xbd38aa3b, v31
	v_mul_f32_e32 v168, 0xbd38aa3b, v20
	v_mul_f32_e32 v169, 0xbd38aa3b, v21
	v_mul_f32_e32 v170, 0xbd38aa3b, v22
	v_mul_f32_e32 v171, 0xbd38aa3b, v23
	v_exp_f32_e32 v164, v164
	v_exp_f32_e32 v165, v165
	v_exp_f32_e32 v166, v166
	v_exp_f32_e32 v167, v167
	v_exp_f32_e32 v168, v168
	v_exp_f32_e32 v169, v169
	v_exp_f32_e32 v170, v170
	v_exp_f32_e32 v171, v171
	v_add_f32_e32 v164, 1.0, v164
	v_add_f32_e32 v165, 1.0, v165
	v_add_f32_e32 v166, 1.0, v166
	v_add_f32_e32 v167, 1.0, v167
	v_add_f32_e32 v168, 1.0, v168
	v_add_f32_e32 v169, 1.0, v169
	v_add_f32_e32 v170, 1.0, v170
	v_add_f32_e32 v171, 1.0, v171
	v_rcp_f32_e32 v164, v164
	v_rcp_f32_e32 v165, v165
	v_rcp_f32_e32 v166, v166
	v_rcp_f32_e32 v167, v167
	v_rcp_f32_e32 v168, v168
	v_rcp_f32_e32 v169, v169
	v_rcp_f32_e32 v170, v170
	v_rcp_f32_e32 v171, v171
	v_mul_f32_e32 v164, v28, v164
	v_mul_f32_e32 v165, v29, v165
	v_mul_f32_e32 v166, v30, v166
	v_mul_f32_e32 v167, v31, v167
	v_mul_f32_e32 v168, v20, v168
	v_mul_f32_e32 v169, v21, v169
	v_mul_f32_e32 v170, v22, v170
	v_mul_f32_e32 v171, v23, v171
	v_mul_f32_e32 v164, v164, v24
	v_mul_f32_e32 v165, v165, v25
	v_mul_f32_e32 v166, v166, v26
	v_mul_f32_e32 v167, v167, v27
	v_mul_f32_e32 v168, v168, v16
	v_mul_f32_e32 v169, v169, v17
	v_mul_f32_e32 v170, v170, v18
	v_mul_f32_e32 v171, v171, v19
	v_mul_f32_e32 v164, v164, v163
	v_mul_f32_e32 v165, v165, v163
	v_mul_f32_e32 v166, v166, v163
	v_mul_f32_e32 v167, v167, v163
	v_mul_f32_e32 v168, v168, v163
	v_mul_f32_e32 v169, v169, v163
	v_mul_f32_e32 v170, v170, v163
	v_mul_f32_e32 v171, v171, v163
	v_max_f32_e32 v164, 0xc3e00000, v164
	v_max_f32_e32 v165, 0xc3e00000, v165
	v_max_f32_e32 v166, 0xc3e00000, v166
	v_max_f32_e32 v167, 0xc3e00000, v167
	v_max_f32_e32 v168, 0xc3e00000, v168
	v_max_f32_e32 v169, 0xc3e00000, v169
	v_max_f32_e32 v170, 0xc3e00000, v170
	v_max_f32_e32 v171, 0xc3e00000, v171
	v_min_f32_e32 v164, 0x43e00000, v164
	v_min_f32_e32 v165, 0x43e00000, v165
	v_min_f32_e32 v166, 0x43e00000, v166
	v_min_f32_e32 v167, 0x43e00000, v167
	v_min_f32_e32 v168, 0x43e00000, v168
	v_min_f32_e32 v169, 0x43e00000, v169
	v_min_f32_e32 v170, 0x43e00000, v170
	v_min_f32_e32 v171, 0x43e00000, v171
	v_cndmask_b32_e32 v164, 0, v164, vcc
	v_cndmask_b32_e32 v165, 0, v165, vcc
	v_cndmask_b32_e32 v166, 0, v166, vcc
	v_cndmask_b32_e32 v167, 0, v167, vcc
	v_cndmask_b32_e32 v168, 0, v168, vcc
	v_cndmask_b32_e32 v169, 0, v169, vcc
	v_cndmask_b32_e32 v170, 0, v170, vcc
	v_cndmask_b32_e32 v171, 0, v171, vcc
	v_mov_b32_e32 v188, 0
	v_mov_b32_e32 v189, 0
	v_cvt_pk_fp8_f32 v188, v164, v165
	v_cvt_pk_fp8_f32 v189, v168, v169
	v_add_u32_e32 v192, 0xa000, v150
	v_cvt_pk_fp8_f32 v188, v166, v167 op_sel:[0,0,1]
	v_cvt_pk_fp8_f32 v189, v170, v171 op_sel:[0,0,1]
	s_nop 1
	global_store_dwordx2 v192, v[188:189], s[12:13] sc1
	v_add_u32_e32 v162, 0xb0, v130
	v_cmp_lt_i32_e32 vcc, v162, v145
	s_waitcnt vmcnt(7)
	v_mul_f32_e32 v163, 0x3c800000, v161
	v_mul_f32_e32 v164, 0xbd38aa3b, v12
	v_mul_f32_e32 v165, 0xbd38aa3b, v13
	v_mul_f32_e32 v166, 0xbd38aa3b, v14
	v_mul_f32_e32 v167, 0xbd38aa3b, v15
	v_mul_f32_e32 v168, 0xbd38aa3b, v4
	v_mul_f32_e32 v169, 0xbd38aa3b, v5
	v_mul_f32_e32 v170, 0xbd38aa3b, v6
	v_mul_f32_e32 v171, 0xbd38aa3b, v7
	v_exp_f32_e32 v164, v164
	v_exp_f32_e32 v165, v165
	v_exp_f32_e32 v166, v166
	v_exp_f32_e32 v167, v167
	v_exp_f32_e32 v168, v168
	v_exp_f32_e32 v169, v169
	v_exp_f32_e32 v170, v170
	v_exp_f32_e32 v171, v171
	v_add_f32_e32 v164, 1.0, v164
	v_add_f32_e32 v165, 1.0, v165
	v_add_f32_e32 v166, 1.0, v166
	v_add_f32_e32 v167, 1.0, v167
	v_add_f32_e32 v168, 1.0, v168
	v_add_f32_e32 v169, 1.0, v169
	v_add_f32_e32 v170, 1.0, v170
	v_add_f32_e32 v171, 1.0, v171
	v_rcp_f32_e32 v164, v164
	v_rcp_f32_e32 v165, v165
	v_rcp_f32_e32 v166, v166
	v_rcp_f32_e32 v167, v167
	v_rcp_f32_e32 v168, v168
	v_rcp_f32_e32 v169, v169
	v_rcp_f32_e32 v170, v170
	v_rcp_f32_e32 v171, v171
	v_mul_f32_e32 v164, v12, v164
	v_mul_f32_e32 v165, v13, v165
	v_mul_f32_e32 v166, v14, v166
	v_mul_f32_e32 v167, v15, v167
	v_mul_f32_e32 v168, v4, v168
	v_mul_f32_e32 v169, v5, v169
	v_mul_f32_e32 v170, v6, v170
	v_mul_f32_e32 v171, v7, v171
	v_mul_f32_e32 v164, v164, v8
	v_mul_f32_e32 v165, v165, v9
	v_mul_f32_e32 v166, v166, v10
	v_mul_f32_e32 v167, v167, v11
	v_mul_f32_e32 v168, v168, v0
	v_mul_f32_e32 v169, v169, v1
	v_mul_f32_e32 v170, v170, v2
	v_mul_f32_e32 v171, v171, v3
	v_mul_f32_e32 v164, v164, v163
	v_mul_f32_e32 v165, v165, v163
	v_mul_f32_e32 v166, v166, v163
	v_mul_f32_e32 v167, v167, v163
	v_mul_f32_e32 v168, v168, v163
	v_mul_f32_e32 v169, v169, v163
	v_mul_f32_e32 v170, v170, v163
	v_mul_f32_e32 v171, v171, v163
	v_max_f32_e32 v164, 0xc3e00000, v164
	v_max_f32_e32 v165, 0xc3e00000, v165
	v_max_f32_e32 v166, 0xc3e00000, v166
	v_max_f32_e32 v167, 0xc3e00000, v167
	v_max_f32_e32 v168, 0xc3e00000, v168
	v_max_f32_e32 v169, 0xc3e00000, v169
	v_max_f32_e32 v170, 0xc3e00000, v170
	v_max_f32_e32 v171, 0xc3e00000, v171
	v_min_f32_e32 v164, 0x43e00000, v164
	v_min_f32_e32 v165, 0x43e00000, v165
	v_min_f32_e32 v166, 0x43e00000, v166
	v_min_f32_e32 v167, 0x43e00000, v167
	v_min_f32_e32 v168, 0x43e00000, v168
	v_min_f32_e32 v169, 0x43e00000, v169
	v_min_f32_e32 v170, 0x43e00000, v170
	v_min_f32_e32 v171, 0x43e00000, v171
	v_cndmask_b32_e32 v164, 0, v164, vcc
	v_cndmask_b32_e32 v165, 0, v165, vcc
	v_cndmask_b32_e32 v166, 0, v166, vcc
	v_cndmask_b32_e32 v167, 0, v167, vcc
	v_cndmask_b32_e32 v168, 0, v168, vcc
	v_cndmask_b32_e32 v169, 0, v169, vcc
	v_cndmask_b32_e32 v170, 0, v170, vcc
	v_cndmask_b32_e32 v171, 0, v171, vcc
	v_mov_b32_e32 v190, 0
	v_mov_b32_e32 v191, 0
	v_cvt_pk_fp8_f32 v190, v164, v165
	v_cvt_pk_fp8_f32 v191, v168, v169
	v_add_u32_e32 v192, 0xb000, v150
	v_cvt_pk_fp8_f32 v190, v166, v167 op_sel:[0,0,1]
	v_cvt_pk_fp8_f32 v191, v170, v171 op_sel:[0,0,1]
	s_nop 1
	global_store_dwordx2 v192, v[190:191], s[12:13] sc1
	v_bfe_u32 v114, v146, 4, 2
	s_waitcnt vmcnt(0)
	v_or_b32_e32 v0, v114, v143
	v_cmp_eq_u32_e32 vcc, 0, v0
	s_and_saveexec_b64 s[22:23], vcc
	s_cbranch_execz .LBB0_2596
	s_mov_b64 s[24:25], exec
	v_mbcnt_lo_u32_b32 v0, s24, 0
	v_mbcnt_hi_u32_b32 v0, s25, v0
	v_cmp_eq_u32_e32 vcc, 0, v0
	s_and_b64 s[26:27], exec, vcc
	s_mov_b64 exec, s[26:27]
	s_cbranch_execz .LBB0_2596
	s_lshl_b32 s26, s31, 5
	s_ashr_i32 s27, s26, 31
	s_lshl_b64 s[26:27], s[26:27], 2
	s_add_u32 s26, s48, s26
	s_addc_u32 s27, s49, s27
	s_bcnt1_i32_b64 s14, s[24:25]
	s_lshl_b32 s14, s14, 1
	v_mov_b32_e32 v0, s14
	global_atomic_add v140, v0, s[26:27]

.LBB0_2611:
	s_getpc_b64 s[100:101]
	v_min_u32_e32 v251, 0x4e80, v250
	global_load_dword a0, v251, s[100:101]
	s_lshl_b32 s0, s18, 2
	s_add_i32 s0, s3, s0
	v_mbcnt_lo_u32_b32 v72, -1, 0
	v_mbcnt_hi_u32_b32 v72, -1, v72
	v_mov_b32_e32 v64, s0
	ds_read2_b32 v[64:65], v64 offset0:64 offset1:224
	s_lshl_b32 s0, s20, 7
	v_and_b32_e32 v70, 15, v72
	s_add_i32 s0, s0, s24
	v_or_b32_e32 v71, s0, v70
	s_waitcnt lgkmcnt(0)
	v_ashrrev_i32_e32 v67, 31, v64
	v_mov_b32_e32 v66, v64
	v_lshlrev_b32_e32 v64, 2, v64
	v_add_u32_e32 v64, s3, v64
	ds_read_b32 v64, v64 offset:4
	v_lshlrev_b64 v[68:69], 16, v[66:67]
	v_add_u32_e32 v66, v65, v71
	v_mov_b32_e32 v73, 0
	v_lshl_add_u64 v[68:69], s[10:11], 0, v[68:69]
	s_waitcnt lgkmcnt(0)
	v_cmp_lt_i32_e32 vcc, v66, v64
	v_ashrrev_i32_e32 v67, 31, v66
	v_mov_b32_e32 v74, 0
	v_bfe_u32 v140, v72, 4, 2
	s_lshl_b32 s0, s19, 7
	v_lshl_add_u64 v[144:145], v[66:67], 2, v[68:69]
	v_lshl_or_b32 v141, v140, 3, s0
	global_load_dword v146, v[144:145], off
	global_load_dword v147, v[144:145], off offset:64
	global_load_dword v148, v[144:145], off offset:128
	global_load_dword v149, v[144:145], off offset:192
	s_lshl_b32 s4, s18, 8
	v_or_b32_e32 v141, s21, v141
	v_add_u32_e32 v142, s4, v71
	v_lshl_add_u32 v142, v142, 8, v141
	v_cmp_lt_i32_e32 vcc, v66, v64
	s_waitcnt vmcnt(3)
	v_mul_f32_e32 v155, 0x3c800000, v146
	v_mul_f32_e32 v156, 0xbd38aa3b, v60
	v_mul_f32_e32 v157, 0xbd38aa3b, v61
	v_mul_f32_e32 v158, 0xbd38aa3b, v62
	v_mul_f32_e32 v159, 0xbd38aa3b, v63
	v_mul_f32_e32 v160, 0xbd38aa3b, v52
	v_mul_f32_e32 v161, 0xbd38aa3b, v53
	v_mul_f32_e32 v162, 0xbd38aa3b, v54
	v_mul_f32_e32 v163, 0xbd38aa3b, v55
	v_exp_f32_e32 v156, v156
	v_exp_f32_e32 v157, v157
	v_exp_f32_e32 v158, v158
	v_exp_f32_e32 v159, v159
	v_exp_f32_e32 v160, v160
	v_exp_f32_e32 v161, v161
	v_exp_f32_e32 v162, v162
	v_exp_f32_e32 v163, v163
	v_add_f32_e32 v156, 1.0, v156
	v_add_f32_e32 v157, 1.0, v157
	v_add_f32_e32 v158, 1.0, v158
	v_add_f32_e32 v159, 1.0, v159
	v_add_f32_e32 v160, 1.0, v160
	v_add_f32_e32 v161, 1.0, v161
	v_add_f32_e32 v162, 1.0, v162
	v_add_f32_e32 v163, 1.0, v163
	v_rcp_f32_e32 v156, v156
	v_rcp_f32_e32 v157, v157
	v_rcp_f32_e32 v158, v158
	v_rcp_f32_e32 v159, v159
	v_rcp_f32_e32 v160, v160
	v_rcp_f32_e32 v161, v161
	v_rcp_f32_e32 v162, v162
	v_rcp_f32_e32 v163, v163
	v_mul_f32_e32 v156, v60, v156
	v_mul_f32_e32 v157, v61, v157
	v_mul_f32_e32 v158, v62, v158
	v_mul_f32_e32 v159, v63, v159
	v_mul_f32_e32 v160, v52, v160
	v_mul_f32_e32 v161, v53, v161
	v_mul_f32_e32 v162, v54, v162
	v_mul_f32_e32 v163, v55, v163
	v_mul_f32_e32 v156, v156, v56
	v_mul_f32_e32 v157, v157, v57
	v_mul_f32_e32 v158, v158, v58
	v_mul_f32_e32 v159, v159, v59
	v_mul_f32_e32 v160, v160, v48
	v_mul_f32_e32 v161, v161, v49
	v_mul_f32_e32 v162, v162, v50
	v_mul_f32_e32 v163, v163, v51
	v_mul_f32_e32 v156, v156, v155
	v_mul_f32_e32 v157, v157, v155
	v_mul_f32_e32 v158, v158, v155
	v_mul_f32_e32 v159, v159, v155
	v_mul_f32_e32 v160, v160, v155
	v_mul_f32_e32 v161, v161, v155
	v_mul_f32_e32 v162, v162, v155
	v_mul_f32_e32 v163, v163, v155
	v_max_f32_e32 v156, 0xc3e00000, v156
	v_max_f32_e32 v157, 0xc3e00000, v157
	v_max_f32_e32 v158, 0xc3e00000, v158
	v_max_f32_e32 v159, 0xc3e00000, v159
	v_max_f32_e32 v160, 0xc3e00000, v160
	v_max_f32_e32 v161, 0xc3e00000, v161
	v_max_f32_e32 v162, 0xc3e00000, v162
	v_max_f32_e32 v163, 0xc3e00000, v163
	v_min_f32_e32 v156, 0x43e00000, v156
	v_min_f32_e32 v157, 0x43e00000, v157
	v_min_f32_e32 v158, 0x43e00000, v158
	v_min_f32_e32 v159, 0x43e00000, v159
	v_min_f32_e32 v160, 0x43e00000, v160
	v_min_f32_e32 v161, 0x43e00000, v161
	v_min_f32_e32 v162, 0x43e00000, v162
	v_min_f32_e32 v163, 0x43e00000, v163
	v_cndmask_b32_e32 v156, 0, v156, vcc
	v_cndmask_b32_e32 v157, 0, v157, vcc
	v_cndmask_b32_e32 v158, 0, v158, vcc
	v_cndmask_b32_e32 v159, 0, v159, vcc
	v_cndmask_b32_e32 v160, 0, v160, vcc
	v_cndmask_b32_e32 v161, 0, v161, vcc
	v_cndmask_b32_e32 v162, 0, v162, vcc
	v_cndmask_b32_e32 v163, 0, v163, vcc
	v_mov_b32_e32 v180, 0
	v_mov_b32_e32 v181, 0
	v_cvt_pk_fp8_f32 v180, v156, v157
	v_cvt_pk_fp8_f32 v181, v160, v161
	v_mov_b32_e32 v184, v142
	v_cvt_pk_fp8_f32 v180, v158, v159 op_sel:[0,0,1]
	v_cvt_pk_fp8_f32 v181, v162, v163 op_sel:[0,0,1]
	s_nop 1
	global_store_dwordx2 v184, v[180:181], s[12:13] sc1
	v_add_u32_e32 v154, 0x10, v66
	v_cmp_lt_i32_e32 vcc, v154, v64
	s_waitcnt vmcnt(3)
	v_mul_f32_e32 v155, 0x3c800000, v147
	v_mul_f32_e32 v156, 0xbd38aa3b, v44
	v_mul_f32_e32 v157, 0xbd38aa3b, v45
	v_mul_f32_e32 v158, 0xbd38aa3b, v46
	v_mul_f32_e32 v159, 0xbd38aa3b, v47
	v_mul_f32_e32 v160, 0xbd38aa3b, v36
	v_mul_f32_e32 v161, 0xbd38aa3b, v37
	v_mul_f32_e32 v162, 0xbd38aa3b, v38
	v_mul_f32_e32 v163, 0xbd38aa3b, v39
	v_exp_f32_e32 v156, v156
	v_exp_f32_e32 v157, v157
	v_exp_f32_e32 v158, v158
	v_exp_f32_e32 v159, v159
	v_exp_f32_e32 v160, v160
	v_exp_f32_e32 v161, v161
	v_exp_f32_e32 v162, v162
	v_exp_f32_e32 v163, v163
	v_add_f32_e32 v156, 1.0, v156
	v_add_f32_e32 v157, 1.0, v157
	v_add_f32_e32 v158, 1.0, v158
	v_add_f32_e32 v159, 1.0, v159
	v_add_f32_e32 v160, 1.0, v160
	v_add_f32_e32 v161, 1.0, v161
	v_add_f32_e32 v162, 1.0, v162
	v_add_f32_e32 v163, 1.0, v163
	v_rcp_f32_e32 v156, v156
	v_rcp_f32_e32 v157, v157
	v_rcp_f32_e32 v158, v158
	v_rcp_f32_e32 v159, v159
	v_rcp_f32_e32 v160, v160
	v_rcp_f32_e32 v161, v161
	v_rcp_f32_e32 v162, v162
	v_rcp_f32_e32 v163, v163
	v_mul_f32_e32 v156, v44, v156
	v_mul_f32_e32 v157, v45, v157
	v_mul_f32_e32 v158, v46, v158
	v_mul_f32_e32 v159, v47, v159
	v_mul_f32_e32 v160, v36, v160
	v_mul_f32_e32 v161, v37, v161
	v_mul_f32_e32 v162, v38, v162
	v_mul_f32_e32 v163, v39, v163
	v_mul_f32_e32 v156, v156, v40
	v_mul_f32_e32 v157, v157, v41
	v_mul_f32_e32 v158, v158, v42
	v_mul_f32_e32 v159, v159, v43
	v_mul_f32_e32 v160, v160, v32
	v_mul_f32_e32 v161, v161, v33
	v_mul_f32_e32 v162, v162, v34
	v_mul_f32_e32 v163, v163, v35
	v_mul_f32_e32 v156, v156, v155
	v_mul_f32_e32 v157, v157, v155
	v_mul_f32_e32 v158, v158, v155
	v_mul_f32_e32 v159, v159, v155
	v_mul_f32_e32 v160, v160, v155
	v_mul_f32_e32 v161, v161, v155
	v_mul_f32_e32 v162, v162, v155
	v_mul_f32_e32 v163, v163, v155
	v_max_f32_e32 v156, 0xc3e00000, v156
	v_max_f32_e32 v157, 0xc3e00000, v157
	v_max_f32_e32 v158, 0xc3e00000, v158
	v_max_f32_e32 v159, 0xc3e00000, v159
	v_max_f32_e32 v160, 0xc3e00000, v160
	v_max_f32_e32 v161, 0xc3e00000, v161
	v_max_f32_e32 v162, 0xc3e00000, v162
	v_max_f32_e32 v163, 0xc3e00000, v163
	v_min_f32_e32 v156, 0x43e00000, v156
	v_min_f32_e32 v157, 0x43e00000, v157
	v_min_f32_e32 v158, 0x43e00000, v158
	v_min_f32_e32 v159, 0x43e00000, v159
	v_min_f32_e32 v160, 0x43e00000, v160
	v_min_f32_e32 v161, 0x43e00000, v161
	v_min_f32_e32 v162, 0x43e00000, v162
	v_min_f32_e32 v163, 0x43e00000, v163
	v_cndmask_b32_e32 v156, 0, v156, vcc
	v_cndmask_b32_e32 v157, 0, v157, vcc
	v_cndmask_b32_e32 v158, 0, v158, vcc
	v_cndmask_b32_e32 v159, 0, v159, vcc
	v_cndmask_b32_e32 v160, 0, v160, vcc
	v_cndmask_b32_e32 v161, 0, v161, vcc
	v_cndmask_b32_e32 v162, 0, v162, vcc
	v_cndmask_b32_e32 v163, 0, v163, vcc
	v_mov_b32_e32 v182, 0
	v_mov_b32_e32 v183, 0
	v_cvt_pk_fp8_f32 v182, v156, v157
	v_cvt_pk_fp8_f32 v183, v160, v161
	v_add_u32_e32 v184, 0x1000, v142
	v_cvt_pk_fp8_f32 v182, v158, v159 op_sel:[0,0,1]
	v_cvt_pk_fp8_f32 v183, v162, v163 op_sel:[0,0,1]
	s_nop 1
	global_store_dwordx2 v184, v[182:183], s[12:13] sc1
	v_add_u32_e32 v154, 0x20, v66
	v_cmp_lt_i32_e32 vcc, v154, v64
	s_waitcnt vmcnt(3)
	v_mul_f32_e32 v155, 0x3c800000, v148
	v_mul_f32_e32 v156, 0xbd38aa3b, v28
	v_mul_f32_e32 v157, 0xbd38aa3b, v29
	v_mul_f32_e32 v158, 0xbd38aa3b, v30
	v_mul_f32_e32 v159, 0xbd38aa3b, v31
	v_mul_f32_e32 v160, 0xbd38aa3b, v20
	v_mul_f32_e32 v161, 0xbd38aa3b, v21
	v_mul_f32_e32 v162, 0xbd38aa3b, v22
	v_mul_f32_e32 v163, 0xbd38aa3b, v23
	v_exp_f32_e32 v156, v156
	v_exp_f32_e32 v157, v157
	v_exp_f32_e32 v158, v158
	v_exp_f32_e32 v159, v159
	v_exp_f32_e32 v160, v160
	v_exp_f32_e32 v161, v161
	v_exp_f32_e32 v162, v162
	v_exp_f32_e32 v163, v163
	v_add_f32_e32 v156, 1.0, v156
	v_add_f32_e32 v157, 1.0, v157
	v_add_f32_e32 v158, 1.0, v158
	v_add_f32_e32 v159, 1.0, v159
	v_add_f32_e32 v160, 1.0, v160
	v_add_f32_e32 v161, 1.0, v161
	v_add_f32_e32 v162, 1.0, v162
	v_add_f32_e32 v163, 1.0, v163
	v_rcp_f32_e32 v156, v156
	v_rcp_f32_e32 v157, v157
	v_rcp_f32_e32 v158, v158
	v_rcp_f32_e32 v159, v159
	v_rcp_f32_e32 v160, v160
	v_rcp_f32_e32 v161, v161
	v_rcp_f32_e32 v162, v162
	v_rcp_f32_e32 v163, v163
	v_mul_f32_e32 v156, v28, v156
	v_mul_f32_e32 v157, v29, v157
	v_mul_f32_e32 v158, v30, v158
	v_mul_f32_e32 v159, v31, v159
	v_mul_f32_e32 v160, v20, v160
	v_mul_f32_e32 v161, v21, v161
	v_mul_f32_e32 v162, v22, v162
	v_mul_f32_e32 v163, v23, v163
	v_mul_f32_e32 v156, v156, v24
	v_mul_f32_e32 v157, v157, v25
	v_mul_f32_e32 v158, v158, v26
	v_mul_f32_e32 v159, v159, v27
	v_mul_f32_e32 v160, v160, v16
	v_mul_f32_e32 v161, v161, v17
	v_mul_f32_e32 v162, v162, v18
	v_mul_f32_e32 v163, v163, v19
	v_mul_f32_e32 v156, v156, v155
	v_mul_f32_e32 v157, v157, v155
	v_mul_f32_e32 v158, v158, v155
	v_mul_f32_e32 v159, v159, v155
	v_mul_f32_e32 v160, v160, v155
	v_mul_f32_e32 v161, v161, v155
	v_mul_f32_e32 v162, v162, v155
	v_mul_f32_e32 v163, v163, v155
	v_max_f32_e32 v156, 0xc3e00000, v156
	v_max_f32_e32 v157, 0xc3e00000, v157
	v_max_f32_e32 v158, 0xc3e00000, v158
	v_max_f32_e32 v159, 0xc3e00000, v159
	v_max_f32_e32 v160, 0xc3e00000, v160
	v_max_f32_e32 v161, 0xc3e00000, v161
	v_max_f32_e32 v162, 0xc3e00000, v162
	v_max_f32_e32 v163, 0xc3e00000, v163
	v_min_f32_e32 v156, 0x43e00000, v156
	v_min_f32_e32 v157, 0x43e00000, v157
	v_min_f32_e32 v158, 0x43e00000, v158
	v_min_f32_e32 v159, 0x43e00000, v159
	v_min_f32_e32 v160, 0x43e00000, v160
	v_min_f32_e32 v161, 0x43e00000, v161
	v_min_f32_e32 v162, 0x43e00000, v162
	v_min_f32_e32 v163, 0x43e00000, v163
	v_cndmask_b32_e32 v156, 0, v156, vcc
	v_cndmask_b32_e32 v157, 0, v157, vcc
	v_cndmask_b32_e32 v158, 0, v158, vcc
	v_cndmask_b32_e32 v159, 0, v159, vcc
	v_cndmask_b32_e32 v160, 0, v160, vcc
	v_cndmask_b32_e32 v161, 0, v161, vcc
	v_cndmask_b32_e32 v162, 0, v162, vcc
	v_cndmask_b32_e32 v163, 0, v163, vcc
	v_mov_b32_e32 v180, 0
	v_mov_b32_e32 v181, 0
	v_cvt_pk_fp8_f32 v180, v156, v157
	v_cvt_pk_fp8_f32 v181, v160, v161
	v_add_u32_e32 v184, 0x2000, v142
	v_cvt_pk_fp8_f32 v180, v158, v159 op_sel:[0,0,1]
	v_cvt_pk_fp8_f32 v181, v162, v163 op_sel:[0,0,1]
	s_nop 1
	global_store_dwordx2 v184, v[180:181], s[12:13] sc1
	v_add_u32_e32 v154, 0x30, v66
	v_cmp_lt_i32_e32 vcc, v154, v64
	s_waitcnt vmcnt(3)
	v_mul_f32_e32 v155, 0x3c800000, v149
	v_mul_f32_e32 v156, 0xbd38aa3b, v12
	v_mul_f32_e32 v157, 0xbd38aa3b, v13
	v_mul_f32_e32 v158, 0xbd38aa3b, v14
	v_mul_f32_e32 v159, 0xbd38aa3b, v15
	v_mul_f32_e32 v160, 0xbd38aa3b, v4
	v_mul_f32_e32 v161, 0xbd38aa3b, v5
	v_mul_f32_e32 v162, 0xbd38aa3b, v6
	v_mul_f32_e32 v163, 0xbd38aa3b, v7
	v_exp_f32_e32 v156, v156
	v_exp_f32_e32 v157, v157
	v_exp_f32_e32 v158, v158
	v_exp_f32_e32 v159, v159
	v_exp_f32_e32 v160, v160
	v_exp_f32_e32 v161, v161
	v_exp_f32_e32 v162, v162
	v_exp_f32_e32 v163, v163
	v_add_f32_e32 v156, 1.0, v156
	v_add_f32_e32 v157, 1.0, v157
	v_add_f32_e32 v158, 1.0, v158
	v_add_f32_e32 v159, 1.0, v159
	v_add_f32_e32 v160, 1.0, v160
	v_add_f32_e32 v161, 1.0, v161
	v_add_f32_e32 v162, 1.0, v162
	v_add_f32_e32 v163, 1.0, v163
	v_rcp_f32_e32 v156, v156
	v_rcp_f32_e32 v157, v157
	v_rcp_f32_e32 v158, v158
	v_rcp_f32_e32 v159, v159
	v_rcp_f32_e32 v160, v160
	v_rcp_f32_e32 v161, v161
	v_rcp_f32_e32 v162, v162
	v_rcp_f32_e32 v163, v163
	v_mul_f32_e32 v156, v12, v156
	v_mul_f32_e32 v157, v13, v157
	v_mul_f32_e32 v158, v14, v158
	v_mul_f32_e32 v159, v15, v159
	v_mul_f32_e32 v160, v4, v160
	v_mul_f32_e32 v161, v5, v161
	v_mul_f32_e32 v162, v6, v162
	v_mul_f32_e32 v163, v7, v163
	v_mul_f32_e32 v156, v156, v8
	v_mul_f32_e32 v157, v157, v9
	v_mul_f32_e32 v158, v158, v10
	v_mul_f32_e32 v159, v159, v11
	v_mul_f32_e32 v160, v160, v0
	v_mul_f32_e32 v161, v161, v1
	v_mul_f32_e32 v162, v162, v2
	v_mul_f32_e32 v163, v163, v3
	v_mul_f32_e32 v156, v156, v155
	v_mul_f32_e32 v157, v157, v155
	v_mul_f32_e32 v158, v158, v155
	v_mul_f32_e32 v159, v159, v155
	v_mul_f32_e32 v160, v160, v155
	v_mul_f32_e32 v161, v161, v155
	v_mul_f32_e32 v162, v162, v155
	v_mul_f32_e32 v163, v163, v155
	v_max_f32_e32 v156, 0xc3e00000, v156
	v_max_f32_e32 v157, 0xc3e00000, v157
	v_max_f32_e32 v158, 0xc3e00000, v158
	v_max_f32_e32 v159, 0xc3e00000, v159
	v_max_f32_e32 v160, 0xc3e00000, v160
	v_max_f32_e32 v161, 0xc3e00000, v161
	v_max_f32_e32 v162, 0xc3e00000, v162
	v_max_f32_e32 v163, 0xc3e00000, v163
	v_min_f32_e32 v156, 0x43e00000, v156
	v_min_f32_e32 v157, 0x43e00000, v157
	v_min_f32_e32 v158, 0x43e00000, v158
	v_min_f32_e32 v159, 0x43e00000, v159
	v_min_f32_e32 v160, 0x43e00000, v160
	v_min_f32_e32 v161, 0x43e00000, v161
	v_min_f32_e32 v162, 0x43e00000, v162
	v_min_f32_e32 v163, 0x43e00000, v163
	v_cndmask_b32_e32 v156, 0, v156, vcc
	v_cndmask_b32_e32 v157, 0, v157, vcc
	v_cndmask_b32_e32 v158, 0, v158, vcc
	v_cndmask_b32_e32 v159, 0, v159, vcc
	v_cndmask_b32_e32 v160, 0, v160, vcc
	v_cndmask_b32_e32 v161, 0, v161, vcc
	v_cndmask_b32_e32 v162, 0, v162, vcc
	v_cndmask_b32_e32 v163, 0, v163, vcc
	v_mov_b32_e32 v182, 0
	v_mov_b32_e32 v183, 0
	v_cvt_pk_fp8_f32 v182, v156, v157
	v_cvt_pk_fp8_f32 v183, v160, v161
	v_add_u32_e32 v184, 0x3000, v142
	v_cvt_pk_fp8_f32 v182, v158, v159 op_sel:[0,0,1]
	v_cvt_pk_fp8_f32 v183, v162, v163 op_sel:[0,0,1]
	s_nop 1
	global_store_dwordx2 v184, v[182:183], s[12:13] sc1
	v_bfe_u32 v50, v72, 4, 2
	s_waitcnt vmcnt(0)
	v_or_b32_e32 v0, v50, v70
	v_cmp_eq_u32_e32 vcc, 0, v0
	s_and_saveexec_b64 s[0:1], vcc
	s_cbranch_execz .LBB0_2686
	s_mov_b64 s[4:5], exec
	v_mbcnt_lo_u32_b32 v0, s4, 0
	v_mbcnt_hi_u32_b32 v0, s5, v0
	v_cmp_eq_u32_e32 vcc, 0, v0
	s_and_b64 s[8:9], exec, vcc
	s_mov_b64 exec, s[8:9]
	s_cbranch_execz .LBB0_2686
	s_lshl_b32 s8, s18, 5
	s_ashr_i32 s9, s8, 31
	s_lshl_b64 s[8:9], s[8:9], 2
	s_add_u32 s8, s48, s8
	s_addc_u32 s9, s49, s9
	s_bcnt1_i32_b64 s4, s[4:5]
	v_mov_b32_e32 v0, 0
	v_mov_b32_e32 v1, s4
	global_atomic_add v0, v1, s[8:9]

.LBB0_2703:
	s_getpc_b64 s[100:101]
	v_min_u32_e32 v251, 0x4380, v250
	global_load_dword a0, v251, s[100:101]
	v_bfe_i32 v3, v0, 27, 1
	v_lshlrev_b32_e32 v1, 4, v0
	v_lshrrev_b32_e32 v3, 22, v3
	v_add_u32_e32 v3, v1, v3
	v_and_b32_e32 v3, 0xfffffc00, v3
	v_ashrrev_i32_e32 v2, 31, v0
	v_sub_u32_e32 v1, v1, v3
	v_lshrrev_b32_e32 v2, 26, v2
	v_lshrrev_b32_e32 v3, 4, v1
	v_add_u32_e32 v2, v0, v2
	v_bitop3_b32 v3, v3, v1, 32 bitop3:0x6c
	v_ashrrev_i32_e32 v1, 31, v1
	v_ashrrev_i32_e32 v2, 6, v2
	v_lshrrev_b32_e32 v1, 26, v1
	v_lshlrev_b32_e32 v4, 3, v2
	v_add_u32_e32 v1, v3, v1
	s_add_u32 s10, s78, 0x6d00000
	v_and_b32_e32 v4, -16, v4
	v_ashrrev_i32_e32 v1, 6, v1
	v_lshlrev_b32_e32 v2, 5, v2
	s_addc_u32 s11, s79, 0
	s_ashr_i32 s4, s19, 6
	v_add_u32_e32 v4, v1, v4
	v_and_b32_e32 v5, 32, v2
	v_mul_i32_i24_e32 v2, 64, v1
	v_and_b32_e32 v1, 3, v1
	s_mov_b32 s14, 0xffffe0
	s_ashr_i32 s39, s38, 31
	s_ashr_i32 s5, s19, 8
	v_and_or_b32 v1, v4, s14, v1
	s_lshl_b32 s27, s4, 10
	s_lshl_b64 s[14:15], s[38:39], 16
	v_sub_u32_e32 v2, v3, v2
	v_mov_b32_e32 v3, 1
	s_add_u32 s40, s12, s14
	v_ashrrev_i16_sdwa v2, v3, sext(v2) dst_sel:DWORD dst_unused:UNUSED_PAD src0_sel:DWORD src1_sel:BYTE_0
	s_addc_u32 s41, s13, s15
	s_lshl_b32 s14, s38, 2
	v_bfe_i32 v3, v2, 0, 16
	v_lshlrev_b32_e32 v2, 1, v4
	s_add_i32 s14, s14, 0
	v_and_b32_e32 v6, 24, v2
	v_lshrrev_b32_e32 v2, 2, v4
	s_add_i32 s14, s14, 0x24100
	v_and_b32_e32 v7, 4, v2
	s_barrier
	v_mov_b32_e32 v2, s14
	ds_read_b32 v2, v2
	v_or3_b32 v1, v1, v7, v6
	v_add_lshl_u32 v3, v5, v3, 1
	v_lshl_add_u32 v194, v1, 8, v3
	v_lshl_add_u32 v195, v4, 8, v3
	s_waitcnt lgkmcnt(0)
	v_ashrrev_i32_e32 v3, 31, v2
	v_lshlrev_b64 v[2:3], 18, v[2:3]
	s_ashr_i32 s37, s36, 31
	v_lshl_add_u64 v[2:3], s[10:11], 0, v[2:3]
	s_lshl_b64 s[14:15], s[36:37], 16
	v_lshl_add_u64 v[2:3], v[2:3], 0, s[14:15]
	s_add_i32 s50, s27, 0
	v_readfirstlane_b32 s15, v3
	v_readfirstlane_b32 s14, v2
	s_mov_b64 s[16:17], s[14:15]
	s_add_i32 m0, s50, 0x10000
	s_mov_b32 s54, 0
	global_load_lds_dwordx4 v194, s[16:17]
	s_add_u32 s16, s14, 0x4000
	s_addc_u32 s17, s15, 0
	s_add_i32 m0, s50, 0x12000
	s_nop 0
	global_load_lds_dwordx4 v194, s[16:17]
	s_add_i32 m0, s50, 0x14000
	s_add_u32 s16, s14, 0x8000
	s_addc_u32 s17, s15, 0
	s_nop 0
	global_load_lds_dwordx4 v194, s[16:17]
	s_add_u32 s16, s14, 0xc000
	s_addc_u32 s17, s15, 0
	s_add_i32 m0, s50, 0x16000
	s_nop 0
	global_load_lds_dwordx4 v194, s[16:17]
	v_mov_b32_e32 v1, v195
	s_mov_b64 s[16:17], s[40:41]
	s_mov_b32 m0, s50
	s_nop 0
	global_load_lds_dwordx4 v1, s[16:17] sc1
	s_add_u32 s16, s40, 0x4000
	v_mov_b32_e32 v1, v195
	s_addc_u32 s17, s41, 0
	s_add_i32 s51, s50, 0x2000
	s_mov_b32 m0, s51
	s_add_i32 s52, s50, 0x4000
	global_load_lds_dwordx4 v1, s[16:17] sc1
	s_add_u32 s16, s40, 0x8000
	v_mov_b32_e32 v1, v195
	s_addc_u32 s17, s41, 0
	s_mov_b32 m0, s52
	s_nop 0
	global_load_lds_dwordx4 v1, s[16:17] sc1
	s_add_u32 s16, s40, 0xc000
	s_addc_u32 s17, s41, 0
	s_add_i32 s53, s50, 0x6000
	v_mov_b32_e32 v1, v195
	s_mov_b32 m0, s53
	s_cmp_eq_u32 s5, 1
	global_load_lds_dwordx4 v1, s[16:17] sc1
	s_cselect_b64 s[16:17], -1, 0
	s_cmp_lg_u32 s5, 1
	s_cbranch_scc1 .LBB0_2705
	s_barrier

.LBB0_2723:
	s_getpc_b64 s[100:101]
	v_min_u32_e32 v251, 0x3e80, v250
	global_load_dword a0, v251, s[100:101]
	s_barrier

.LBB0_2762:
	v_readlane_b32 s4, v249, 51
	v_readlane_b32 s5, v249, 52
	s_mov_b64 s[44:45], s[4:5]
	s_cmp_lt_i32 s44, 15
	v_readlane_b32 s6, v249, 53
	v_readlane_b32 s7, v249, 54
	s_cselect_b64 s[0:1], -1, 0
	s_cmp_gt_i32 s45, 15
	s_cselect_b64 s[6:7], -1, 0
	s_and_b64 s[0:1], s[0:1], s[6:7]
	s_andn2_b64 vcc, exec, s[0:1]
	s_cbranch_vccnz .LBB0_2822
	s_waitcnt vmcnt(0)
	s_waitcnt vmcnt(0) lgkmcnt(0)
	s_barrier
	s_cmp_lt_u32 s98, 4
	s_cbranch_scc1 .Lipf_a53
	s_getpc_b64 s[100:101]
	v_lshlrev_b32_e32 v251, 1, v250
	v_add_u32_e32 v251, 0xffff8000, v251
	v_min_u32_e32 v251, 0x2f80, v251
	global_load_dword a0, v251, s[100:101]

.LBB0_2865:
	s_getpc_b64 s[100:101]
	v_min_u32_e32 v251, 0xb80, v250
	global_load_dword a0, v251, s[100:101]
	s_or_b64 exec, exec, s[6:7]
